# 16-read load segments: scalar address arithmetic moved behind the LDS fragment reads so the reads issue first (14 segments)
# baseline (speedup 1.0000x reference)
.LBB0_261:
	s_nop 2
	ds_read_b128 v[0:3], v219
	ds_read_b128 v[4:7], v219 offset:1024
	ds_read_b128 v[8:11], v219 offset:2048
	ds_read_b128 v[12:15], v219 offset:3072
	ds_read_b128 v[16:19], v220
	ds_read_b128 v[20:23], v220 offset:1024
	ds_read_b128 v[24:27], v220 offset:2048
	ds_read_b128 v[28:31], v220 offset:3072
	ds_read_b128 v[32:35], v221
	ds_read_b128 v[36:39], v221 offset:1024
	ds_read_b128 v[40:43], v221 offset:2048
	ds_read_b128 v[44:47], v221 offset:3072
	ds_read_b128 v[48:51], v221 offset:4096
	ds_read_b128 v[52:55], v221 offset:5120
	ds_read_b128 v[56:59], v221 offset:6144
	ds_read_b128 v[60:63], v221 offset:7168
	s_add_u32 s8, s46, 0x100
	s_addc_u32 s9, s47, 0
	s_cmp_eq_u32 s76, 12
	s_cselect_b32 s52, s11, s8
	s_cselect_b32 s53, s7, s9
	s_cselect_b32 s48, s41, s77
	s_cselect_b32 s49, s39, s80
	s_add_u32 s12, s52, 0x80
	s_addc_u32 s13, s53, 0
	s_add_u32 s50, s48, 0x80
	s_addc_u32 s51, s49, 0
	s_add_u32 s46, s46, 0x40080
	s_addc_u32 s47, s47, 0
	s_add_i32 m0, s59, 0xc000
	s_nop 0
	global_load_lds_dwordx4 v215, s[46:47]
	s_nop 0
	s_add_i32 m0, s59, 0xe000
	s_nop 0
	global_load_lds_dwordx4 v217, s[46:47]
	s_waitcnt vmcnt(8)
	s_waitcnt lgkmcnt(0)
	s_barrier
	v_mfma_i32_16x16x64_i8 v[172:175], v[0:3], v[48:51], v[172:175]
	v_mfma_i32_16x16x64_i8 v[168:171], v[8:11], v[48:51], v[168:171]
	v_mfma_i32_16x16x64_i8 v[152:155], v[8:11], v[56:59], v[152:155]
	v_mfma_i32_16x16x64_i8 v[156:159], v[0:3], v[56:59], v[156:159]
	v_mfma_i32_16x16x64_i8 v[64:67], v[0:3], v[32:35], v[204:207]
	v_mfma_i32_16x16x64_i8 v[76:79], v[8:11], v[32:35], v[200:203]
	v_mfma_i32_16x16x64_i8 v[92:95], v[8:11], v[40:43], v[184:187]
	v_mfma_i32_16x16x64_i8 v[80:83], v[0:3], v[40:43], v[188:191]
	v_mfma_i32_16x16x64_i8 v[172:175], v[4:7], v[52:55], v[172:175]
	v_mfma_i32_16x16x64_i8 v[168:171], v[12:15], v[52:55], v[168:171]
	v_mfma_i32_16x16x64_i8 v[152:155], v[12:15], v[60:63], v[152:155]
	v_mfma_i32_16x16x64_i8 v[156:159], v[4:7], v[60:63], v[156:159]
	v_mfma_i32_16x16x64_i8 v[64:67], v[4:7], v[36:39], v[64:67]
	v_mfma_i32_16x16x64_i8 v[76:79], v[12:15], v[36:39], v[76:79]
	v_mfma_i32_16x16x64_i8 v[92:95], v[12:15], v[44:47], v[92:95]
	v_mfma_i32_16x16x64_i8 v[80:83], v[4:7], v[44:47], v[80:83]
	v_mfma_i32_16x16x64_i8 v[184:187], v[16:19], v[32:35], v[196:199]
	v_mfma_i32_16x16x64_i8 v[32:35], v[24:27], v[32:35], v[192:195]
	v_mfma_i32_16x16x64_i8 v[196:199], v[20:23], v[36:39], v[184:187]
	v_mfma_i32_16x16x64_i8 v[32:35], v[28:31], v[36:39], v[32:35]
	v_mfma_i32_16x16x64_i8 v[36:39], v[16:19], v[40:43], v[180:183]
	v_mfma_i32_16x16x64_i8 v[40:43], v[24:27], v[40:43], v[176:179]
	v_mfma_i32_16x16x64_i8 v[36:39], v[20:23], v[44:47], v[36:39]
	v_mfma_i32_16x16x64_i8 v[40:43], v[28:31], v[44:47], v[40:43]
	v_mfma_i32_16x16x64_i8 v[44:47], v[16:19], v[48:51], v[164:167]
	v_mfma_i32_16x16x64_i8 v[48:51], v[24:27], v[48:51], v[160:163]
	v_mfma_i32_16x16x64_i8 v[44:47], v[20:23], v[52:55], v[44:47]
	v_mfma_i32_16x16x64_i8 v[48:51], v[28:31], v[52:55], v[48:51]
	v_mfma_i32_16x16x64_i8 v[52:55], v[16:19], v[56:59], v[148:151]
	v_mfma_i32_16x16x64_i8 v[56:59], v[24:27], v[56:59], v[144:147]
	v_mfma_i32_16x16x64_i8 v[52:55], v[20:23], v[60:63], v[52:55]
	v_mfma_i32_16x16x64_i8 v[56:59], v[28:31], v[60:63], v[56:59]
	s_barrier
	ds_read_b128 v[60:63], v221 offset:16384
	ds_read_b128 v[144:147], v221 offset:17408
	ds_read_b128 v[148:151], v221 offset:18432
	ds_read_b128 v[160:163], v221 offset:19456
	ds_read_b128 v[164:167], v221 offset:20480
	ds_read_b128 v[176:179], v221 offset:21504
	ds_read_b128 v[180:183], v221 offset:22528
	ds_read_b128 v[184:187], v221 offset:23552
	s_add_i32 m0, s59, 0x10000
	s_nop 0
	global_load_lds_dwordx4 v216, s[48:49]
	s_nop 0
	s_add_i32 m0, s59, 0x12000
	s_nop 0
	global_load_lds_dwordx4 v218, s[48:49]
	s_add_u32 s46, s48, 0x40000
	s_addc_u32 s47, s49, 0
	s_add_i32 m0, s59, 0x14000
	s_nop 0
	global_load_lds_dwordx4 v216, s[46:47]
	s_nop 0
	s_add_i32 m0, s59, 0x16000
	s_nop 0
	global_load_lds_dwordx4 v218, s[46:47]
	s_nop 0
	s_add_i32 m0, s59, 0
	s_nop 0
	global_load_lds_dwordx4 v215, s[52:53]
	s_nop 0
	s_add_i32 m0, s59, 0x2000
	s_nop 0
	global_load_lds_dwordx4 v217, s[52:53]
	s_waitcnt vmcnt(8)
	s_waitcnt lgkmcnt(0)
	s_barrier
	v_mfma_i32_16x16x64_i8 v[140:143], v[0:3], v[60:63], v[140:143]
	v_mfma_i32_16x16x64_i8 v[124:127], v[0:3], v[148:151], v[124:127]
	v_mfma_i32_16x16x64_i8 v[108:111], v[0:3], v[164:167], v[108:111]
	v_mfma_i32_16x16x64_i8 v[0:3], v[0:3], v[180:183], v[88:91]
	v_mfma_i32_16x16x64_i8 v[136:139], v[8:11], v[60:63], v[136:139]
	v_mfma_i32_16x16x64_i8 v[120:123], v[8:11], v[148:151], v[120:123]
	v_mfma_i32_16x16x64_i8 v[104:107], v[8:11], v[164:167], v[104:107]
	v_mfma_i32_16x16x64_i8 v[88:91], v[4:7], v[184:187], v[0:3]
	v_mfma_i32_16x16x64_i8 v[0:3], v[8:11], v[180:183], v[84:87]
	v_mfma_i32_16x16x64_i8 v[140:143], v[4:7], v[144:147], v[140:143]
	v_mfma_i32_16x16x64_i8 v[136:139], v[12:15], v[144:147], v[136:139]
	v_mfma_i32_16x16x64_i8 v[124:127], v[4:7], v[160:163], v[124:127]
	v_mfma_i32_16x16x64_i8 v[120:123], v[12:15], v[160:163], v[120:123]
	v_mfma_i32_16x16x64_i8 v[108:111], v[4:7], v[176:179], v[108:111]
	v_mfma_i32_16x16x64_i8 v[104:107], v[12:15], v[176:179], v[104:107]
	v_mfma_i32_16x16x64_i8 v[84:87], v[12:15], v[184:187], v[0:3]
	v_mfma_i32_16x16x64_i8 v[0:3], v[16:19], v[60:63], v[132:135]
	v_mfma_i32_16x16x64_i8 v[132:135], v[20:23], v[144:147], v[0:3]
	v_mfma_i32_16x16x64_i8 v[0:3], v[24:27], v[60:63], v[128:131]
	v_mfma_i32_16x16x64_i8 v[128:131], v[28:31], v[144:147], v[0:3]
	v_mfma_i32_16x16x64_i8 v[0:3], v[16:19], v[148:151], v[116:119]
	v_mfma_i32_16x16x64_i8 v[116:119], v[20:23], v[160:163], v[0:3]
	v_mfma_i32_16x16x64_i8 v[0:3], v[24:27], v[148:151], v[112:115]
	v_mfma_i32_16x16x64_i8 v[112:115], v[28:31], v[160:163], v[0:3]
	v_mfma_i32_16x16x64_i8 v[0:3], v[16:19], v[164:167], v[100:103]
	v_mfma_i32_16x16x64_i8 v[100:103], v[20:23], v[176:179], v[0:3]
	v_mfma_i32_16x16x64_i8 v[0:3], v[24:27], v[164:167], v[96:99]
	v_mfma_i32_16x16x64_i8 v[96:99], v[28:31], v[176:179], v[0:3]
	v_mfma_i32_16x16x64_i8 v[0:3], v[16:19], v[180:183], v[72:75]
	v_mfma_i32_16x16x64_i8 v[72:75], v[20:23], v[184:187], v[0:3]
	v_mfma_i32_16x16x64_i8 v[0:3], v[24:27], v[180:183], v[68:71]
	v_mfma_i32_16x16x64_i8 v[68:71], v[28:31], v[184:187], v[0:3]
	s_barrier
	ds_read_b128 v[16:19], v222
	ds_read_b128 v[8:11], v222 offset:1024
	ds_read_b128 v[4:7], v222 offset:2048
	s_nop 1
	ds_read_b128 v[0:3], v222 offset:3072
	ds_read_b128 v[28:31], v223
	ds_read_b128 v[24:27], v223 offset:1024
	ds_read_b128 v[20:23], v223 offset:2048
	ds_read_b128 v[12:15], v223 offset:3072
	ds_read_b128 v[60:63], v221 offset:32768
	ds_read_b128 v[144:147], v221 offset:33792
	ds_read_b128 v[148:151], v221 offset:34816
	ds_read_b128 v[160:163], v221 offset:35840
	ds_read_b128 v[208:211], v221 offset:36864
	ds_read_b128 v[224:227], v221 offset:37888
	ds_read_b128 v[228:231], v221 offset:38912
	ds_read_b128 v[232:235], v221 offset:39936
	s_add_u32 s46, s52, 0x40000
	s_addc_u32 s47, s53, 0
	s_add_i32 m0, s59, 0x4000
	s_nop 0
	global_load_lds_dwordx4 v215, s[46:47]
	s_nop 0
	s_add_i32 m0, s59, 0x6000
	s_nop 0
	global_load_lds_dwordx4 v217, s[46:47]
	s_waitcnt vmcnt(8)
	s_waitcnt lgkmcnt(0)
	s_barrier
	v_mfma_i32_16x16x64_i8 v[64:67], v[16:19], v[60:63], v[64:67]
	v_mfma_i32_16x16x64_i8 v[204:207], v[8:11], v[144:147], v[64:67]
	v_mfma_i32_16x16x64_i8 v[64:67], v[4:7], v[60:63], v[76:79]
	v_mfma_i32_16x16x64_i8 v[200:203], v[0:3], v[144:147], v[64:67]
	v_mfma_i32_16x16x64_i8 v[64:67], v[16:19], v[148:151], v[80:83]
	v_mfma_i32_16x16x64_i8 v[188:191], v[8:11], v[160:163], v[64:67]
	v_mfma_i32_16x16x64_i8 v[64:67], v[4:7], v[148:151], v[92:95]
	v_mfma_i32_16x16x64_i8 v[184:187], v[0:3], v[160:163], v[64:67]
	v_mfma_i32_16x16x64_i8 v[64:67], v[16:19], v[208:211], v[172:175]
	v_mfma_i32_16x16x64_i8 v[172:175], v[8:11], v[224:227], v[64:67]
	v_mfma_i32_16x16x64_i8 v[64:67], v[4:7], v[208:211], v[168:171]
	v_mfma_i32_16x16x64_i8 v[168:171], v[0:3], v[224:227], v[64:67]
	v_mfma_i32_16x16x64_i8 v[64:67], v[16:19], v[228:231], v[156:159]
	v_mfma_i32_16x16x64_i8 v[156:159], v[8:11], v[232:235], v[64:67]
	v_mfma_i32_16x16x64_i8 v[64:67], v[4:7], v[228:231], v[152:155]
	v_mfma_i32_16x16x64_i8 v[152:155], v[0:3], v[232:235], v[64:67]
	v_mfma_i32_16x16x64_i8 v[32:35], v[20:23], v[60:63], v[32:35]
	v_mfma_i32_16x16x64_i8 v[192:195], v[12:15], v[144:147], v[32:35]
	v_mfma_i32_16x16x64_i8 v[32:35], v[28:31], v[148:151], v[36:39]
	v_mfma_i32_16x16x64_i8 v[180:183], v[24:27], v[160:163], v[32:35]
	v_mfma_i32_16x16x64_i8 v[32:35], v[20:23], v[148:151], v[40:43]
	v_mfma_i32_16x16x64_i8 v[176:179], v[12:15], v[160:163], v[32:35]
	v_mfma_i32_16x16x64_i8 v[32:35], v[28:31], v[208:211], v[44:47]
	v_mfma_i32_16x16x64_i8 v[164:167], v[24:27], v[224:227], v[32:35]
	v_mfma_i32_16x16x64_i8 v[32:35], v[20:23], v[208:211], v[48:51]
	v_mfma_i32_16x16x64_i8 v[160:163], v[12:15], v[224:227], v[32:35]
	v_mfma_i32_16x16x64_i8 v[32:35], v[28:31], v[228:231], v[52:55]
	v_mfma_i32_16x16x64_i8 v[64:67], v[28:31], v[60:63], v[196:199]
	v_mfma_i32_16x16x64_i8 v[148:151], v[24:27], v[232:235], v[32:35]
	v_mfma_i32_16x16x64_i8 v[32:35], v[20:23], v[228:231], v[56:59]
	v_mfma_i32_16x16x64_i8 v[196:199], v[24:27], v[144:147], v[64:67]
	v_mfma_i32_16x16x64_i8 v[144:147], v[12:15], v[232:235], v[32:35]
	s_barrier
	ds_read_b128 v[60:63], v221 offset:49152
	ds_read_b128 v[56:59], v221 offset:50176
	ds_read_b128 v[52:55], v221 offset:51200
	ds_read_b128 v[48:51], v221 offset:52224
	ds_read_b128 v[44:47], v221 offset:53248
	ds_read_b128 v[40:43], v221 offset:54272
	ds_read_b128 v[36:39], v221 offset:55296
	ds_read_b128 v[32:35], v221 offset:56320
	s_add_i32 m0, s59, 0x18000
	s_nop 0
	global_load_lds_dwordx4 v216, s[50:51]
	s_nop 0
	s_add_i32 m0, s59, 0x1a000
	s_nop 0
	global_load_lds_dwordx4 v218, s[50:51]
	s_add_u32 s46, s48, 0x40080
	s_addc_u32 s47, s49, 0
	s_add_i32 m0, s59, 0x1c000
	s_nop 0
	global_load_lds_dwordx4 v216, s[46:47]
	s_nop 0
	s_add_i32 m0, s59, 0x1e000
	s_nop 0
	global_load_lds_dwordx4 v218, s[46:47]
	s_nop 0
	s_add_i32 m0, s59, 0x8000
	s_nop 0
	global_load_lds_dwordx4 v215, s[12:13]
	s_nop 0
	s_add_i32 m0, s59, 0xa000
	s_nop 0
	global_load_lds_dwordx4 v217, s[12:13]
	s_waitcnt vmcnt(8)
	s_waitcnt lgkmcnt(0)
	s_barrier
	v_mfma_i32_16x16x64_i8 v[64:67], v[16:19], v[60:63], v[140:143]
	v_mfma_i32_16x16x64_i8 v[140:143], v[8:11], v[56:59], v[64:67]
	v_mfma_i32_16x16x64_i8 v[64:67], v[4:7], v[60:63], v[136:139]
	v_mfma_i32_16x16x64_i8 v[136:139], v[0:3], v[56:59], v[64:67]
	v_mfma_i32_16x16x64_i8 v[64:67], v[16:19], v[52:55], v[124:127]
	v_mfma_i32_16x16x64_i8 v[124:127], v[8:11], v[48:51], v[64:67]
	v_mfma_i32_16x16x64_i8 v[64:67], v[4:7], v[52:55], v[120:123]
	v_mfma_i32_16x16x64_i8 v[120:123], v[0:3], v[48:51], v[64:67]
	v_mfma_i32_16x16x64_i8 v[64:67], v[16:19], v[44:47], v[108:111]
	v_mfma_i32_16x16x64_i8 v[108:111], v[8:11], v[40:43], v[64:67]
	v_mfma_i32_16x16x64_i8 v[64:67], v[4:7], v[44:47], v[104:107]
	v_mfma_i32_16x16x64_i8 v[104:107], v[0:3], v[40:43], v[64:67]
	v_mfma_i32_16x16x64_i8 v[64:67], v[16:19], v[36:39], v[88:91]
	v_mfma_i32_16x16x64_i8 v[88:91], v[8:11], v[32:35], v[64:67]
	v_mfma_i32_16x16x64_i8 v[64:67], v[4:7], v[36:39], v[84:87]
	v_mfma_i32_16x16x64_i8 v[84:87], v[0:3], v[32:35], v[64:67]
	v_mfma_i32_16x16x64_i8 v[64:67], v[28:31], v[60:63], v[132:135]
	v_mfma_i32_16x16x64_i8 v[132:135], v[24:27], v[56:59], v[64:67]
	v_mfma_i32_16x16x64_i8 v[64:67], v[20:23], v[60:63], v[128:131]
	v_mfma_i32_16x16x64_i8 v[128:131], v[12:15], v[56:59], v[64:67]
	v_mfma_i32_16x16x64_i8 v[64:67], v[28:31], v[52:55], v[116:119]
	v_mfma_i32_16x16x64_i8 v[116:119], v[24:27], v[48:51], v[64:67]
	v_mfma_i32_16x16x64_i8 v[64:67], v[20:23], v[52:55], v[112:115]
	v_mfma_i32_16x16x64_i8 v[112:115], v[12:15], v[48:51], v[64:67]
	v_mfma_i32_16x16x64_i8 v[64:67], v[28:31], v[44:47], v[100:103]
	v_mfma_i32_16x16x64_i8 v[100:103], v[24:27], v[40:43], v[64:67]
	v_mfma_i32_16x16x64_i8 v[64:67], v[20:23], v[44:47], v[96:99]
	v_mfma_i32_16x16x64_i8 v[96:99], v[12:15], v[40:43], v[64:67]
	v_mfma_i32_16x16x64_i8 v[64:67], v[28:31], v[36:39], v[72:75]
	v_mfma_i32_16x16x64_i8 v[72:75], v[24:27], v[32:35], v[64:67]
	v_mfma_i32_16x16x64_i8 v[64:67], v[20:23], v[36:39], v[68:71]
	v_mfma_i32_16x16x64_i8 v[68:71], v[12:15], v[32:35], v[64:67]
	s_barrier
	s_add_i32 s76, s76, 2
	s_add_u32 s77, s77, 0x100
	s_addc_u32 s80, s80, 0
	s_cmp_gt_u32 s76, 13
	s_mov_b64 s[46:47], s[8:9]
	s_cbranch_scc0 .LBB0_261
	s_and_b64 vcc, exec, s[28:29]
	s_cbranch_vccz .LBB0_264
	s_barrier

.LBB0_602:
	s_ashr_i32 s25, s24, 31
	s_lshl_b64 s[26:27], s[24:25], 20
	s_add_u32 s26, s44, s26
	s_addc_u32 s27, s45, s27
	s_and_b64 s[28:29], s[4:5], exec
	s_waitcnt lgkmcnt(0)
	ds_read_b128 v[0:3], v217
	ds_read_b128 v[4:7], v217 offset:1024
	ds_read_b128 v[8:11], v217 offset:2048
	ds_read_b128 v[12:15], v217 offset:3072
	ds_read_b128 v[16:19], v218
	ds_read_b128 v[20:23], v218 offset:1024
	ds_read_b128 v[24:27], v218 offset:2048
	ds_read_b128 v[28:31], v218 offset:3072
	ds_read_b128 v[32:35], v219
	ds_read_b128 v[36:39], v219 offset:1024
	ds_read_b128 v[40:43], v219 offset:2048
	ds_read_b128 v[44:47], v219 offset:3072
	ds_read_b128 v[48:51], v219 offset:4096
	ds_read_b128 v[52:55], v219 offset:5120
	ds_read_b128 v[56:59], v219 offset:6144
	ds_read_b128 v[60:63], v219 offset:7168
	s_cselect_b32 s7, s27, s35
	s_cselect_b32 s9, s26, s34
	s_ashr_i32 s23, s22, 31
	s_lshl_b64 s[28:29], s[22:23], 20
	s_add_u32 s28, s46, s28
	s_addc_u32 s29, s47, s29
	s_and_b64 s[36:37], s[4:5], exec
	s_cselect_b32 s23, s29, s31
	s_cselect_b32 s25, s28, s30
	s_add_u32 s36, s34, 0x100
	s_addc_u32 s37, s35, 0
	s_add_u32 s42, s30, 0x100
	s_addc_u32 s43, s31, 0
	s_add_u32 s38, s34, 0x180
	s_addc_u32 s39, s35, 0
	s_add_u32 s40, s30, 0x180
	s_addc_u32 s41, s31, 0
	s_add_u32 s60, s34, 0x80080
	s_addc_u32 s61, s35, 0
	s_add_i32 m0, s48, 0xc000
	s_nop 0
	global_load_lds_dwordx4 v213, s[60:61]
	s_nop 0
	s_add_i32 m0, s48, 0xe000
	s_nop 0
	global_load_lds_dwordx4 v214, s[60:61]
	s_waitcnt vmcnt(8)
	s_waitcnt lgkmcnt(0)
	s_barrier
	v_mfma_f32_16x16x32_bf16 v[64:67], v[0:3], v[32:35], 0
	v_mfma_f32_16x16x32_bf16 v[68:71], v[8:11], v[32:35], 0
	v_mfma_f32_16x16x32_bf16 v[72:75], v[0:3], v[40:43], 0
	v_mfma_f32_16x16x32_bf16 v[76:79], v[8:11], v[40:43], 0
	v_mfma_f32_16x16x32_bf16 v[80:83], v[0:3], v[48:51], 0
	v_mfma_f32_16x16x32_bf16 v[84:87], v[8:11], v[48:51], 0
	v_mfma_f32_16x16x32_bf16 v[88:91], v[0:3], v[56:59], 0
	v_mfma_f32_16x16x32_bf16 v[64:67], v[4:7], v[36:39], v[64:67]
	v_mfma_f32_16x16x32_bf16 v[68:71], v[12:15], v[36:39], v[68:71]
	v_mfma_f32_16x16x32_bf16 v[72:75], v[4:7], v[44:47], v[72:75]
	v_mfma_f32_16x16x32_bf16 v[76:79], v[12:15], v[44:47], v[76:79]
	v_mfma_f32_16x16x32_bf16 v[80:83], v[4:7], v[52:55], v[80:83]
	v_mfma_f32_16x16x32_bf16 v[84:87], v[12:15], v[52:55], v[84:87]
	v_mfma_f32_16x16x32_bf16 v[96:99], v[4:7], v[60:63], v[88:91]
	v_mfma_f32_16x16x32_bf16 v[88:91], v[8:11], v[56:59], 0
	v_mfma_f32_16x16x32_bf16 v[100:103], v[12:15], v[60:63], v[88:91]
	v_mfma_f32_16x16x32_bf16 v[88:91], v[16:19], v[32:35], 0
	v_mfma_f32_16x16x32_bf16 v[32:35], v[24:27], v[32:35], 0
	v_mfma_f32_16x16x32_bf16 v[104:107], v[20:23], v[36:39], v[88:91]
	v_mfma_f32_16x16x32_bf16 v[32:35], v[28:31], v[36:39], v[32:35]
	v_mfma_f32_16x16x32_bf16 v[36:39], v[16:19], v[40:43], 0
	v_mfma_f32_16x16x32_bf16 v[40:43], v[24:27], v[40:43], 0
	v_mfma_f32_16x16x32_bf16 v[36:39], v[20:23], v[44:47], v[36:39]
	v_mfma_f32_16x16x32_bf16 v[40:43], v[28:31], v[44:47], v[40:43]
	v_mfma_f32_16x16x32_bf16 v[44:47], v[16:19], v[48:51], 0
	v_mfma_f32_16x16x32_bf16 v[48:51], v[24:27], v[48:51], 0
	v_mfma_f32_16x16x32_bf16 v[44:47], v[20:23], v[52:55], v[44:47]
	v_mfma_f32_16x16x32_bf16 v[48:51], v[28:31], v[52:55], v[48:51]
	v_mfma_f32_16x16x32_bf16 v[52:55], v[16:19], v[56:59], 0
	v_mfma_f32_16x16x32_bf16 v[56:59], v[24:27], v[56:59], 0
	v_mfma_f32_16x16x32_bf16 v[52:55], v[20:23], v[60:63], v[52:55]
	v_mfma_f32_16x16x32_bf16 v[56:59], v[28:31], v[60:63], v[56:59]
	s_barrier
	ds_read_b128 v[60:63], v219 offset:16384
	ds_read_b128 v[88:91], v219 offset:17408
	ds_read_b128 v[92:95], v219 offset:18432
	ds_read_b128 v[108:111], v219 offset:19456
	ds_read_b128 v[112:115], v219 offset:20480
	ds_read_b128 v[116:119], v219 offset:21504
	ds_read_b128 v[120:123], v219 offset:22528
	ds_read_b128 v[124:127], v219 offset:23552
	s_add_i32 m0, s48, 0x10000
	s_nop 0
	global_load_lds_dwordx4 v213, s[42:43]
	s_nop 0
	s_add_i32 m0, s48, 0x12000
	s_nop 0
	global_load_lds_dwordx4 v214, s[42:43]
	s_add_u32 s42, s30, 0x80100
	s_addc_u32 s43, s31, 0
	s_add_i32 m0, s48, 0x14000
	s_nop 0
	global_load_lds_dwordx4 v213, s[42:43]
	s_nop 0
	s_add_i32 m0, s48, 0x16000
	s_nop 0
	global_load_lds_dwordx4 v214, s[42:43]
	s_nop 0
	s_add_i32 m0, s48, 0
	s_nop 0
	global_load_lds_dwordx4 v213, s[36:37]
	s_nop 0
	s_add_i32 m0, s48, 0x2000
	s_nop 0
	global_load_lds_dwordx4 v214, s[36:37]
	s_waitcnt vmcnt(8)
	s_waitcnt lgkmcnt(0)
	s_barrier
	v_mfma_f32_16x16x32_bf16 v[128:131], v[0:3], v[60:63], 0
	v_mfma_f32_16x16x32_bf16 v[132:135], v[4:7], v[88:91], v[128:131]
	v_mfma_f32_16x16x32_bf16 v[128:131], v[8:11], v[60:63], 0
	v_mfma_f32_16x16x32_bf16 v[140:143], v[12:15], v[88:91], v[128:131]
	v_mfma_f32_16x16x32_bf16 v[128:131], v[0:3], v[92:95], 0
	v_mfma_f32_16x16x32_bf16 v[148:151], v[4:7], v[108:111], v[128:131]
	v_mfma_f32_16x16x32_bf16 v[128:131], v[8:11], v[92:95], 0
	v_mfma_f32_16x16x32_bf16 v[156:159], v[12:15], v[108:111], v[128:131]
	v_mfma_f32_16x16x32_bf16 v[128:131], v[0:3], v[112:115], 0
	v_mfma_f32_16x16x32_bf16 v[0:3], v[0:3], v[120:123], 0
	v_mfma_f32_16x16x32_bf16 v[160:163], v[4:7], v[116:119], v[128:131]
	v_mfma_f32_16x16x32_bf16 v[0:3], v[4:7], v[124:127], v[0:3]
	v_mfma_f32_16x16x32_bf16 v[4:7], v[8:11], v[120:123], 0
	v_mfma_f32_16x16x32_bf16 v[128:131], v[8:11], v[112:115], 0
	v_mfma_f32_16x16x32_bf16 v[4:7], v[12:15], v[124:127], v[4:7]
	v_mfma_f32_16x16x32_bf16 v[164:167], v[12:15], v[116:119], v[128:131]
	v_mfma_f32_16x16x32_bf16 v[8:11], v[16:19], v[60:63], 0
	v_mfma_f32_16x16x32_bf16 v[168:171], v[20:23], v[88:91], v[8:11]
	v_mfma_f32_16x16x32_bf16 v[8:11], v[24:27], v[60:63], 0
	v_mfma_f32_16x16x32_bf16 v[172:175], v[28:31], v[88:91], v[8:11]
	v_mfma_f32_16x16x32_bf16 v[8:11], v[16:19], v[92:95], 0
	v_mfma_f32_16x16x32_bf16 v[176:179], v[20:23], v[108:111], v[8:11]
	v_mfma_f32_16x16x32_bf16 v[8:11], v[24:27], v[92:95], 0
	v_mfma_f32_16x16x32_bf16 v[108:111], v[28:31], v[108:111], v[8:11]
	v_mfma_f32_16x16x32_bf16 v[8:11], v[16:19], v[112:115], 0
	v_mfma_f32_16x16x32_bf16 v[180:183], v[20:23], v[116:119], v[8:11]
	v_mfma_f32_16x16x32_bf16 v[8:11], v[24:27], v[112:115], 0
	v_mfma_f32_16x16x32_bf16 v[116:119], v[28:31], v[116:119], v[8:11]
	v_mfma_f32_16x16x32_bf16 v[8:11], v[16:19], v[120:123], 0
	v_mfma_f32_16x16x32_bf16 v[184:187], v[20:23], v[124:127], v[8:11]
	v_mfma_f32_16x16x32_bf16 v[8:11], v[24:27], v[120:123], 0
	v_mfma_f32_16x16x32_bf16 v[124:127], v[28:31], v[124:127], v[8:11]
	s_barrier
	s_nop 4
	ds_read_b128 v[8:11], v220
	ds_read_b128 v[12:15], v220 offset:1024
	ds_read_b128 v[16:19], v220 offset:2048
	ds_read_b128 v[20:23], v220 offset:3072
	ds_read_b128 v[194:197], v221
	ds_read_b128 v[198:201], v221 offset:1024
	ds_read_b128 v[202:205], v221 offset:2048
	ds_read_b128 v[206:209], v221 offset:3072
	ds_read_b128 v[24:27], v219 offset:32768
	ds_read_b128 v[28:31], v219 offset:33792
	ds_read_b128 v[60:63], v219 offset:34816
	ds_read_b128 v[224:227], v219 offset:35840
	ds_read_b128 v[228:231], v219 offset:36864
	ds_read_b128 v[232:235], v219 offset:37888
	ds_read_b128 v[236:239], v219 offset:38912
	ds_read_b128 v[240:243], v219 offset:39936
	s_add_u32 s34, s34, 0x80100
	s_addc_u32 s35, s35, 0
	s_add_i32 m0, s48, 0x4000
	s_nop 0
	global_load_lds_dwordx4 v213, s[34:35]
	s_nop 0
	s_add_i32 m0, s48, 0x6000
	s_nop 0
	global_load_lds_dwordx4 v214, s[34:35]
	s_waitcnt vmcnt(8)
	s_waitcnt lgkmcnt(0)
	s_barrier
	v_mfma_f32_16x16x32_bf16 v[64:67], v[8:11], v[24:27], v[64:67]
	v_mfma_f32_16x16x32_bf16 v[152:155], v[12:15], v[28:31], v[64:67]
	v_mfma_f32_16x16x32_bf16 v[64:67], v[16:19], v[24:27], v[68:71]
	v_mfma_f32_16x16x32_bf16 v[144:147], v[20:23], v[28:31], v[64:67]
	v_mfma_f32_16x16x32_bf16 v[64:67], v[8:11], v[60:63], v[72:75]
	v_mfma_f32_16x16x32_bf16 v[120:123], v[12:15], v[224:227], v[64:67]
	v_mfma_f32_16x16x32_bf16 v[64:67], v[16:19], v[60:63], v[76:79]
	v_mfma_f32_16x16x32_bf16 v[112:115], v[20:23], v[224:227], v[64:67]
	v_mfma_f32_16x16x32_bf16 v[64:67], v[8:11], v[228:231], v[80:83]
	v_mfma_f32_16x16x32_bf16 v[92:95], v[12:15], v[232:235], v[64:67]
	v_mfma_f32_16x16x32_bf16 v[64:67], v[16:19], v[228:231], v[84:87]
	v_mfma_f32_16x16x32_bf16 v[88:91], v[20:23], v[232:235], v[64:67]
	v_mfma_f32_16x16x32_bf16 v[64:67], v[8:11], v[236:239], v[96:99]
	v_mfma_f32_16x16x32_bf16 v[76:79], v[12:15], v[240:243], v[64:67]
	v_mfma_f32_16x16x32_bf16 v[64:67], v[16:19], v[236:239], v[100:103]
	v_mfma_f32_16x16x32_bf16 v[72:75], v[20:23], v[240:243], v[64:67]
	v_mfma_f32_16x16x32_bf16 v[64:67], v[194:197], v[24:27], v[104:107]
	v_mfma_f32_16x16x32_bf16 v[24:27], v[202:205], v[24:27], v[32:35]
	v_mfma_f32_16x16x32_bf16 v[128:131], v[206:209], v[28:31], v[24:27]
	v_mfma_f32_16x16x32_bf16 v[24:27], v[194:197], v[60:63], v[36:39]
	v_mfma_f32_16x16x32_bf16 v[104:107], v[198:201], v[224:227], v[24:27]
	v_mfma_f32_16x16x32_bf16 v[24:27], v[202:205], v[60:63], v[40:43]
	v_mfma_f32_16x16x32_bf16 v[96:99], v[206:209], v[224:227], v[24:27]
	v_mfma_f32_16x16x32_bf16 v[24:27], v[194:197], v[228:231], v[44:47]
	v_mfma_f32_16x16x32_bf16 v[84:87], v[198:201], v[232:235], v[24:27]
	v_mfma_f32_16x16x32_bf16 v[24:27], v[202:205], v[228:231], v[48:51]
	v_mfma_f32_16x16x32_bf16 v[80:83], v[206:209], v[232:235], v[24:27]
	v_mfma_f32_16x16x32_bf16 v[24:27], v[194:197], v[236:239], v[52:55]
	v_mfma_f32_16x16x32_bf16 v[68:71], v[198:201], v[240:243], v[24:27]
	v_mfma_f32_16x16x32_bf16 v[24:27], v[202:205], v[236:239], v[56:59]
	v_mfma_f32_16x16x32_bf16 v[136:139], v[198:201], v[28:31], v[64:67]
	v_mfma_f32_16x16x32_bf16 v[64:67], v[206:209], v[240:243], v[24:27]
	s_barrier
	ds_read_b128 v[32:35], v219 offset:49152
	ds_read_b128 v[36:39], v219 offset:50176
	ds_read_b128 v[100:103], v219 offset:51200
	ds_read_b128 v[224:227], v219 offset:52224
	ds_read_b128 v[228:231], v219 offset:53248
	ds_read_b128 v[232:235], v219 offset:54272
	ds_read_b128 v[236:239], v219 offset:55296
	ds_read_b128 v[240:243], v219 offset:56320
	s_add_i32 m0, s48, 0x18000
	s_nop 0
	global_load_lds_dwordx4 v213, s[40:41]
	s_nop 0
	s_add_i32 m0, s48, 0x1a000
	s_nop 0
	global_load_lds_dwordx4 v214, s[40:41]
	s_add_u32 s34, s30, 0x80180
	s_addc_u32 s35, s31, 0
	s_add_i32 m0, s48, 0x1c000
	s_nop 0
	global_load_lds_dwordx4 v213, s[34:35]
	s_nop 0
	s_add_i32 m0, s48, 0x1e000
	s_nop 0
	global_load_lds_dwordx4 v214, s[34:35]
	s_nop 0
	s_add_i32 m0, s48, 0x8000
	s_nop 0
	global_load_lds_dwordx4 v213, s[38:39]
	s_nop 0
	s_add_i32 m0, s48, 0xa000
	s_nop 0
	global_load_lds_dwordx4 v214, s[38:39]
	s_waitcnt vmcnt(8)
	s_waitcnt lgkmcnt(0)
	s_barrier
	v_mfma_f32_16x16x32_bf16 v[24:27], v[8:11], v[32:35], v[132:135]
	v_mfma_f32_16x16x32_bf16 v[60:63], v[12:15], v[36:39], v[24:27]
	v_mfma_f32_16x16x32_bf16 v[24:27], v[16:19], v[32:35], v[140:143]
	v_mfma_f32_16x16x32_bf16 v[56:59], v[20:23], v[36:39], v[24:27]
	v_mfma_f32_16x16x32_bf16 v[24:27], v[8:11], v[100:103], v[148:151]
	v_mfma_f32_16x16x32_bf16 v[44:47], v[12:15], v[224:227], v[24:27]
	v_mfma_f32_16x16x32_bf16 v[24:27], v[16:19], v[100:103], v[156:159]
	v_mfma_f32_16x16x32_bf16 v[40:43], v[20:23], v[224:227], v[24:27]
	v_mfma_f32_16x16x32_bf16 v[24:27], v[8:11], v[228:231], v[160:163]
	v_mfma_f32_16x16x32_bf16 v[0:3], v[8:11], v[236:239], v[0:3]
	v_mfma_f32_16x16x32_bf16 v[28:31], v[12:15], v[232:235], v[24:27]
	v_mfma_f32_16x16x32_bf16 v[24:27], v[16:19], v[228:231], v[164:167]
	v_mfma_f32_16x16x32_bf16 v[12:15], v[12:15], v[240:243], v[0:3]
	v_mfma_f32_16x16x32_bf16 v[0:3], v[16:19], v[236:239], v[4:7]
	v_mfma_f32_16x16x32_bf16 v[24:27], v[20:23], v[232:235], v[24:27]
	v_mfma_f32_16x16x32_bf16 v[8:11], v[20:23], v[240:243], v[0:3]
	v_mfma_f32_16x16x32_bf16 v[0:3], v[194:197], v[32:35], v[168:171]
	v_mfma_f32_16x16x32_bf16 v[52:55], v[198:201], v[36:39], v[0:3]
	v_mfma_f32_16x16x32_bf16 v[0:3], v[202:205], v[32:35], v[172:175]
	v_mfma_f32_16x16x32_bf16 v[48:51], v[206:209], v[36:39], v[0:3]
	v_mfma_f32_16x16x32_bf16 v[0:3], v[194:197], v[100:103], v[176:179]
	v_mfma_f32_16x16x32_bf16 v[36:39], v[198:201], v[224:227], v[0:3]
	v_mfma_f32_16x16x32_bf16 v[0:3], v[202:205], v[100:103], v[108:111]
	v_mfma_f32_16x16x32_bf16 v[32:35], v[206:209], v[224:227], v[0:3]
	v_mfma_f32_16x16x32_bf16 v[0:3], v[194:197], v[228:231], v[180:183]
	v_mfma_f32_16x16x32_bf16 v[20:23], v[198:201], v[232:235], v[0:3]
	v_mfma_f32_16x16x32_bf16 v[0:3], v[202:205], v[228:231], v[116:119]
	v_mfma_f32_16x16x32_bf16 v[16:19], v[206:209], v[232:235], v[0:3]
	v_mfma_f32_16x16x32_bf16 v[0:3], v[194:197], v[236:239], v[184:187]
	v_mfma_f32_16x16x32_bf16 v[4:7], v[198:201], v[240:243], v[0:3]
	v_mfma_f32_16x16x32_bf16 v[0:3], v[202:205], v[236:239], v[124:127]
	v_mfma_f32_16x16x32_bf16 v[0:3], v[206:209], v[240:243], v[0:3]
	s_barrier
	s_add_u32 s59, s30, 0x200
	s_addc_u32 s60, s31, 0
	s_mov_b32 s61, 0
.LBB0_603:
	ds_read_b128 v[100:103], v217
	ds_read_b128 v[108:111], v217 offset:1024
	ds_read_b128 v[116:119], v217 offset:2048
	ds_read_b128 v[124:127], v217 offset:3072
	ds_read_b128 v[132:135], v218
	ds_read_b128 v[140:143], v218 offset:1024
	ds_read_b128 v[148:151], v218 offset:2048
	ds_read_b128 v[156:159], v218 offset:3072
	ds_read_b128 v[160:163], v219
	ds_read_b128 v[164:167], v219 offset:1024
	ds_read_b128 v[168:171], v219 offset:2048
	ds_read_b128 v[172:175], v219 offset:3072
	ds_read_b128 v[176:179], v219 offset:4096
	ds_read_b128 v[180:183], v219 offset:5120
	ds_read_b128 v[184:187], v219 offset:6144
	ds_read_b128 v[194:197], v219 offset:7168
	s_add_u32 s30, s36, 0x100
	s_addc_u32 s31, s37, 0
	s_cmp_eq_u32 s61, 28
	s_cselect_b32 s42, s9, s30
	s_cselect_b32 s43, s7, s31
	s_cselect_b32 s38, s25, s59
	s_cselect_b32 s39, s23, s60
	s_add_u32 s34, s42, 0x80
	s_addc_u32 s35, s43, 0
	s_add_u32 s40, s38, 0x80
	s_addc_u32 s41, s39, 0
	s_add_u32 s36, s36, 0x80080
	s_addc_u32 s37, s37, 0
	s_add_i32 m0, s48, 0xc000
	s_nop 0
	global_load_lds_dwordx4 v213, s[36:37]
	s_nop 0
	s_add_i32 m0, s48, 0xe000
	s_nop 0
	global_load_lds_dwordx4 v214, s[36:37]
	s_waitcnt vmcnt(8)
	s_waitcnt lgkmcnt(0)
	s_barrier
	v_mfma_f32_16x16x32_bf16 v[152:155], v[100:103], v[160:163], v[152:155]
	v_mfma_f32_16x16x32_bf16 v[144:147], v[116:119], v[160:163], v[144:147]
	v_mfma_f32_16x16x32_bf16 v[112:115], v[116:119], v[168:171], v[112:115]
	v_mfma_f32_16x16x32_bf16 v[120:123], v[100:103], v[168:171], v[120:123]
	v_mfma_f32_16x16x32_bf16 v[92:95], v[100:103], v[176:179], v[92:95]
	v_mfma_f32_16x16x32_bf16 v[88:91], v[116:119], v[176:179], v[88:91]
	v_mfma_f32_16x16x32_bf16 v[72:75], v[116:119], v[184:187], v[72:75]
	v_mfma_f32_16x16x32_bf16 v[76:79], v[100:103], v[184:187], v[76:79]
	v_mfma_f32_16x16x32_bf16 v[152:155], v[108:111], v[164:167], v[152:155]
	v_mfma_f32_16x16x32_bf16 v[144:147], v[124:127], v[164:167], v[144:147]
	v_mfma_f32_16x16x32_bf16 v[112:115], v[124:127], v[172:175], v[112:115]
	v_mfma_f32_16x16x32_bf16 v[120:123], v[108:111], v[172:175], v[120:123]
	v_mfma_f32_16x16x32_bf16 v[92:95], v[108:111], v[180:183], v[92:95]
	v_mfma_f32_16x16x32_bf16 v[88:91], v[124:127], v[180:183], v[88:91]
	v_mfma_f32_16x16x32_bf16 v[72:75], v[124:127], v[194:197], v[72:75]
	v_mfma_f32_16x16x32_bf16 v[76:79], v[108:111], v[194:197], v[76:79]
	v_mfma_f32_16x16x32_bf16 v[136:139], v[132:135], v[160:163], v[136:139]
	v_mfma_f32_16x16x32_bf16 v[128:131], v[148:151], v[160:163], v[128:131]
	v_mfma_f32_16x16x32_bf16 v[96:99], v[148:151], v[168:171], v[96:99]
	v_mfma_f32_16x16x32_bf16 v[104:107], v[132:135], v[168:171], v[104:107]
	v_mfma_f32_16x16x32_bf16 v[84:87], v[132:135], v[176:179], v[84:87]
	v_mfma_f32_16x16x32_bf16 v[80:83], v[148:151], v[176:179], v[80:83]
	v_mfma_f32_16x16x32_bf16 v[64:67], v[148:151], v[184:187], v[64:67]
	v_mfma_f32_16x16x32_bf16 v[68:71], v[132:135], v[184:187], v[68:71]
	v_mfma_f32_16x16x32_bf16 v[136:139], v[140:143], v[164:167], v[136:139]
	v_mfma_f32_16x16x32_bf16 v[128:131], v[156:159], v[164:167], v[128:131]
	v_mfma_f32_16x16x32_bf16 v[96:99], v[156:159], v[172:175], v[96:99]
	v_mfma_f32_16x16x32_bf16 v[104:107], v[140:143], v[172:175], v[104:107]
	v_mfma_f32_16x16x32_bf16 v[84:87], v[140:143], v[180:183], v[84:87]
	v_mfma_f32_16x16x32_bf16 v[80:83], v[156:159], v[180:183], v[80:83]
	v_mfma_f32_16x16x32_bf16 v[64:67], v[156:159], v[194:197], v[64:67]
	v_mfma_f32_16x16x32_bf16 v[68:71], v[140:143], v[194:197], v[68:71]
	s_barrier
	ds_read_b128 v[160:163], v219 offset:16384
	ds_read_b128 v[164:167], v219 offset:17408
	ds_read_b128 v[168:171], v219 offset:18432
	ds_read_b128 v[172:175], v219 offset:19456
	ds_read_b128 v[176:179], v219 offset:20480
	ds_read_b128 v[180:183], v219 offset:21504
	ds_read_b128 v[184:187], v219 offset:22528
	ds_read_b128 v[194:197], v219 offset:23552
	s_add_i32 m0, s48, 0x10000
	s_nop 0
	global_load_lds_dwordx4 v213, s[38:39]
	s_nop 0
	s_add_i32 m0, s48, 0x12000
	s_nop 0
	global_load_lds_dwordx4 v214, s[38:39]
	s_add_u32 s36, s38, 0x80000
	s_addc_u32 s37, s39, 0
	s_add_i32 m0, s48, 0x14000
	s_nop 0
	global_load_lds_dwordx4 v213, s[36:37]
	s_nop 0
	s_add_i32 m0, s48, 0x16000
	s_nop 0
	global_load_lds_dwordx4 v214, s[36:37]
	s_nop 0
	s_add_i32 m0, s48, 0
	s_nop 0
	global_load_lds_dwordx4 v213, s[42:43]
	s_nop 0
	s_add_i32 m0, s48, 0x2000
	s_nop 0
	global_load_lds_dwordx4 v214, s[42:43]
	s_waitcnt vmcnt(8)
	s_waitcnt lgkmcnt(0)
	s_barrier
	v_mfma_f32_16x16x32_bf16 v[60:63], v[100:103], v[160:163], v[60:63]
	v_mfma_f32_16x16x32_bf16 v[56:59], v[116:119], v[160:163], v[56:59]
	v_mfma_f32_16x16x32_bf16 v[40:43], v[116:119], v[168:171], v[40:43]
	v_mfma_f32_16x16x32_bf16 v[44:47], v[100:103], v[168:171], v[44:47]
	v_mfma_f32_16x16x32_bf16 v[28:31], v[100:103], v[176:179], v[28:31]
	v_mfma_f32_16x16x32_bf16 v[24:27], v[116:119], v[176:179], v[24:27]
	v_mfma_f32_16x16x32_bf16 v[8:11], v[116:119], v[184:187], v[8:11]
	v_mfma_f32_16x16x32_bf16 v[12:15], v[100:103], v[184:187], v[12:15]
	v_mfma_f32_16x16x32_bf16 v[60:63], v[108:111], v[164:167], v[60:63]
	v_mfma_f32_16x16x32_bf16 v[56:59], v[124:127], v[164:167], v[56:59]
	v_mfma_f32_16x16x32_bf16 v[40:43], v[124:127], v[172:175], v[40:43]
	v_mfma_f32_16x16x32_bf16 v[44:47], v[108:111], v[172:175], v[44:47]
	v_mfma_f32_16x16x32_bf16 v[28:31], v[108:111], v[180:183], v[28:31]
	v_mfma_f32_16x16x32_bf16 v[24:27], v[124:127], v[180:183], v[24:27]
	v_mfma_f32_16x16x32_bf16 v[8:11], v[124:127], v[194:197], v[8:11]
	v_mfma_f32_16x16x32_bf16 v[12:15], v[108:111], v[194:197], v[12:15]
	v_mfma_f32_16x16x32_bf16 v[52:55], v[132:135], v[160:163], v[52:55]
	v_mfma_f32_16x16x32_bf16 v[48:51], v[148:151], v[160:163], v[48:51]
	v_mfma_f32_16x16x32_bf16 v[32:35], v[148:151], v[168:171], v[32:35]
	v_mfma_f32_16x16x32_bf16 v[36:39], v[132:135], v[168:171], v[36:39]
	v_mfma_f32_16x16x32_bf16 v[20:23], v[132:135], v[176:179], v[20:23]
	v_mfma_f32_16x16x32_bf16 v[16:19], v[148:151], v[176:179], v[16:19]
	v_mfma_f32_16x16x32_bf16 v[0:3], v[148:151], v[184:187], v[0:3]
	v_mfma_f32_16x16x32_bf16 v[4:7], v[132:135], v[184:187], v[4:7]
	v_mfma_f32_16x16x32_bf16 v[52:55], v[140:143], v[164:167], v[52:55]
	v_mfma_f32_16x16x32_bf16 v[48:51], v[156:159], v[164:167], v[48:51]
	v_mfma_f32_16x16x32_bf16 v[32:35], v[156:159], v[172:175], v[32:35]
	v_mfma_f32_16x16x32_bf16 v[36:39], v[140:143], v[172:175], v[36:39]
	v_mfma_f32_16x16x32_bf16 v[20:23], v[140:143], v[180:183], v[20:23]
	v_mfma_f32_16x16x32_bf16 v[16:19], v[156:159], v[180:183], v[16:19]
	v_mfma_f32_16x16x32_bf16 v[0:3], v[156:159], v[194:197], v[0:3]
	v_mfma_f32_16x16x32_bf16 v[4:7], v[140:143], v[194:197], v[4:7]
	s_barrier
	ds_read_b128 v[100:103], v220
	ds_read_b128 v[108:111], v220 offset:1024
	ds_read_b128 v[116:119], v220 offset:2048
	ds_read_b128 v[124:127], v220 offset:3072
	ds_read_b128 v[132:135], v221
	ds_read_b128 v[140:143], v221 offset:1024
	ds_read_b128 v[148:151], v221 offset:2048
	ds_read_b128 v[156:159], v221 offset:3072
	ds_read_b128 v[160:163], v219 offset:32768
	ds_read_b128 v[164:167], v219 offset:33792
	ds_read_b128 v[168:171], v219 offset:34816
	ds_read_b128 v[172:175], v219 offset:35840
	ds_read_b128 v[176:179], v219 offset:36864
	ds_read_b128 v[180:183], v219 offset:37888
	ds_read_b128 v[184:187], v219 offset:38912
	ds_read_b128 v[194:197], v219 offset:39936
	s_add_u32 s36, s42, 0x80000
	s_addc_u32 s37, s43, 0
	s_add_i32 m0, s48, 0x4000
	s_nop 0
	global_load_lds_dwordx4 v213, s[36:37]
	s_nop 0
	s_add_i32 m0, s48, 0x6000
	s_nop 0
	global_load_lds_dwordx4 v214, s[36:37]
	s_waitcnt vmcnt(8)
	s_waitcnt lgkmcnt(0)
	s_barrier
	v_mfma_f32_16x16x32_bf16 v[152:155], v[100:103], v[160:163], v[152:155]
	v_mfma_f32_16x16x32_bf16 v[144:147], v[116:119], v[160:163], v[144:147]
	v_mfma_f32_16x16x32_bf16 v[112:115], v[116:119], v[168:171], v[112:115]
	v_mfma_f32_16x16x32_bf16 v[120:123], v[100:103], v[168:171], v[120:123]
	v_mfma_f32_16x16x32_bf16 v[92:95], v[100:103], v[176:179], v[92:95]
	v_mfma_f32_16x16x32_bf16 v[88:91], v[116:119], v[176:179], v[88:91]
	v_mfma_f32_16x16x32_bf16 v[72:75], v[116:119], v[184:187], v[72:75]
	v_mfma_f32_16x16x32_bf16 v[76:79], v[100:103], v[184:187], v[76:79]
	v_mfma_f32_16x16x32_bf16 v[152:155], v[108:111], v[164:167], v[152:155]
	v_mfma_f32_16x16x32_bf16 v[144:147], v[124:127], v[164:167], v[144:147]
	v_mfma_f32_16x16x32_bf16 v[112:115], v[124:127], v[172:175], v[112:115]
	v_mfma_f32_16x16x32_bf16 v[120:123], v[108:111], v[172:175], v[120:123]
	v_mfma_f32_16x16x32_bf16 v[92:95], v[108:111], v[180:183], v[92:95]
	v_mfma_f32_16x16x32_bf16 v[88:91], v[124:127], v[180:183], v[88:91]
	v_mfma_f32_16x16x32_bf16 v[72:75], v[124:127], v[194:197], v[72:75]
	v_mfma_f32_16x16x32_bf16 v[76:79], v[108:111], v[194:197], v[76:79]
	v_mfma_f32_16x16x32_bf16 v[136:139], v[132:135], v[160:163], v[136:139]
	v_mfma_f32_16x16x32_bf16 v[128:131], v[148:151], v[160:163], v[128:131]
	v_mfma_f32_16x16x32_bf16 v[96:99], v[148:151], v[168:171], v[96:99]
	v_mfma_f32_16x16x32_bf16 v[104:107], v[132:135], v[168:171], v[104:107]
	v_mfma_f32_16x16x32_bf16 v[84:87], v[132:135], v[176:179], v[84:87]
	v_mfma_f32_16x16x32_bf16 v[80:83], v[148:151], v[176:179], v[80:83]
	v_mfma_f32_16x16x32_bf16 v[64:67], v[148:151], v[184:187], v[64:67]
	v_mfma_f32_16x16x32_bf16 v[68:71], v[132:135], v[184:187], v[68:71]
	v_mfma_f32_16x16x32_bf16 v[136:139], v[140:143], v[164:167], v[136:139]
	v_mfma_f32_16x16x32_bf16 v[128:131], v[156:159], v[164:167], v[128:131]
	v_mfma_f32_16x16x32_bf16 v[96:99], v[156:159], v[172:175], v[96:99]
	v_mfma_f32_16x16x32_bf16 v[104:107], v[140:143], v[172:175], v[104:107]
	v_mfma_f32_16x16x32_bf16 v[84:87], v[140:143], v[180:183], v[84:87]
	v_mfma_f32_16x16x32_bf16 v[80:83], v[156:159], v[180:183], v[80:83]
	v_mfma_f32_16x16x32_bf16 v[64:67], v[156:159], v[194:197], v[64:67]
	v_mfma_f32_16x16x32_bf16 v[68:71], v[140:143], v[194:197], v[68:71]
	s_barrier
	ds_read_b128 v[160:163], v219 offset:49152
	ds_read_b128 v[164:167], v219 offset:50176
	ds_read_b128 v[168:171], v219 offset:51200
	ds_read_b128 v[172:175], v219 offset:52224
	ds_read_b128 v[176:179], v219 offset:53248
	ds_read_b128 v[180:183], v219 offset:54272
	ds_read_b128 v[184:187], v219 offset:55296
	ds_read_b128 v[194:197], v219 offset:56320
	s_add_i32 m0, s48, 0x18000
	s_nop 0
	global_load_lds_dwordx4 v213, s[40:41]
	s_nop 0
	s_add_i32 m0, s48, 0x1a000
	s_nop 0
	global_load_lds_dwordx4 v214, s[40:41]
	s_add_u32 s36, s38, 0x80080
	s_addc_u32 s37, s39, 0
	s_add_i32 m0, s48, 0x1c000
	s_nop 0
	global_load_lds_dwordx4 v213, s[36:37]
	s_nop 0
	s_add_i32 m0, s48, 0x1e000
	s_nop 0
	global_load_lds_dwordx4 v214, s[36:37]
	s_nop 0
	s_add_i32 m0, s48, 0x8000
	s_nop 0
	global_load_lds_dwordx4 v213, s[34:35]
	s_nop 0
	s_add_i32 m0, s48, 0xa000
	s_nop 0
	global_load_lds_dwordx4 v214, s[34:35]
	s_waitcnt vmcnt(8)
	s_waitcnt lgkmcnt(0)
	s_barrier
	v_mfma_f32_16x16x32_bf16 v[60:63], v[100:103], v[160:163], v[60:63]
	v_mfma_f32_16x16x32_bf16 v[56:59], v[116:119], v[160:163], v[56:59]
	v_mfma_f32_16x16x32_bf16 v[40:43], v[116:119], v[168:171], v[40:43]
	v_mfma_f32_16x16x32_bf16 v[44:47], v[100:103], v[168:171], v[44:47]
	v_mfma_f32_16x16x32_bf16 v[28:31], v[100:103], v[176:179], v[28:31]
	v_mfma_f32_16x16x32_bf16 v[24:27], v[116:119], v[176:179], v[24:27]
	v_mfma_f32_16x16x32_bf16 v[8:11], v[116:119], v[184:187], v[8:11]
	v_mfma_f32_16x16x32_bf16 v[12:15], v[100:103], v[184:187], v[12:15]
	v_mfma_f32_16x16x32_bf16 v[60:63], v[108:111], v[164:167], v[60:63]
	v_mfma_f32_16x16x32_bf16 v[56:59], v[124:127], v[164:167], v[56:59]
	v_mfma_f32_16x16x32_bf16 v[40:43], v[124:127], v[172:175], v[40:43]
	v_mfma_f32_16x16x32_bf16 v[44:47], v[108:111], v[172:175], v[44:47]
	v_mfma_f32_16x16x32_bf16 v[28:31], v[108:111], v[180:183], v[28:31]
	v_mfma_f32_16x16x32_bf16 v[24:27], v[124:127], v[180:183], v[24:27]
	v_mfma_f32_16x16x32_bf16 v[8:11], v[124:127], v[194:197], v[8:11]
	v_mfma_f32_16x16x32_bf16 v[12:15], v[108:111], v[194:197], v[12:15]
	v_mfma_f32_16x16x32_bf16 v[52:55], v[132:135], v[160:163], v[52:55]
	v_mfma_f32_16x16x32_bf16 v[48:51], v[148:151], v[160:163], v[48:51]
	v_mfma_f32_16x16x32_bf16 v[32:35], v[148:151], v[168:171], v[32:35]
	v_mfma_f32_16x16x32_bf16 v[36:39], v[132:135], v[168:171], v[36:39]
	v_mfma_f32_16x16x32_bf16 v[20:23], v[132:135], v[176:179], v[20:23]
	v_mfma_f32_16x16x32_bf16 v[16:19], v[148:151], v[176:179], v[16:19]
	v_mfma_f32_16x16x32_bf16 v[0:3], v[148:151], v[184:187], v[0:3]
	v_mfma_f32_16x16x32_bf16 v[4:7], v[132:135], v[184:187], v[4:7]
	v_mfma_f32_16x16x32_bf16 v[52:55], v[140:143], v[164:167], v[52:55]
	v_mfma_f32_16x16x32_bf16 v[48:51], v[156:159], v[164:167], v[48:51]
	v_mfma_f32_16x16x32_bf16 v[32:35], v[156:159], v[172:175], v[32:35]
	v_mfma_f32_16x16x32_bf16 v[36:39], v[140:143], v[172:175], v[36:39]
	v_mfma_f32_16x16x32_bf16 v[20:23], v[140:143], v[180:183], v[20:23]
	v_mfma_f32_16x16x32_bf16 v[16:19], v[156:159], v[180:183], v[16:19]
	v_mfma_f32_16x16x32_bf16 v[0:3], v[156:159], v[194:197], v[0:3]
	v_mfma_f32_16x16x32_bf16 v[4:7], v[140:143], v[194:197], v[4:7]
	s_barrier
	s_add_i32 s61, s61, 2
	s_add_u32 s59, s59, 0x100
	s_addc_u32 s60, s60, 0
	s_cmp_gt_u32 s61, 29
	s_mov_b64 s[36:37], s[30:31]
	s_cbranch_scc0 .LBB0_603
	s_and_b64 vcc, exec, s[20:21]
	s_cbranch_vccz .LBB0_606
	s_barrier

.LBB0_752:
	s_ashr_i32 s17, s16, 31
	s_lshl_b64 s[18:19], s[16:17], 19
	s_add_u32 s18, s40, s18
	s_addc_u32 s19, s41, s19
	s_and_b64 s[20:21], s[4:5], exec
	s_cselect_b32 s58, s19, s29
	s_cselect_b32 s59, s18, s28
	s_ashr_i32 s15, s14, 31
	s_lshl_b64 s[20:21], s[14:15], 19
	s_add_u32 s20, s42, s20
	s_addc_u32 s21, s43, s21
	s_and_b64 s[26:27], s[4:5], exec
	ds_read_b128 v[0:3], v204 offset:3072
	ds_read_b128 v[4:7], v204 offset:2048
	ds_read_b128 v[8:11], v204 offset:1024
	ds_read_b128 v[12:15], v204
	ds_read_b128 v[16:19], v205 offset:3072
	ds_read_b128 v[20:23], v205 offset:2048
	ds_read_b128 v[24:27], v205 offset:1024
	ds_read_b128 v[28:31], v205
	ds_read_b128 v[32:35], v206
	ds_read_b128 v[36:39], v206 offset:1024
	ds_read_b128 v[40:43], v206 offset:2048
	ds_read_b128 v[44:47], v206 offset:3072
	ds_read_b128 v[48:51], v206 offset:4096
	ds_read_b128 v[52:55], v206 offset:5120
	ds_read_b128 v[56:59], v206 offset:6144
	ds_read_b128 v[60:63], v206 offset:7168
	s_cselect_b32 s15, s21, s25
	s_cselect_b32 s60, s20, s24
	s_lshl_b32 s26, s55, 11
	s_and_b32 s26, s26, 0x800
	s_or_b32 s38, s26, s49
	s_lshl_b64 s[30:31], s[16:17], 11
	s_add_u32 s26, s28, 0x100
	s_addc_u32 s27, s29, 0
	s_add_u32 s62, s24, 0x100
	s_addc_u32 s63, s25, 0
	s_add_u32 s34, s28, 0x180
	s_addc_u32 s35, s29, 0
	s_add_u32 s36, s24, 0x180
	s_addc_u32 s37, s25, 0
	s_add_u32 s66, s28, 0x40080
	s_addc_u32 s67, s29, 0
	s_add_i32 m0, s46, 0xc000
	s_nop 0
	global_load_lds_dwordx4 v199, s[66:67]
	s_nop 0
	s_add_i32 m0, s46, 0xe000
	s_nop 0
	global_load_lds_dwordx4 v201, s[66:67]
	s_waitcnt vmcnt(8)
	s_waitcnt lgkmcnt(0)
	s_barrier
	s_waitcnt lgkmcnt(7)
	v_mfma_i32_16x16x64_i8 v[64:67], v[28:31], v[32:35], 0
	s_mov_b32 s17, 0
	v_mfma_i32_16x16x64_i8 v[68:71], v[20:23], v[32:35], 0
	s_waitcnt lgkmcnt(5)
	v_mfma_i32_16x16x64_i8 v[72:75], v[28:31], v[40:43], 0
	v_mfma_i32_16x16x64_i8 v[132:135], v[24:27], v[36:39], v[64:67]
	v_mfma_i32_16x16x64_i8 v[136:139], v[16:19], v[36:39], v[68:71]
	s_waitcnt lgkmcnt(4)
	v_mfma_i32_16x16x64_i8 v[144:147], v[24:27], v[44:47], v[72:75]
	v_mfma_i32_16x16x64_i8 v[76:79], v[20:23], v[40:43], 0
	s_waitcnt lgkmcnt(3)
	v_mfma_i32_16x16x64_i8 v[80:83], v[28:31], v[48:51], 0
	v_mfma_i32_16x16x64_i8 v[84:87], v[20:23], v[48:51], 0
	s_waitcnt lgkmcnt(1)
	v_mfma_i32_16x16x64_i8 v[88:91], v[28:31], v[56:59], 0
	v_mfma_i32_16x16x64_i8 v[92:95], v[20:23], v[56:59], 0
	v_mfma_i32_16x16x64_i8 v[76:79], v[16:19], v[44:47], v[76:79]
	v_mfma_i32_16x16x64_i8 v[80:83], v[24:27], v[52:55], v[80:83]
	v_mfma_i32_16x16x64_i8 v[84:87], v[16:19], v[52:55], v[84:87]
	s_waitcnt lgkmcnt(0)
	v_mfma_i32_16x16x64_i8 v[88:91], v[24:27], v[60:63], v[88:91]
	v_mfma_i32_16x16x64_i8 v[92:95], v[16:19], v[60:63], v[92:95]
	v_mfma_i32_16x16x64_i8 v[96:99], v[12:15], v[32:35], 0
	v_mfma_i32_16x16x64_i8 v[32:35], v[4:7], v[32:35], 0
	v_mfma_i32_16x16x64_i8 v[96:99], v[8:11], v[36:39], v[96:99]
	v_mfma_i32_16x16x64_i8 v[32:35], v[0:3], v[36:39], v[32:35]
	v_mfma_i32_16x16x64_i8 v[36:39], v[12:15], v[40:43], 0
	v_mfma_i32_16x16x64_i8 v[40:43], v[4:7], v[40:43], 0
	v_mfma_i32_16x16x64_i8 v[36:39], v[8:11], v[44:47], v[36:39]
	v_mfma_i32_16x16x64_i8 v[40:43], v[0:3], v[44:47], v[40:43]
	v_mfma_i32_16x16x64_i8 v[44:47], v[12:15], v[48:51], 0
	v_mfma_i32_16x16x64_i8 v[48:51], v[4:7], v[48:51], 0
	v_mfma_i32_16x16x64_i8 v[44:47], v[8:11], v[52:55], v[44:47]
	v_mfma_i32_16x16x64_i8 v[48:51], v[0:3], v[52:55], v[48:51]
	v_mfma_i32_16x16x64_i8 v[52:55], v[12:15], v[56:59], 0
	v_mfma_i32_16x16x64_i8 v[56:59], v[4:7], v[56:59], 0
	v_mfma_i32_16x16x64_i8 v[52:55], v[8:11], v[60:63], v[52:55]
	v_mfma_i32_16x16x64_i8 v[56:59], v[0:3], v[60:63], v[56:59]
	s_barrier
	ds_read_b128 v[60:63], v206 offset:16384
	ds_read_b128 v[100:103], v206 offset:17408
	ds_read_b128 v[104:107], v206 offset:18432
	ds_read_b128 v[108:111], v206 offset:19456
	ds_read_b128 v[112:115], v206 offset:20480
	ds_read_b128 v[116:119], v206 offset:21504
	ds_read_b128 v[120:123], v206 offset:22528
	ds_read_b128 v[124:127], v206 offset:23552
	s_add_i32 m0, s46, 0x10000
	s_nop 0
	global_load_lds_dwordx4 v200, s[62:63]
	s_nop 0
	s_add_i32 m0, s46, 0x12000
	s_nop 0
	global_load_lds_dwordx4 v202, s[62:63]
	s_add_u32 s62, s24, 0x40100
	s_addc_u32 s63, s25, 0
	s_add_i32 m0, s46, 0x14000
	s_nop 0
	global_load_lds_dwordx4 v200, s[62:63]
	s_nop 0
	s_add_i32 m0, s46, 0x16000
	s_nop 0
	global_load_lds_dwordx4 v202, s[62:63]
	s_nop 0
	s_add_i32 m0, s46, 0
	s_nop 0
	global_load_lds_dwordx4 v199, s[26:27]
	s_nop 0
	s_add_i32 m0, s46, 0x2000
	s_nop 0
	global_load_lds_dwordx4 v201, s[26:27]
	s_waitcnt vmcnt(8)
	s_waitcnt lgkmcnt(0)
	s_barrier
	v_mfma_i32_16x16x64_i8 v[128:131], v[28:31], v[60:63], 0
	v_mfma_i32_16x16x64_i8 v[210:213], v[24:27], v[100:103], v[128:131]
	v_mfma_i32_16x16x64_i8 v[128:131], v[20:23], v[60:63], 0
	v_mfma_i32_16x16x64_i8 v[214:217], v[16:19], v[100:103], v[128:131]
	v_mfma_i32_16x16x64_i8 v[128:131], v[28:31], v[104:107], 0
	v_mfma_i32_16x16x64_i8 v[218:221], v[24:27], v[108:111], v[128:131]
	v_mfma_i32_16x16x64_i8 v[128:131], v[20:23], v[104:107], 0
	v_mfma_i32_16x16x64_i8 v[222:225], v[16:19], v[108:111], v[128:131]
	v_mfma_i32_16x16x64_i8 v[128:131], v[28:31], v[112:115], 0
	v_mfma_i32_16x16x64_i8 v[226:229], v[24:27], v[116:119], v[128:131]
	v_mfma_i32_16x16x64_i8 v[128:131], v[20:23], v[112:115], 0
	v_mfma_i32_16x16x64_i8 v[28:31], v[28:31], v[120:123], 0
	v_mfma_i32_16x16x64_i8 v[20:23], v[20:23], v[120:123], 0
	v_mfma_i32_16x16x64_i8 v[230:233], v[16:19], v[116:119], v[128:131]
	v_mfma_i32_16x16x64_i8 v[24:27], v[24:27], v[124:127], v[28:31]
	v_mfma_i32_16x16x64_i8 v[20:23], v[16:19], v[124:127], v[20:23]
	v_mfma_i32_16x16x64_i8 v[16:19], v[12:15], v[60:63], 0
	v_mfma_i32_16x16x64_i8 v[28:31], v[8:11], v[100:103], v[16:19]
	v_mfma_i32_16x16x64_i8 v[16:19], v[4:7], v[60:63], 0
	v_mfma_i32_16x16x64_i8 v[60:63], v[0:3], v[100:103], v[16:19]
	v_mfma_i32_16x16x64_i8 v[16:19], v[12:15], v[104:107], 0
	v_mfma_i32_16x16x64_i8 v[100:103], v[8:11], v[108:111], v[16:19]
	v_mfma_i32_16x16x64_i8 v[16:19], v[4:7], v[104:107], 0
	v_mfma_i32_16x16x64_i8 v[234:237], v[0:3], v[108:111], v[16:19]
	v_mfma_i32_16x16x64_i8 v[16:19], v[12:15], v[112:115], 0
	v_mfma_i32_16x16x64_i8 v[238:241], v[8:11], v[116:119], v[16:19]
	v_mfma_i32_16x16x64_i8 v[16:19], v[4:7], v[112:115], 0
	v_mfma_i32_16x16x64_i8 v[12:15], v[12:15], v[120:123], 0
	v_mfma_i32_16x16x64_i8 v[4:7], v[4:7], v[120:123], 0
	v_mfma_i32_16x16x64_i8 v[12:15], v[8:11], v[124:127], v[12:15]
	v_mfma_i32_16x16x64_i8 v[4:7], v[0:3], v[124:127], v[4:7]
	v_mfma_i32_16x16x64_i8 v[242:245], v[0:3], v[116:119], v[16:19]
	s_barrier
	ds_read_b128 v[0:3], v207
	ds_read_b128 v[8:11], v207 offset:1024
	ds_read_b128 v[108:111], v207 offset:2048
	ds_read_b128 v[116:119], v207 offset:3072
	ds_read_b128 v[246:249], v208
	ds_read_b128 v[250:253], v208 offset:1024
	ds_read_b128 v[192:195], v208 offset:2048
	ds_read_b128 v[64:67], v208 offset:3072
	ds_read_b128 v[16:19], v206 offset:32768
	ds_read_b128 v[104:107], v206 offset:33792
	ds_read_b128 v[112:115], v206 offset:34816
	ds_read_b128 v[120:123], v206 offset:35840
	ds_read_b128 v[124:127], v206 offset:36864
	ds_read_b128 v[140:143], v206 offset:37888
	ds_read_b128 v[68:71], v206 offset:38912
	ds_read_b128 v[72:75], v206 offset:39936
	s_add_u32 s28, s28, 0x40100
	s_addc_u32 s29, s29, 0
	s_add_i32 m0, s46, 0x4000
	s_nop 0
	global_load_lds_dwordx4 v199, s[28:29]
	s_nop 0
	s_add_i32 m0, s46, 0x6000
	s_nop 0
	global_load_lds_dwordx4 v201, s[28:29]
	s_waitcnt vmcnt(8)
	s_waitcnt lgkmcnt(0)
	s_barrier
	v_mfma_i32_16x16x64_i8 v[76:79], v[108:111], v[112:115], v[76:79]
	v_mfma_i32_16x16x64_i8 v[128:131], v[0:3], v[16:19], v[132:135]
	v_mfma_i32_16x16x64_i8 v[160:163], v[116:119], v[120:123], v[76:79]
	v_mfma_i32_16x16x64_i8 v[76:79], v[0:3], v[124:127], v[80:83]
	v_mfma_i32_16x16x64_i8 v[184:187], v[8:11], v[104:107], v[128:131]
	v_mfma_i32_16x16x64_i8 v[128:131], v[108:111], v[16:19], v[136:139]
	v_mfma_i32_16x16x64_i8 v[152:155], v[8:11], v[140:143], v[76:79]
	v_mfma_i32_16x16x64_i8 v[76:79], v[108:111], v[124:127], v[84:87]
	v_mfma_i32_16x16x64_i8 v[176:179], v[116:119], v[104:107], v[128:131]
	v_mfma_i32_16x16x64_i8 v[128:131], v[0:3], v[112:115], v[144:147]
	v_mfma_i32_16x16x64_i8 v[144:147], v[116:119], v[140:143], v[76:79]
	v_mfma_i32_16x16x64_i8 v[76:79], v[0:3], v[68:71], v[88:91]
	v_mfma_i32_16x16x64_i8 v[136:139], v[8:11], v[72:75], v[76:79]
	v_mfma_i32_16x16x64_i8 v[76:79], v[108:111], v[68:71], v[92:95]
	v_mfma_i32_16x16x64_i8 v[168:171], v[8:11], v[120:123], v[128:131]
	v_mfma_i32_16x16x64_i8 v[128:131], v[116:119], v[72:75], v[76:79]
	v_mfma_i32_16x16x64_i8 v[76:79], v[246:249], v[16:19], v[96:99]
	v_mfma_i32_16x16x64_i8 v[16:19], v[192:195], v[16:19], v[32:35]
	v_mfma_i32_16x16x64_i8 v[180:183], v[64:67], v[104:107], v[16:19]
	v_mfma_i32_16x16x64_i8 v[16:19], v[246:249], v[112:115], v[36:39]
	v_mfma_i32_16x16x64_i8 v[172:175], v[250:253], v[120:123], v[16:19]
	v_mfma_i32_16x16x64_i8 v[16:19], v[192:195], v[112:115], v[40:43]
	v_mfma_i32_16x16x64_i8 v[164:167], v[64:67], v[120:123], v[16:19]
	v_mfma_i32_16x16x64_i8 v[16:19], v[246:249], v[124:127], v[44:47]
	v_mfma_i32_16x16x64_i8 v[156:159], v[250:253], v[140:143], v[16:19]
	v_mfma_i32_16x16x64_i8 v[16:19], v[192:195], v[124:127], v[48:51]
	v_mfma_i32_16x16x64_i8 v[148:151], v[64:67], v[140:143], v[16:19]
	v_mfma_i32_16x16x64_i8 v[16:19], v[246:249], v[68:71], v[52:55]
	v_mfma_i32_16x16x64_i8 v[140:143], v[250:253], v[72:75], v[16:19]
	v_mfma_i32_16x16x64_i8 v[16:19], v[192:195], v[68:71], v[56:59]
	v_mfma_i32_16x16x64_i8 v[188:191], v[250:253], v[104:107], v[76:79]
	v_mfma_i32_16x16x64_i8 v[132:135], v[64:67], v[72:75], v[16:19]
	s_barrier
	ds_read_b128 v[32:35], v206 offset:49152
	ds_read_b128 v[36:39], v206 offset:50176
	ds_read_b128 v[40:43], v206 offset:51200
	ds_read_b128 v[44:47], v206 offset:52224
	ds_read_b128 v[52:55], v206 offset:53248
	ds_read_b128 v[56:59], v206 offset:54272
	ds_read_b128 v[68:71], v206 offset:55296
	ds_read_b128 v[72:75], v206 offset:56320
	s_add_i32 m0, s46, 0x18000
	s_nop 0
	global_load_lds_dwordx4 v200, s[36:37]
	s_nop 0
	s_add_i32 m0, s46, 0x1a000
	s_nop 0
	global_load_lds_dwordx4 v202, s[36:37]
	s_add_u32 s28, s24, 0x40180
	s_addc_u32 s29, s25, 0
	s_add_i32 m0, s46, 0x1c000
	s_nop 0
	global_load_lds_dwordx4 v200, s[28:29]
	s_nop 0
	s_add_i32 m0, s46, 0x1e000
	s_nop 0
	global_load_lds_dwordx4 v202, s[28:29]
	s_nop 0
	s_add_i32 m0, s46, 0x8000
	s_nop 0
	global_load_lds_dwordx4 v199, s[34:35]
	s_nop 0
	s_add_i32 m0, s46, 0xa000
	s_nop 0
	global_load_lds_dwordx4 v201, s[34:35]
	s_waitcnt vmcnt(8)
	s_waitcnt lgkmcnt(0)
	s_barrier
	v_mfma_i32_16x16x64_i8 v[16:19], v[0:3], v[32:35], v[210:213]
	v_mfma_i32_16x16x64_i8 v[120:123], v[8:11], v[36:39], v[16:19]
	v_mfma_i32_16x16x64_i8 v[16:19], v[108:111], v[32:35], v[214:217]
	v_mfma_i32_16x16x64_i8 v[112:115], v[116:119], v[36:39], v[16:19]
	v_mfma_i32_16x16x64_i8 v[16:19], v[0:3], v[40:43], v[218:221]
	v_mfma_i32_16x16x64_i8 v[104:107], v[8:11], v[44:47], v[16:19]
	v_mfma_i32_16x16x64_i8 v[16:19], v[108:111], v[40:43], v[222:225]
	v_mfma_i32_16x16x64_i8 v[96:99], v[116:119], v[44:47], v[16:19]
	v_mfma_i32_16x16x64_i8 v[16:19], v[0:3], v[52:55], v[226:229]
	v_mfma_i32_16x16x64_i8 v[0:3], v[0:3], v[68:71], v[24:27]
	v_mfma_i32_16x16x64_i8 v[48:51], v[8:11], v[56:59], v[16:19]
	v_mfma_i32_16x16x64_i8 v[16:19], v[108:111], v[52:55], v[230:233]
	v_mfma_i32_16x16x64_i8 v[8:11], v[8:11], v[72:75], v[0:3]
	v_mfma_i32_16x16x64_i8 v[0:3], v[108:111], v[68:71], v[20:23]
	v_mfma_i32_16x16x64_i8 v[16:19], v[116:119], v[56:59], v[16:19]
	v_mfma_i32_16x16x64_i8 v[0:3], v[116:119], v[72:75], v[0:3]
	v_mfma_i32_16x16x64_i8 v[20:23], v[246:249], v[32:35], v[28:31]
	v_mfma_i32_16x16x64_i8 v[124:127], v[250:253], v[36:39], v[20:23]
	v_mfma_i32_16x16x64_i8 v[20:23], v[192:195], v[32:35], v[60:63]
	v_mfma_i32_16x16x64_i8 v[116:119], v[64:67], v[36:39], v[20:23]
	v_mfma_i32_16x16x64_i8 v[20:23], v[246:249], v[40:43], v[100:103]
	v_mfma_i32_16x16x64_i8 v[108:111], v[250:253], v[44:47], v[20:23]
	v_mfma_i32_16x16x64_i8 v[20:23], v[192:195], v[40:43], v[234:237]
	v_mfma_i32_16x16x64_i8 v[100:103], v[64:67], v[44:47], v[20:23]
	v_mfma_i32_16x16x64_i8 v[20:23], v[246:249], v[52:55], v[238:241]
	v_mfma_i32_16x16x64_i8 v[60:63], v[250:253], v[56:59], v[20:23]
	v_mfma_i32_16x16x64_i8 v[20:23], v[192:195], v[52:55], v[242:245]
	v_mfma_i32_16x16x64_i8 v[12:15], v[246:249], v[68:71], v[12:15]
	v_mfma_i32_16x16x64_i8 v[4:7], v[192:195], v[68:71], v[4:7]
	v_mfma_i32_16x16x64_i8 v[44:47], v[64:67], v[56:59], v[20:23]
	v_mfma_i32_16x16x64_i8 v[12:15], v[250:253], v[72:75], v[12:15]
	v_mfma_i32_16x16x64_i8 v[4:7], v[64:67], v[72:75], v[4:7]
	s_barrier
	s_add_u32 s28, s44, s30
	s_addc_u32 s29, s45, s31
	s_add_u32 s61, s24, 0x200
	s_addc_u32 s62, s25, 0
	s_add_i32 s63, s38, 0
	s_add_i32 s63, s63, 0x20000

.LBB0_755:
	ds_read_b128 v[20:23], v205
	ds_read_b128 v[24:27], v205 offset:1024
	ds_read_b128 v[28:31], v205 offset:2048
	ds_read_b128 v[32:35], v205 offset:3072
	ds_read_b128 v[36:39], v204
	ds_read_b128 v[40:43], v204 offset:1024
	ds_read_b128 v[52:55], v204 offset:2048
	ds_read_b128 v[56:59], v204 offset:3072
	ds_read_b128 v[64:67], v206
	ds_read_b128 v[68:71], v206 offset:1024
	ds_read_b128 v[72:75], v206 offset:2048
	ds_read_b128 v[76:79], v206 offset:3072
	ds_read_b128 v[80:83], v206 offset:4096
	ds_read_b128 v[84:87], v206 offset:5120
	ds_read_b128 v[88:91], v206 offset:6144
	ds_read_b128 v[92:95], v206 offset:7168
	s_add_u32 s24, s26, 0x100
	s_addc_u32 s25, s27, 0
	s_and_b64 s[30:31], s[30:31], exec
	s_cselect_b32 s38, s59, s24
	s_cselect_b32 s39, s58, s25
	s_cselect_b32 s35, s15, s62
	s_cselect_b32 s34, s60, s61
	s_add_u32 s30, s38, 0x80
	s_addc_u32 s31, s39, 0
	s_add_u32 s36, s34, 0x80
	s_addc_u32 s37, s35, 0
	s_add_u32 s26, s26, 0x40080
	s_addc_u32 s27, s27, 0
	s_add_i32 m0, s46, 0xc000
	s_nop 0
	global_load_lds_dwordx4 v199, s[26:27]
	s_nop 0
	s_add_i32 m0, s46, 0xe000
	s_nop 0
	global_load_lds_dwordx4 v201, s[26:27]
	s_waitcnt vmcnt(8)
	s_waitcnt lgkmcnt(0)
	s_barrier
	v_mfma_i32_16x16x64_i8 v[184:187], v[20:23], v[64:67], v[184:187]
	v_mfma_i32_16x16x64_i8 v[176:179], v[28:31], v[64:67], v[176:179]
	v_mfma_i32_16x16x64_i8 v[160:163], v[28:31], v[72:75], v[160:163]
	v_mfma_i32_16x16x64_i8 v[168:171], v[20:23], v[72:75], v[168:171]
	v_mfma_i32_16x16x64_i8 v[152:155], v[20:23], v[80:83], v[152:155]
	v_mfma_i32_16x16x64_i8 v[144:147], v[28:31], v[80:83], v[144:147]
	v_mfma_i32_16x16x64_i8 v[128:131], v[28:31], v[88:91], v[128:131]
	v_mfma_i32_16x16x64_i8 v[136:139], v[20:23], v[88:91], v[136:139]
	v_mfma_i32_16x16x64_i8 v[184:187], v[24:27], v[68:71], v[184:187]
	v_mfma_i32_16x16x64_i8 v[176:179], v[32:35], v[68:71], v[176:179]
	v_mfma_i32_16x16x64_i8 v[160:163], v[32:35], v[76:79], v[160:163]
	v_mfma_i32_16x16x64_i8 v[168:171], v[24:27], v[76:79], v[168:171]
	v_mfma_i32_16x16x64_i8 v[152:155], v[24:27], v[84:87], v[152:155]
	v_mfma_i32_16x16x64_i8 v[144:147], v[32:35], v[84:87], v[144:147]
	v_mfma_i32_16x16x64_i8 v[128:131], v[32:35], v[92:95], v[128:131]
	v_mfma_i32_16x16x64_i8 v[136:139], v[24:27], v[92:95], v[136:139]
	v_mfma_i32_16x16x64_i8 v[188:191], v[36:39], v[64:67], v[188:191]
	v_mfma_i32_16x16x64_i8 v[64:67], v[52:55], v[64:67], v[180:183]
	v_mfma_i32_16x16x64_i8 v[188:191], v[40:43], v[68:71], v[188:191]
	v_mfma_i32_16x16x64_i8 v[64:67], v[56:59], v[68:71], v[64:67]
	v_mfma_i32_16x16x64_i8 v[68:71], v[36:39], v[72:75], v[172:175]
	v_mfma_i32_16x16x64_i8 v[72:75], v[52:55], v[72:75], v[164:167]
	v_mfma_i32_16x16x64_i8 v[68:71], v[40:43], v[76:79], v[68:71]
	v_mfma_i32_16x16x64_i8 v[72:75], v[56:59], v[76:79], v[72:75]
	v_mfma_i32_16x16x64_i8 v[76:79], v[36:39], v[80:83], v[156:159]
	v_mfma_i32_16x16x64_i8 v[80:83], v[52:55], v[80:83], v[148:151]
	v_mfma_i32_16x16x64_i8 v[76:79], v[40:43], v[84:87], v[76:79]
	v_mfma_i32_16x16x64_i8 v[80:83], v[56:59], v[84:87], v[80:83]
	v_mfma_i32_16x16x64_i8 v[84:87], v[36:39], v[88:91], v[140:143]
	v_mfma_i32_16x16x64_i8 v[88:91], v[52:55], v[88:91], v[132:135]
	v_mfma_i32_16x16x64_i8 v[84:87], v[40:43], v[92:95], v[84:87]
	v_mfma_i32_16x16x64_i8 v[88:91], v[56:59], v[92:95], v[88:91]
	s_barrier
	ds_read_b128 v[92:95], v206 offset:16384
	ds_read_b128 v[132:135], v206 offset:17408
	ds_read_b128 v[140:143], v206 offset:18432
	ds_read_b128 v[148:151], v206 offset:19456
	ds_read_b128 v[156:159], v206 offset:20480
	ds_read_b128 v[164:167], v206 offset:21504
	ds_read_b128 v[172:175], v206 offset:22528
	ds_read_b128 v[180:183], v206 offset:23552
	s_add_i32 m0, s46, 0x10000
	s_nop 0
	global_load_lds_dwordx4 v200, s[34:35]
	s_nop 0
	s_add_i32 m0, s46, 0x12000
	s_nop 0
	global_load_lds_dwordx4 v202, s[34:35]
	s_add_u32 s26, s34, 0x40000
	s_addc_u32 s27, s35, 0
	s_add_i32 m0, s46, 0x14000
	s_nop 0
	global_load_lds_dwordx4 v200, s[26:27]
	s_nop 0
	s_add_i32 m0, s46, 0x16000
	s_nop 0
	global_load_lds_dwordx4 v202, s[26:27]
	s_nop 0
	s_add_i32 m0, s46, 0
	s_nop 0
	global_load_lds_dwordx4 v199, s[38:39]
	s_nop 0
	s_add_i32 m0, s46, 0x2000
	s_nop 0
	global_load_lds_dwordx4 v201, s[38:39]
	s_waitcnt vmcnt(8)
	s_waitcnt lgkmcnt(0)
	s_barrier
	v_mfma_i32_16x16x64_i8 v[120:123], v[20:23], v[92:95], v[120:123]
	v_mfma_i32_16x16x64_i8 v[112:115], v[28:31], v[92:95], v[112:115]
	v_mfma_i32_16x16x64_i8 v[96:99], v[28:31], v[140:143], v[96:99]
	v_mfma_i32_16x16x64_i8 v[104:107], v[20:23], v[140:143], v[104:107]
	v_mfma_i32_16x16x64_i8 v[48:51], v[20:23], v[156:159], v[48:51]
	v_mfma_i32_16x16x64_i8 v[16:19], v[28:31], v[156:159], v[16:19]
	v_mfma_i32_16x16x64_i8 v[0:3], v[28:31], v[172:175], v[0:3]
	v_mfma_i32_16x16x64_i8 v[8:11], v[20:23], v[172:175], v[8:11]
	v_mfma_i32_16x16x64_i8 v[120:123], v[24:27], v[132:135], v[120:123]
	v_mfma_i32_16x16x64_i8 v[112:115], v[32:35], v[132:135], v[112:115]
	v_mfma_i32_16x16x64_i8 v[96:99], v[32:35], v[148:151], v[96:99]
	v_mfma_i32_16x16x64_i8 v[104:107], v[24:27], v[148:151], v[104:107]
	v_mfma_i32_16x16x64_i8 v[48:51], v[24:27], v[164:167], v[48:51]
	v_mfma_i32_16x16x64_i8 v[16:19], v[32:35], v[164:167], v[16:19]
	v_mfma_i32_16x16x64_i8 v[0:3], v[32:35], v[180:183], v[0:3]
	v_mfma_i32_16x16x64_i8 v[8:11], v[24:27], v[180:183], v[8:11]
	v_mfma_i32_16x16x64_i8 v[20:23], v[36:39], v[92:95], v[124:127]
	v_mfma_i32_16x16x64_i8 v[124:127], v[40:43], v[132:135], v[20:23]
	v_mfma_i32_16x16x64_i8 v[20:23], v[52:55], v[92:95], v[116:119]
	v_mfma_i32_16x16x64_i8 v[116:119], v[56:59], v[132:135], v[20:23]
	v_mfma_i32_16x16x64_i8 v[20:23], v[36:39], v[140:143], v[108:111]
	v_mfma_i32_16x16x64_i8 v[108:111], v[40:43], v[148:151], v[20:23]
	v_mfma_i32_16x16x64_i8 v[20:23], v[52:55], v[140:143], v[100:103]
	v_mfma_i32_16x16x64_i8 v[100:103], v[56:59], v[148:151], v[20:23]
	v_mfma_i32_16x16x64_i8 v[20:23], v[36:39], v[156:159], v[60:63]
	v_mfma_i32_16x16x64_i8 v[60:63], v[40:43], v[164:167], v[20:23]
	v_mfma_i32_16x16x64_i8 v[20:23], v[52:55], v[156:159], v[44:47]
	v_mfma_i32_16x16x64_i8 v[12:15], v[36:39], v[172:175], v[12:15]
	v_mfma_i32_16x16x64_i8 v[4:7], v[52:55], v[172:175], v[4:7]
	v_mfma_i32_16x16x64_i8 v[44:47], v[56:59], v[164:167], v[20:23]
	v_mfma_i32_16x16x64_i8 v[12:15], v[40:43], v[180:183], v[12:15]
	v_mfma_i32_16x16x64_i8 v[4:7], v[56:59], v[180:183], v[4:7]
	s_barrier
	ds_read_b128 v[36:39], v207
	ds_read_b128 v[28:31], v207 offset:1024
	ds_read_b128 v[24:27], v207 offset:2048
	ds_read_b128 v[20:23], v207 offset:3072
	ds_read_b128 v[56:59], v208
	ds_read_b128 v[52:55], v208 offset:1024
	ds_read_b128 v[40:43], v208 offset:2048
	ds_read_b128 v[32:35], v208 offset:3072
	ds_read_b128 v[92:95], v206 offset:32768
	ds_read_b128 v[132:135], v206 offset:33792
	ds_read_b128 v[140:143], v206 offset:34816
	ds_read_b128 v[148:151], v206 offset:35840
	ds_read_b128 v[192:195], v206 offset:36864
	ds_read_b128 v[210:213], v206 offset:37888
	ds_read_b128 v[214:217], v206 offset:38912
	ds_read_b128 v[218:221], v206 offset:39936
	s_add_u32 s26, s38, 0x40000
	s_addc_u32 s27, s39, 0
	s_add_i32 m0, s46, 0x4000
	s_nop 0
	global_load_lds_dwordx4 v199, s[26:27]
	s_nop 0
	s_add_i32 m0, s46, 0x6000
	s_nop 0
	global_load_lds_dwordx4 v201, s[26:27]
	s_waitcnt vmcnt(8)
	s_waitcnt lgkmcnt(0)
	s_barrier
	v_mfma_i32_16x16x64_i8 v[156:159], v[36:39], v[92:95], v[184:187]
	v_mfma_i32_16x16x64_i8 v[184:187], v[28:31], v[132:135], v[156:159]
	v_mfma_i32_16x16x64_i8 v[156:159], v[24:27], v[92:95], v[176:179]
	v_mfma_i32_16x16x64_i8 v[176:179], v[20:23], v[132:135], v[156:159]
	v_mfma_i32_16x16x64_i8 v[156:159], v[36:39], v[140:143], v[168:171]
	v_mfma_i32_16x16x64_i8 v[168:171], v[28:31], v[148:151], v[156:159]
	v_mfma_i32_16x16x64_i8 v[156:159], v[24:27], v[140:143], v[160:163]
	v_mfma_i32_16x16x64_i8 v[152:155], v[36:39], v[192:195], v[152:155]
	v_mfma_i32_16x16x64_i8 v[144:147], v[24:27], v[192:195], v[144:147]
	v_mfma_i32_16x16x64_i8 v[136:139], v[36:39], v[214:217], v[136:139]
	v_mfma_i32_16x16x64_i8 v[128:131], v[24:27], v[214:217], v[128:131]
	v_mfma_i32_16x16x64_i8 v[160:163], v[20:23], v[148:151], v[156:159]
	v_mfma_i32_16x16x64_i8 v[152:155], v[28:31], v[210:213], v[152:155]
	v_mfma_i32_16x16x64_i8 v[144:147], v[20:23], v[210:213], v[144:147]
	v_mfma_i32_16x16x64_i8 v[136:139], v[28:31], v[218:221], v[136:139]
	v_mfma_i32_16x16x64_i8 v[128:131], v[20:23], v[218:221], v[128:131]
	v_mfma_i32_16x16x64_i8 v[64:67], v[40:43], v[92:95], v[64:67]
	v_mfma_i32_16x16x64_i8 v[180:183], v[32:35], v[132:135], v[64:67]
	v_mfma_i32_16x16x64_i8 v[64:67], v[56:59], v[140:143], v[68:71]
	v_mfma_i32_16x16x64_i8 v[172:175], v[52:55], v[148:151], v[64:67]
	v_mfma_i32_16x16x64_i8 v[64:67], v[40:43], v[140:143], v[72:75]
	v_mfma_i32_16x16x64_i8 v[156:159], v[56:59], v[92:95], v[188:191]
	v_mfma_i32_16x16x64_i8 v[164:167], v[32:35], v[148:151], v[64:67]
	v_mfma_i32_16x16x64_i8 v[64:67], v[56:59], v[192:195], v[76:79]
	v_mfma_i32_16x16x64_i8 v[188:191], v[52:55], v[132:135], v[156:159]
	v_mfma_i32_16x16x64_i8 v[156:159], v[52:55], v[210:213], v[64:67]
	v_mfma_i32_16x16x64_i8 v[64:67], v[40:43], v[192:195], v[80:83]
	v_mfma_i32_16x16x64_i8 v[148:151], v[32:35], v[210:213], v[64:67]
	v_mfma_i32_16x16x64_i8 v[64:67], v[56:59], v[214:217], v[84:87]
	v_mfma_i32_16x16x64_i8 v[140:143], v[52:55], v[218:221], v[64:67]
	v_mfma_i32_16x16x64_i8 v[64:67], v[40:43], v[214:217], v[88:91]
	v_mfma_i32_16x16x64_i8 v[132:135], v[32:35], v[218:221], v[64:67]
	s_barrier
	ds_read_b128 v[92:95], v206 offset:49152
	ds_read_b128 v[88:91], v206 offset:50176
	ds_read_b128 v[84:87], v206 offset:51200
	ds_read_b128 v[80:83], v206 offset:52224
	ds_read_b128 v[76:79], v206 offset:53248
	ds_read_b128 v[72:75], v206 offset:54272
	ds_read_b128 v[68:71], v206 offset:55296
	ds_read_b128 v[64:67], v206 offset:56320
	s_add_i32 m0, s46, 0x18000
	s_nop 0
	global_load_lds_dwordx4 v200, s[36:37]
	s_nop 0
	s_add_i32 m0, s46, 0x1a000
	s_nop 0
	global_load_lds_dwordx4 v202, s[36:37]
	s_add_u32 s26, s34, 0x40080
	s_addc_u32 s27, s35, 0
	s_add_i32 m0, s46, 0x1c000
	s_nop 0
	global_load_lds_dwordx4 v200, s[26:27]
	s_nop 0
	s_add_i32 m0, s46, 0x1e000
	s_nop 0
	global_load_lds_dwordx4 v202, s[26:27]
	s_nop 0
	s_add_i32 m0, s46, 0x8000
	s_nop 0
	global_load_lds_dwordx4 v199, s[30:31]
	s_nop 0
	s_add_i32 m0, s46, 0xa000
	s_nop 0
	global_load_lds_dwordx4 v201, s[30:31]
	s_waitcnt vmcnt(8)
	s_waitcnt lgkmcnt(0)
	s_barrier
	v_mfma_i32_16x16x64_i8 v[120:123], v[36:39], v[92:95], v[120:123]
	v_mfma_i32_16x16x64_i8 v[112:115], v[24:27], v[92:95], v[112:115]
	v_mfma_i32_16x16x64_i8 v[96:99], v[24:27], v[84:87], v[96:99]
	v_mfma_i32_16x16x64_i8 v[104:107], v[36:39], v[84:87], v[104:107]
	v_mfma_i32_16x16x64_i8 v[48:51], v[36:39], v[76:79], v[48:51]
	v_mfma_i32_16x16x64_i8 v[16:19], v[24:27], v[76:79], v[16:19]
	v_mfma_i32_16x16x64_i8 v[0:3], v[24:27], v[68:71], v[0:3]
	v_mfma_i32_16x16x64_i8 v[8:11], v[36:39], v[68:71], v[8:11]
	v_mfma_i32_16x16x64_i8 v[120:123], v[28:31], v[88:91], v[120:123]
	v_mfma_i32_16x16x64_i8 v[112:115], v[20:23], v[88:91], v[112:115]
	v_mfma_i32_16x16x64_i8 v[96:99], v[20:23], v[80:83], v[96:99]
	v_mfma_i32_16x16x64_i8 v[104:107], v[28:31], v[80:83], v[104:107]
	v_mfma_i32_16x16x64_i8 v[48:51], v[28:31], v[72:75], v[48:51]
	v_mfma_i32_16x16x64_i8 v[16:19], v[20:23], v[72:75], v[16:19]
	v_mfma_i32_16x16x64_i8 v[0:3], v[20:23], v[64:67], v[0:3]
	v_mfma_i32_16x16x64_i8 v[8:11], v[28:31], v[64:67], v[8:11]
	v_mfma_i32_16x16x64_i8 v[124:127], v[56:59], v[92:95], v[124:127]
	v_mfma_i32_16x16x64_i8 v[116:119], v[40:43], v[92:95], v[116:119]
	v_mfma_i32_16x16x64_i8 v[100:103], v[40:43], v[84:87], v[100:103]
	v_mfma_i32_16x16x64_i8 v[108:111], v[56:59], v[84:87], v[108:111]
	v_mfma_i32_16x16x64_i8 v[60:63], v[56:59], v[76:79], v[60:63]
	v_mfma_i32_16x16x64_i8 v[44:47], v[40:43], v[76:79], v[44:47]
	v_mfma_i32_16x16x64_i8 v[4:7], v[40:43], v[68:71], v[4:7]
	v_mfma_i32_16x16x64_i8 v[12:15], v[56:59], v[68:71], v[12:15]
	v_mfma_i32_16x16x64_i8 v[124:127], v[52:55], v[88:91], v[124:127]
	v_mfma_i32_16x16x64_i8 v[116:119], v[32:35], v[88:91], v[116:119]
	v_mfma_i32_16x16x64_i8 v[100:103], v[32:35], v[80:83], v[100:103]
	v_mfma_i32_16x16x64_i8 v[108:111], v[52:55], v[80:83], v[108:111]
	v_mfma_i32_16x16x64_i8 v[60:63], v[52:55], v[72:75], v[60:63]
	v_mfma_i32_16x16x64_i8 v[44:47], v[32:35], v[72:75], v[44:47]
	v_mfma_i32_16x16x64_i8 v[4:7], v[32:35], v[64:67], v[4:7]
	v_mfma_i32_16x16x64_i8 v[12:15], v[52:55], v[64:67], v[12:15]
	s_barrier
	s_add_i32 s17, s17, 2
	s_add_u32 s61, s61, 0x100
	s_addc_u32 s62, s62, 0
	s_cmp_gt_u32 s17, 13
	s_cbranch_scc1 .LBB0_757
	s_mov_b64 s[26:27], s[24:25]
	s_branch .LBB0_753

.LBB0_837:
	s_waitcnt lgkmcnt(0)
	ds_read_b128 v[0:3], v181
	ds_read_b128 v[4:7], v181 offset:1024
	ds_read_b128 v[8:11], v181 offset:2048
	ds_read_b128 v[12:15], v181 offset:3072
	ds_read_b128 v[16:19], v182
	ds_read_b128 v[20:23], v182 offset:1024
	ds_read_b128 v[24:27], v182 offset:2048
	ds_read_b128 v[28:31], v182 offset:3072
	ds_read_b128 v[32:35], v183
	ds_read_b128 v[36:39], v183 offset:1024
	ds_read_b128 v[40:43], v183 offset:2048
	ds_read_b128 v[44:47], v183 offset:3072
	ds_read_b128 v[48:51], v183 offset:4096
	ds_read_b128 v[52:55], v183 offset:5120
	ds_read_b128 v[56:59], v183 offset:6144
	ds_read_b128 v[60:63], v183 offset:7168
	s_add_u32 s28, s22, 0x100
	s_addc_u32 s29, s23, 0
	s_add_u32 s52, s24, 0x100
	s_addc_u32 s53, s25, 0
	s_add_u32 s6, s22, 0x180
	s_addc_u32 s7, s23, 0
	s_add_u32 s26, s24, 0x180
	s_addc_u32 s27, s25, 0
	s_add_u32 s54, s22, 0x160080
	s_addc_u32 s55, s23, 0
	s_add_i32 m0, s36, 0xc000
	s_nop 0
	global_load_lds_dwordx4 v175, s[54:55]
	s_nop 0
	s_add_i32 m0, s36, 0xe000
	s_nop 0
	global_load_lds_dwordx4 v177, s[54:55]
	s_waitcnt vmcnt(8)
	s_waitcnt lgkmcnt(0)
	s_barrier
	v_mfma_f32_16x16x32_bf16 v[88:91], v[0:3], v[56:59], 0
	v_mfma_f32_16x16x32_bf16 v[64:67], v[0:3], v[32:35], 0
	v_mfma_f32_16x16x32_bf16 v[68:71], v[8:11], v[32:35], 0
	v_mfma_f32_16x16x32_bf16 v[72:75], v[0:3], v[40:43], 0
	v_mfma_f32_16x16x32_bf16 v[76:79], v[8:11], v[40:43], 0
	v_mfma_f32_16x16x32_bf16 v[80:83], v[0:3], v[48:51], 0
	v_mfma_f32_16x16x32_bf16 v[84:87], v[8:11], v[48:51], 0
	v_mfma_f32_16x16x32_bf16 v[96:99], v[4:7], v[60:63], v[88:91]
	v_mfma_f32_16x16x32_bf16 v[88:91], v[8:11], v[56:59], 0
	v_mfma_f32_16x16x32_bf16 v[64:67], v[4:7], v[36:39], v[64:67]
	v_mfma_f32_16x16x32_bf16 v[68:71], v[12:15], v[36:39], v[68:71]
	v_mfma_f32_16x16x32_bf16 v[72:75], v[4:7], v[44:47], v[72:75]
	v_mfma_f32_16x16x32_bf16 v[76:79], v[12:15], v[44:47], v[76:79]
	v_mfma_f32_16x16x32_bf16 v[80:83], v[4:7], v[52:55], v[80:83]
	v_mfma_f32_16x16x32_bf16 v[84:87], v[12:15], v[52:55], v[84:87]
	v_mfma_f32_16x16x32_bf16 v[100:103], v[12:15], v[60:63], v[88:91]
	v_mfma_f32_16x16x32_bf16 v[88:91], v[16:19], v[32:35], 0
	v_mfma_f32_16x16x32_bf16 v[32:35], v[24:27], v[32:35], 0
	v_mfma_f32_16x16x32_bf16 v[112:115], v[20:23], v[36:39], v[88:91]
	v_mfma_f32_16x16x32_bf16 v[32:35], v[28:31], v[36:39], v[32:35]
	v_mfma_f32_16x16x32_bf16 v[36:39], v[16:19], v[40:43], 0
	v_mfma_f32_16x16x32_bf16 v[40:43], v[24:27], v[40:43], 0
	v_mfma_f32_16x16x32_bf16 v[36:39], v[20:23], v[44:47], v[36:39]
	v_mfma_f32_16x16x32_bf16 v[40:43], v[28:31], v[44:47], v[40:43]
	v_mfma_f32_16x16x32_bf16 v[44:47], v[16:19], v[48:51], 0
	v_mfma_f32_16x16x32_bf16 v[48:51], v[24:27], v[48:51], 0
	v_mfma_f32_16x16x32_bf16 v[44:47], v[20:23], v[52:55], v[44:47]
	v_mfma_f32_16x16x32_bf16 v[48:51], v[28:31], v[52:55], v[48:51]
	v_mfma_f32_16x16x32_bf16 v[52:55], v[16:19], v[56:59], 0
	v_mfma_f32_16x16x32_bf16 v[56:59], v[24:27], v[56:59], 0
	v_mfma_f32_16x16x32_bf16 v[52:55], v[20:23], v[60:63], v[52:55]
	v_mfma_f32_16x16x32_bf16 v[56:59], v[28:31], v[60:63], v[56:59]
	s_barrier
	ds_read_b128 v[60:63], v183 offset:16384
	ds_read_b128 v[88:91], v183 offset:17408
	ds_read_b128 v[92:95], v183 offset:18432
	ds_read_b128 v[104:107], v183 offset:19456
	ds_read_b128 v[108:111], v183 offset:20480
	ds_read_b128 v[116:119], v183 offset:21504
	ds_read_b128 v[120:123], v183 offset:22528
	ds_read_b128 v[124:127], v183 offset:23552
	s_add_i32 m0, s36, 0x10000
	s_nop 0
	global_load_lds_dwordx4 v176, s[52:53]
	s_nop 0
	s_add_i32 m0, s36, 0x12000
	s_nop 0
	global_load_lds_dwordx4 v178, s[52:53]
	s_add_u32 s52, s24, 0x160100
	s_addc_u32 s53, s25, 0
	s_add_i32 m0, s36, 0x14000
	s_nop 0
	global_load_lds_dwordx4 v176, s[52:53]
	s_nop 0
	s_add_i32 m0, s36, 0x16000
	s_nop 0
	global_load_lds_dwordx4 v178, s[52:53]
	s_nop 0
	s_add_i32 m0, s36, 0
	s_nop 0
	global_load_lds_dwordx4 v175, s[28:29]
	s_nop 0
	s_add_i32 m0, s36, 0x2000
	s_nop 0
	global_load_lds_dwordx4 v177, s[28:29]
	s_waitcnt vmcnt(8)
	s_waitcnt lgkmcnt(0)
	s_barrier
	v_mfma_f32_16x16x32_bf16 v[128:131], v[0:3], v[60:63], 0
	v_mfma_f32_16x16x32_bf16 v[136:139], v[4:7], v[88:91], v[128:131]
	v_mfma_f32_16x16x32_bf16 v[128:131], v[8:11], v[60:63], 0
	v_mfma_f32_16x16x32_bf16 v[140:143], v[12:15], v[88:91], v[128:131]
	v_mfma_f32_16x16x32_bf16 v[128:131], v[0:3], v[92:95], 0
	v_mfma_f32_16x16x32_bf16 v[144:147], v[4:7], v[104:107], v[128:131]
	v_mfma_f32_16x16x32_bf16 v[128:131], v[8:11], v[92:95], 0
	v_mfma_f32_16x16x32_bf16 v[148:151], v[12:15], v[104:107], v[128:131]
	v_mfma_f32_16x16x32_bf16 v[128:131], v[0:3], v[108:111], 0
	v_mfma_f32_16x16x32_bf16 v[0:3], v[0:3], v[120:123], 0
	v_mfma_f32_16x16x32_bf16 v[156:159], v[4:7], v[116:119], v[128:131]
	v_mfma_f32_16x16x32_bf16 v[0:3], v[4:7], v[124:127], v[0:3]
	v_mfma_f32_16x16x32_bf16 v[4:7], v[8:11], v[120:123], 0
	v_mfma_f32_16x16x32_bf16 v[128:131], v[8:11], v[108:111], 0
	v_mfma_f32_16x16x32_bf16 v[4:7], v[12:15], v[124:127], v[4:7]
	v_mfma_f32_16x16x32_bf16 v[160:163], v[12:15], v[116:119], v[128:131]
	v_mfma_f32_16x16x32_bf16 v[8:11], v[16:19], v[60:63], 0
	v_mfma_f32_16x16x32_bf16 v[164:167], v[20:23], v[88:91], v[8:11]
	v_mfma_f32_16x16x32_bf16 v[8:11], v[24:27], v[60:63], 0
	v_mfma_f32_16x16x32_bf16 v[168:171], v[28:31], v[88:91], v[8:11]
	v_mfma_f32_16x16x32_bf16 v[8:11], v[16:19], v[92:95], 0
	v_mfma_f32_16x16x32_bf16 v[188:191], v[20:23], v[104:107], v[8:11]
	v_mfma_f32_16x16x32_bf16 v[8:11], v[24:27], v[92:95], 0
	v_mfma_f32_16x16x32_bf16 v[192:195], v[28:31], v[104:107], v[8:11]
	v_mfma_f32_16x16x32_bf16 v[8:11], v[16:19], v[108:111], 0
	v_mfma_f32_16x16x32_bf16 v[196:199], v[20:23], v[116:119], v[8:11]
	v_mfma_f32_16x16x32_bf16 v[8:11], v[24:27], v[108:111], 0
	v_mfma_f32_16x16x32_bf16 v[116:119], v[28:31], v[116:119], v[8:11]
	v_mfma_f32_16x16x32_bf16 v[8:11], v[16:19], v[120:123], 0
	v_mfma_f32_16x16x32_bf16 v[200:203], v[20:23], v[124:127], v[8:11]
	v_mfma_f32_16x16x32_bf16 v[8:11], v[24:27], v[120:123], 0
	v_mfma_f32_16x16x32_bf16 v[204:207], v[28:31], v[124:127], v[8:11]
	s_barrier
	s_nop 4
	ds_read_b128 v[8:11], v184
	ds_read_b128 v[12:15], v184 offset:1024
	ds_read_b128 v[16:19], v184 offset:2048
	ds_read_b128 v[20:23], v184 offset:3072
	ds_read_b128 v[208:211], v185
	ds_read_b128 v[212:215], v185 offset:1024
	ds_read_b128 v[216:219], v185 offset:2048
	ds_read_b128 v[220:223], v185 offset:3072
	ds_read_b128 v[24:27], v183 offset:32768
	ds_read_b128 v[28:31], v183 offset:33792
	ds_read_b128 v[60:63], v183 offset:34816
	ds_read_b128 v[224:227], v183 offset:35840
	ds_read_b128 v[228:231], v183 offset:36864
	ds_read_b128 v[232:235], v183 offset:37888
	ds_read_b128 v[236:239], v183 offset:38912
	ds_read_b128 v[240:243], v183 offset:39936
	s_add_u32 s28, s22, 0x160100
	s_addc_u32 s29, s23, 0
	s_add_i32 m0, s36, 0x4000
	s_nop 0
	global_load_lds_dwordx4 v175, s[28:29]
	s_nop 0
	s_add_i32 m0, s36, 0x6000
	s_nop 0
	global_load_lds_dwordx4 v177, s[28:29]
	s_waitcnt vmcnt(8)
	s_waitcnt lgkmcnt(0)
	s_barrier
	v_mfma_f32_16x16x32_bf16 v[64:67], v[8:11], v[24:27], v[64:67]
	v_mfma_f32_16x16x32_bf16 v[132:135], v[12:15], v[28:31], v[64:67]
	v_mfma_f32_16x16x32_bf16 v[64:67], v[16:19], v[24:27], v[68:71]
	v_mfma_f32_16x16x32_bf16 v[128:131], v[20:23], v[28:31], v[64:67]
	v_mfma_f32_16x16x32_bf16 v[64:67], v[8:11], v[60:63], v[72:75]
	v_mfma_f32_16x16x32_bf16 v[108:111], v[12:15], v[224:227], v[64:67]
	v_mfma_f32_16x16x32_bf16 v[64:67], v[16:19], v[60:63], v[76:79]
	v_mfma_f32_16x16x32_bf16 v[104:107], v[20:23], v[224:227], v[64:67]
	v_mfma_f32_16x16x32_bf16 v[64:67], v[8:11], v[228:231], v[80:83]
	v_mfma_f32_16x16x32_bf16 v[92:95], v[12:15], v[232:235], v[64:67]
	v_mfma_f32_16x16x32_bf16 v[64:67], v[16:19], v[228:231], v[84:87]
	v_mfma_f32_16x16x32_bf16 v[88:91], v[20:23], v[232:235], v[64:67]
	v_mfma_f32_16x16x32_bf16 v[64:67], v[8:11], v[236:239], v[96:99]
	v_mfma_f32_16x16x32_bf16 v[76:79], v[12:15], v[240:243], v[64:67]
	v_mfma_f32_16x16x32_bf16 v[64:67], v[16:19], v[236:239], v[100:103]
	v_mfma_f32_16x16x32_bf16 v[72:75], v[20:23], v[240:243], v[64:67]
	v_mfma_f32_16x16x32_bf16 v[64:67], v[208:211], v[24:27], v[112:115]
	v_mfma_f32_16x16x32_bf16 v[24:27], v[216:219], v[24:27], v[32:35]
	v_mfma_f32_16x16x32_bf16 v[120:123], v[220:223], v[28:31], v[24:27]
	v_mfma_f32_16x16x32_bf16 v[24:27], v[208:211], v[60:63], v[36:39]
	v_mfma_f32_16x16x32_bf16 v[100:103], v[212:215], v[224:227], v[24:27]
	v_mfma_f32_16x16x32_bf16 v[24:27], v[216:219], v[60:63], v[40:43]
	v_mfma_f32_16x16x32_bf16 v[96:99], v[220:223], v[224:227], v[24:27]
	v_mfma_f32_16x16x32_bf16 v[24:27], v[208:211], v[228:231], v[44:47]
	v_mfma_f32_16x16x32_bf16 v[84:87], v[212:215], v[232:235], v[24:27]
	v_mfma_f32_16x16x32_bf16 v[24:27], v[216:219], v[228:231], v[48:51]
	v_mfma_f32_16x16x32_bf16 v[80:83], v[220:223], v[232:235], v[24:27]
	v_mfma_f32_16x16x32_bf16 v[24:27], v[208:211], v[236:239], v[52:55]
	v_mfma_f32_16x16x32_bf16 v[68:71], v[212:215], v[240:243], v[24:27]
	v_mfma_f32_16x16x32_bf16 v[24:27], v[216:219], v[236:239], v[56:59]
	v_mfma_f32_16x16x32_bf16 v[124:127], v[212:215], v[28:31], v[64:67]
	v_mfma_f32_16x16x32_bf16 v[64:67], v[220:223], v[240:243], v[24:27]
	s_barrier
	ds_read_b128 v[32:35], v183 offset:49152
	ds_read_b128 v[36:39], v183 offset:50176
	ds_read_b128 v[112:115], v183 offset:51200
	ds_read_b128 v[224:227], v183 offset:52224
	ds_read_b128 v[228:231], v183 offset:53248
	ds_read_b128 v[232:235], v183 offset:54272
	ds_read_b128 v[236:239], v183 offset:55296
	ds_read_b128 v[240:243], v183 offset:56320
	s_add_i32 m0, s36, 0x18000
	s_nop 0
	global_load_lds_dwordx4 v176, s[26:27]
	s_nop 0
	s_add_i32 m0, s36, 0x1a000
	s_nop 0
	global_load_lds_dwordx4 v178, s[26:27]
	s_add_u32 s26, s24, 0x160180
	s_addc_u32 s27, s25, 0
	s_add_i32 m0, s36, 0x1c000
	s_nop 0
	global_load_lds_dwordx4 v176, s[26:27]
	s_nop 0
	s_add_i32 m0, s36, 0x1e000
	s_nop 0
	global_load_lds_dwordx4 v178, s[26:27]
	s_nop 0
	s_add_i32 m0, s36, 0x8000
	s_nop 0
	global_load_lds_dwordx4 v175, s[6:7]
	s_nop 0
	s_add_i32 m0, s36, 0xa000
	s_nop 0
	global_load_lds_dwordx4 v177, s[6:7]
	s_waitcnt vmcnt(8)
	s_waitcnt lgkmcnt(0)
	s_barrier
	v_mfma_f32_16x16x32_bf16 v[24:27], v[8:11], v[32:35], v[136:139]
	v_mfma_f32_16x16x32_bf16 v[60:63], v[12:15], v[36:39], v[24:27]
	v_mfma_f32_16x16x32_bf16 v[24:27], v[16:19], v[32:35], v[140:143]
	v_mfma_f32_16x16x32_bf16 v[56:59], v[20:23], v[36:39], v[24:27]
	v_mfma_f32_16x16x32_bf16 v[24:27], v[8:11], v[112:115], v[144:147]
	v_mfma_f32_16x16x32_bf16 v[44:47], v[12:15], v[224:227], v[24:27]
	v_mfma_f32_16x16x32_bf16 v[24:27], v[16:19], v[112:115], v[148:151]
	v_mfma_f32_16x16x32_bf16 v[40:43], v[20:23], v[224:227], v[24:27]
	v_mfma_f32_16x16x32_bf16 v[24:27], v[8:11], v[228:231], v[156:159]
	v_mfma_f32_16x16x32_bf16 v[0:3], v[8:11], v[236:239], v[0:3]
	v_mfma_f32_16x16x32_bf16 v[28:31], v[12:15], v[232:235], v[24:27]
	v_mfma_f32_16x16x32_bf16 v[24:27], v[16:19], v[228:231], v[160:163]
	v_mfma_f32_16x16x32_bf16 v[12:15], v[12:15], v[240:243], v[0:3]
	v_mfma_f32_16x16x32_bf16 v[0:3], v[16:19], v[236:239], v[4:7]
	v_mfma_f32_16x16x32_bf16 v[24:27], v[20:23], v[232:235], v[24:27]
	v_mfma_f32_16x16x32_bf16 v[8:11], v[20:23], v[240:243], v[0:3]
	v_mfma_f32_16x16x32_bf16 v[0:3], v[208:211], v[32:35], v[164:167]
	v_mfma_f32_16x16x32_bf16 v[52:55], v[212:215], v[36:39], v[0:3]
	v_mfma_f32_16x16x32_bf16 v[0:3], v[216:219], v[32:35], v[168:171]
	v_mfma_f32_16x16x32_bf16 v[48:51], v[220:223], v[36:39], v[0:3]
	v_mfma_f32_16x16x32_bf16 v[0:3], v[208:211], v[112:115], v[188:191]
	v_mfma_f32_16x16x32_bf16 v[36:39], v[212:215], v[224:227], v[0:3]
	v_mfma_f32_16x16x32_bf16 v[0:3], v[216:219], v[112:115], v[192:195]
	v_mfma_f32_16x16x32_bf16 v[32:35], v[220:223], v[224:227], v[0:3]
	v_mfma_f32_16x16x32_bf16 v[0:3], v[208:211], v[228:231], v[196:199]
	v_mfma_f32_16x16x32_bf16 v[20:23], v[212:215], v[232:235], v[0:3]
	v_mfma_f32_16x16x32_bf16 v[0:3], v[216:219], v[228:231], v[116:119]
	v_mfma_f32_16x16x32_bf16 v[16:19], v[220:223], v[232:235], v[0:3]
	v_mfma_f32_16x16x32_bf16 v[0:3], v[208:211], v[236:239], v[200:203]
	v_mfma_f32_16x16x32_bf16 v[4:7], v[212:215], v[240:243], v[0:3]
	v_mfma_f32_16x16x32_bf16 v[0:3], v[216:219], v[236:239], v[204:207]
	v_mfma_f32_16x16x32_bf16 v[0:3], v[220:223], v[240:243], v[0:3]
	s_barrier
	s_add_u32 s51, s22, 0x200
	s_addc_u32 s52, s23, 0
	s_add_u32 s53, s24, 0x200
	s_addc_u32 s54, s25, 0
	s_add_u32 s6, s22, 0x160180
	s_addc_u32 s7, s23, 0
	s_mov_b32 s55, 0
.LBB0_838:
	ds_read_b128 v[112:115], v181
	ds_read_b128 v[116:119], v181 offset:1024
	ds_read_b128 v[136:139], v181 offset:2048
	ds_read_b128 v[140:143], v181 offset:3072
	ds_read_b128 v[144:147], v182
	ds_read_b128 v[148:151], v182 offset:1024
	ds_read_b128 v[156:159], v182 offset:2048
	ds_read_b128 v[160:163], v182 offset:3072
	ds_read_b128 v[164:167], v183
	ds_read_b128 v[168:171], v183 offset:1024
	ds_read_b128 v[188:191], v183 offset:2048
	ds_read_b128 v[192:195], v183 offset:3072
	ds_read_b128 v[196:199], v183 offset:4096
	ds_read_b128 v[200:203], v183 offset:5120
	ds_read_b128 v[204:207], v183 offset:6144
	ds_read_b128 v[208:211], v183 offset:7168
	s_cmpk_eq_i32 s55, 0x54
	s_cselect_b32 s28, s18, s51
	s_cselect_b32 s29, s19, s52
	s_cselect_b32 s24, s20, s53
	s_cselect_b32 s25, s21, s54
	s_add_u32 s22, s28, 0x80
	s_addc_u32 s23, s29, 0
	s_add_u32 s26, s24, 0x80
	s_addc_u32 s27, s25, 0
	s_add_i32 m0, s36, 0xc000
	s_nop 0
	global_load_lds_dwordx4 v175, s[6:7]
	s_nop 0
	s_add_i32 m0, s36, 0xe000
	s_nop 0
	global_load_lds_dwordx4 v177, s[6:7]
	s_waitcnt vmcnt(8)
	s_waitcnt lgkmcnt(0)
	s_barrier
	v_mfma_f32_16x16x32_bf16 v[132:135], v[112:115], v[164:167], v[132:135]
	v_mfma_f32_16x16x32_bf16 v[128:131], v[136:139], v[164:167], v[128:131]
	v_mfma_f32_16x16x32_bf16 v[104:107], v[136:139], v[188:191], v[104:107]
	v_mfma_f32_16x16x32_bf16 v[108:111], v[112:115], v[188:191], v[108:111]
	v_mfma_f32_16x16x32_bf16 v[92:95], v[112:115], v[196:199], v[92:95]
	v_mfma_f32_16x16x32_bf16 v[88:91], v[136:139], v[196:199], v[88:91]
	v_mfma_f32_16x16x32_bf16 v[72:75], v[136:139], v[204:207], v[72:75]
	v_mfma_f32_16x16x32_bf16 v[76:79], v[112:115], v[204:207], v[76:79]
	v_mfma_f32_16x16x32_bf16 v[132:135], v[116:119], v[168:171], v[132:135]
	v_mfma_f32_16x16x32_bf16 v[128:131], v[140:143], v[168:171], v[128:131]
	v_mfma_f32_16x16x32_bf16 v[104:107], v[140:143], v[192:195], v[104:107]
	v_mfma_f32_16x16x32_bf16 v[108:111], v[116:119], v[192:195], v[108:111]
	v_mfma_f32_16x16x32_bf16 v[92:95], v[116:119], v[200:203], v[92:95]
	v_mfma_f32_16x16x32_bf16 v[88:91], v[140:143], v[200:203], v[88:91]
	v_mfma_f32_16x16x32_bf16 v[72:75], v[140:143], v[208:211], v[72:75]
	v_mfma_f32_16x16x32_bf16 v[76:79], v[116:119], v[208:211], v[76:79]
	v_mfma_f32_16x16x32_bf16 v[124:127], v[144:147], v[164:167], v[124:127]
	v_mfma_f32_16x16x32_bf16 v[120:123], v[156:159], v[164:167], v[120:123]
	v_mfma_f32_16x16x32_bf16 v[96:99], v[156:159], v[188:191], v[96:99]
	v_mfma_f32_16x16x32_bf16 v[100:103], v[144:147], v[188:191], v[100:103]
	v_mfma_f32_16x16x32_bf16 v[84:87], v[144:147], v[196:199], v[84:87]
	v_mfma_f32_16x16x32_bf16 v[80:83], v[156:159], v[196:199], v[80:83]
	v_mfma_f32_16x16x32_bf16 v[64:67], v[156:159], v[204:207], v[64:67]
	v_mfma_f32_16x16x32_bf16 v[68:71], v[144:147], v[204:207], v[68:71]
	v_mfma_f32_16x16x32_bf16 v[124:127], v[148:151], v[168:171], v[124:127]
	v_mfma_f32_16x16x32_bf16 v[120:123], v[160:163], v[168:171], v[120:123]
	v_mfma_f32_16x16x32_bf16 v[96:99], v[160:163], v[192:195], v[96:99]
	v_mfma_f32_16x16x32_bf16 v[100:103], v[148:151], v[192:195], v[100:103]
	v_mfma_f32_16x16x32_bf16 v[84:87], v[148:151], v[200:203], v[84:87]
	v_mfma_f32_16x16x32_bf16 v[80:83], v[160:163], v[200:203], v[80:83]
	v_mfma_f32_16x16x32_bf16 v[64:67], v[160:163], v[208:211], v[64:67]
	v_mfma_f32_16x16x32_bf16 v[68:71], v[148:151], v[208:211], v[68:71]
	s_barrier
	ds_read_b128 v[164:167], v183 offset:16384
	ds_read_b128 v[168:171], v183 offset:17408
	ds_read_b128 v[188:191], v183 offset:18432
	ds_read_b128 v[192:195], v183 offset:19456
	ds_read_b128 v[196:199], v183 offset:20480
	ds_read_b128 v[200:203], v183 offset:21504
	ds_read_b128 v[204:207], v183 offset:22528
	ds_read_b128 v[208:211], v183 offset:23552
	s_add_i32 m0, s36, 0x10000
	s_nop 0
	global_load_lds_dwordx4 v176, s[24:25]
	s_nop 0
	s_add_i32 m0, s36, 0x12000
	s_nop 0
	global_load_lds_dwordx4 v178, s[24:25]
	s_add_u32 s56, s24, 0x160000
	s_addc_u32 s57, s25, 0
	s_add_i32 m0, s36, 0x14000
	s_nop 0
	global_load_lds_dwordx4 v176, s[56:57]
	s_nop 0
	s_add_i32 m0, s36, 0x16000
	s_nop 0
	global_load_lds_dwordx4 v178, s[56:57]
	s_nop 0
	s_add_i32 m0, s36, 0
	s_nop 0
	global_load_lds_dwordx4 v175, s[28:29]
	s_nop 0
	s_add_i32 m0, s36, 0x2000
	s_nop 0
	global_load_lds_dwordx4 v177, s[28:29]
	s_waitcnt vmcnt(8)
	s_waitcnt lgkmcnt(0)
	s_barrier
	v_mfma_f32_16x16x32_bf16 v[60:63], v[112:115], v[164:167], v[60:63]
	v_mfma_f32_16x16x32_bf16 v[56:59], v[136:139], v[164:167], v[56:59]
	v_mfma_f32_16x16x32_bf16 v[40:43], v[136:139], v[188:191], v[40:43]
	v_mfma_f32_16x16x32_bf16 v[44:47], v[112:115], v[188:191], v[44:47]
	v_mfma_f32_16x16x32_bf16 v[28:31], v[112:115], v[196:199], v[28:31]
	v_mfma_f32_16x16x32_bf16 v[24:27], v[136:139], v[196:199], v[24:27]
	v_mfma_f32_16x16x32_bf16 v[8:11], v[136:139], v[204:207], v[8:11]
	v_mfma_f32_16x16x32_bf16 v[12:15], v[112:115], v[204:207], v[12:15]
	v_mfma_f32_16x16x32_bf16 v[60:63], v[116:119], v[168:171], v[60:63]
	v_mfma_f32_16x16x32_bf16 v[56:59], v[140:143], v[168:171], v[56:59]
	v_mfma_f32_16x16x32_bf16 v[40:43], v[140:143], v[192:195], v[40:43]
	v_mfma_f32_16x16x32_bf16 v[44:47], v[116:119], v[192:195], v[44:47]
	v_mfma_f32_16x16x32_bf16 v[28:31], v[116:119], v[200:203], v[28:31]
	v_mfma_f32_16x16x32_bf16 v[24:27], v[140:143], v[200:203], v[24:27]
	v_mfma_f32_16x16x32_bf16 v[8:11], v[140:143], v[208:211], v[8:11]
	v_mfma_f32_16x16x32_bf16 v[12:15], v[116:119], v[208:211], v[12:15]
	v_mfma_f32_16x16x32_bf16 v[52:55], v[144:147], v[164:167], v[52:55]
	v_mfma_f32_16x16x32_bf16 v[48:51], v[156:159], v[164:167], v[48:51]
	v_mfma_f32_16x16x32_bf16 v[32:35], v[156:159], v[188:191], v[32:35]
	v_mfma_f32_16x16x32_bf16 v[36:39], v[144:147], v[188:191], v[36:39]
	v_mfma_f32_16x16x32_bf16 v[20:23], v[144:147], v[196:199], v[20:23]
	v_mfma_f32_16x16x32_bf16 v[16:19], v[156:159], v[196:199], v[16:19]
	v_mfma_f32_16x16x32_bf16 v[0:3], v[156:159], v[204:207], v[0:3]
	v_mfma_f32_16x16x32_bf16 v[4:7], v[144:147], v[204:207], v[4:7]
	v_mfma_f32_16x16x32_bf16 v[52:55], v[148:151], v[168:171], v[52:55]
	v_mfma_f32_16x16x32_bf16 v[48:51], v[160:163], v[168:171], v[48:51]
	v_mfma_f32_16x16x32_bf16 v[32:35], v[160:163], v[192:195], v[32:35]
	v_mfma_f32_16x16x32_bf16 v[36:39], v[148:151], v[192:195], v[36:39]
	v_mfma_f32_16x16x32_bf16 v[20:23], v[148:151], v[200:203], v[20:23]
	v_mfma_f32_16x16x32_bf16 v[16:19], v[160:163], v[200:203], v[16:19]
	v_mfma_f32_16x16x32_bf16 v[0:3], v[160:163], v[208:211], v[0:3]
	v_mfma_f32_16x16x32_bf16 v[4:7], v[148:151], v[208:211], v[4:7]
	s_barrier
	ds_read_b128 v[112:115], v184
	ds_read_b128 v[116:119], v184 offset:1024
	ds_read_b128 v[136:139], v184 offset:2048
	ds_read_b128 v[140:143], v184 offset:3072
	ds_read_b128 v[144:147], v185
	ds_read_b128 v[148:151], v185 offset:1024
	ds_read_b128 v[156:159], v185 offset:2048
	ds_read_b128 v[160:163], v185 offset:3072
	ds_read_b128 v[164:167], v183 offset:32768
	ds_read_b128 v[168:171], v183 offset:33792
	ds_read_b128 v[188:191], v183 offset:34816
	ds_read_b128 v[192:195], v183 offset:35840
	ds_read_b128 v[196:199], v183 offset:36864
	ds_read_b128 v[200:203], v183 offset:37888
	ds_read_b128 v[204:207], v183 offset:38912
	ds_read_b128 v[208:211], v183 offset:39936
	s_add_u32 s28, s28, 0x160000
	s_addc_u32 s29, s29, 0
	s_add_i32 m0, s36, 0x4000
	s_nop 0
	global_load_lds_dwordx4 v175, s[28:29]
	s_nop 0
	s_add_i32 m0, s36, 0x6000
	s_nop 0
	global_load_lds_dwordx4 v177, s[28:29]
	s_waitcnt vmcnt(8)
	s_waitcnt lgkmcnt(0)
	s_barrier
	v_mfma_f32_16x16x32_bf16 v[132:135], v[112:115], v[164:167], v[132:135]
	v_mfma_f32_16x16x32_bf16 v[128:131], v[136:139], v[164:167], v[128:131]
	v_mfma_f32_16x16x32_bf16 v[104:107], v[136:139], v[188:191], v[104:107]
	v_mfma_f32_16x16x32_bf16 v[108:111], v[112:115], v[188:191], v[108:111]
	v_mfma_f32_16x16x32_bf16 v[92:95], v[112:115], v[196:199], v[92:95]
	v_mfma_f32_16x16x32_bf16 v[88:91], v[136:139], v[196:199], v[88:91]
	v_mfma_f32_16x16x32_bf16 v[72:75], v[136:139], v[204:207], v[72:75]
	v_mfma_f32_16x16x32_bf16 v[76:79], v[112:115], v[204:207], v[76:79]
	v_mfma_f32_16x16x32_bf16 v[132:135], v[116:119], v[168:171], v[132:135]
	v_mfma_f32_16x16x32_bf16 v[128:131], v[140:143], v[168:171], v[128:131]
	v_mfma_f32_16x16x32_bf16 v[104:107], v[140:143], v[192:195], v[104:107]
	v_mfma_f32_16x16x32_bf16 v[108:111], v[116:119], v[192:195], v[108:111]
	v_mfma_f32_16x16x32_bf16 v[92:95], v[116:119], v[200:203], v[92:95]
	v_mfma_f32_16x16x32_bf16 v[88:91], v[140:143], v[200:203], v[88:91]
	v_mfma_f32_16x16x32_bf16 v[72:75], v[140:143], v[208:211], v[72:75]
	v_mfma_f32_16x16x32_bf16 v[76:79], v[116:119], v[208:211], v[76:79]
	v_mfma_f32_16x16x32_bf16 v[124:127], v[144:147], v[164:167], v[124:127]
	v_mfma_f32_16x16x32_bf16 v[120:123], v[156:159], v[164:167], v[120:123]
	v_mfma_f32_16x16x32_bf16 v[96:99], v[156:159], v[188:191], v[96:99]
	v_mfma_f32_16x16x32_bf16 v[100:103], v[144:147], v[188:191], v[100:103]
	v_mfma_f32_16x16x32_bf16 v[84:87], v[144:147], v[196:199], v[84:87]
	v_mfma_f32_16x16x32_bf16 v[80:83], v[156:159], v[196:199], v[80:83]
	v_mfma_f32_16x16x32_bf16 v[64:67], v[156:159], v[204:207], v[64:67]
	v_mfma_f32_16x16x32_bf16 v[68:71], v[144:147], v[204:207], v[68:71]
	v_mfma_f32_16x16x32_bf16 v[124:127], v[148:151], v[168:171], v[124:127]
	v_mfma_f32_16x16x32_bf16 v[120:123], v[160:163], v[168:171], v[120:123]
	v_mfma_f32_16x16x32_bf16 v[96:99], v[160:163], v[192:195], v[96:99]
	v_mfma_f32_16x16x32_bf16 v[100:103], v[148:151], v[192:195], v[100:103]
	v_mfma_f32_16x16x32_bf16 v[84:87], v[148:151], v[200:203], v[84:87]
	v_mfma_f32_16x16x32_bf16 v[80:83], v[160:163], v[200:203], v[80:83]
	v_mfma_f32_16x16x32_bf16 v[64:67], v[160:163], v[208:211], v[64:67]
	v_mfma_f32_16x16x32_bf16 v[68:71], v[148:151], v[208:211], v[68:71]
	s_barrier
	ds_read_b128 v[164:167], v183 offset:49152
	ds_read_b128 v[168:171], v183 offset:50176
	ds_read_b128 v[188:191], v183 offset:51200
	ds_read_b128 v[192:195], v183 offset:52224
	ds_read_b128 v[196:199], v183 offset:53248
	ds_read_b128 v[200:203], v183 offset:54272
	ds_read_b128 v[204:207], v183 offset:55296
	ds_read_b128 v[208:211], v183 offset:56320
	s_add_i32 m0, s36, 0x18000
	s_nop 0
	global_load_lds_dwordx4 v176, s[26:27]
	s_nop 0
	s_add_i32 m0, s36, 0x1a000
	s_nop 0
	global_load_lds_dwordx4 v178, s[26:27]
	s_add_u32 s24, s24, 0x160080
	s_addc_u32 s25, s25, 0
	s_add_i32 m0, s36, 0x1c000
	s_nop 0
	global_load_lds_dwordx4 v176, s[24:25]
	s_nop 0
	s_add_i32 m0, s36, 0x1e000
	s_nop 0
	global_load_lds_dwordx4 v178, s[24:25]
	s_nop 0
	s_add_i32 m0, s36, 0x8000
	s_nop 0
	global_load_lds_dwordx4 v175, s[22:23]
	s_nop 0
	s_add_i32 m0, s36, 0xa000
	s_nop 0
	global_load_lds_dwordx4 v177, s[22:23]
	s_waitcnt vmcnt(8)
	s_waitcnt lgkmcnt(0)
	s_barrier
	v_mfma_f32_16x16x32_bf16 v[60:63], v[112:115], v[164:167], v[60:63]
	v_mfma_f32_16x16x32_bf16 v[56:59], v[136:139], v[164:167], v[56:59]
	v_mfma_f32_16x16x32_bf16 v[40:43], v[136:139], v[188:191], v[40:43]
	v_mfma_f32_16x16x32_bf16 v[44:47], v[112:115], v[188:191], v[44:47]
	v_mfma_f32_16x16x32_bf16 v[28:31], v[112:115], v[196:199], v[28:31]
	v_mfma_f32_16x16x32_bf16 v[24:27], v[136:139], v[196:199], v[24:27]
	v_mfma_f32_16x16x32_bf16 v[8:11], v[136:139], v[204:207], v[8:11]
	v_mfma_f32_16x16x32_bf16 v[12:15], v[112:115], v[204:207], v[12:15]
	v_mfma_f32_16x16x32_bf16 v[60:63], v[116:119], v[168:171], v[60:63]
	v_mfma_f32_16x16x32_bf16 v[56:59], v[140:143], v[168:171], v[56:59]
	v_mfma_f32_16x16x32_bf16 v[40:43], v[140:143], v[192:195], v[40:43]
	v_mfma_f32_16x16x32_bf16 v[44:47], v[116:119], v[192:195], v[44:47]
	v_mfma_f32_16x16x32_bf16 v[28:31], v[116:119], v[200:203], v[28:31]
	v_mfma_f32_16x16x32_bf16 v[24:27], v[140:143], v[200:203], v[24:27]
	v_mfma_f32_16x16x32_bf16 v[8:11], v[140:143], v[208:211], v[8:11]
	v_mfma_f32_16x16x32_bf16 v[12:15], v[116:119], v[208:211], v[12:15]
	v_mfma_f32_16x16x32_bf16 v[52:55], v[144:147], v[164:167], v[52:55]
	v_mfma_f32_16x16x32_bf16 v[48:51], v[156:159], v[164:167], v[48:51]
	v_mfma_f32_16x16x32_bf16 v[32:35], v[156:159], v[188:191], v[32:35]
	v_mfma_f32_16x16x32_bf16 v[36:39], v[144:147], v[188:191], v[36:39]
	v_mfma_f32_16x16x32_bf16 v[20:23], v[144:147], v[196:199], v[20:23]
	v_mfma_f32_16x16x32_bf16 v[16:19], v[156:159], v[196:199], v[16:19]
	v_mfma_f32_16x16x32_bf16 v[0:3], v[156:159], v[204:207], v[0:3]
	v_mfma_f32_16x16x32_bf16 v[4:7], v[144:147], v[204:207], v[4:7]
	v_mfma_f32_16x16x32_bf16 v[52:55], v[148:151], v[168:171], v[52:55]
	v_mfma_f32_16x16x32_bf16 v[48:51], v[160:163], v[168:171], v[48:51]
	v_mfma_f32_16x16x32_bf16 v[32:35], v[160:163], v[192:195], v[32:35]
	v_mfma_f32_16x16x32_bf16 v[36:39], v[148:151], v[192:195], v[36:39]
	v_mfma_f32_16x16x32_bf16 v[20:23], v[148:151], v[200:203], v[20:23]
	v_mfma_f32_16x16x32_bf16 v[16:19], v[160:163], v[200:203], v[16:19]
	v_mfma_f32_16x16x32_bf16 v[0:3], v[160:163], v[208:211], v[0:3]
	v_mfma_f32_16x16x32_bf16 v[4:7], v[148:151], v[208:211], v[4:7]
	s_barrier
	s_add_i32 s55, s55, 2
	s_add_u32 s51, s51, 0x100
	s_addc_u32 s52, s52, 0
	s_add_u32 s53, s53, 0x100
	s_addc_u32 s54, s54, 0
	s_add_u32 s6, s6, 0x100
	s_addc_u32 s7, s7, 0
	s_cmpk_gt_u32 s55, 0x55
	s_cbranch_scc0 .LBB0_838
	s_and_b64 vcc, exec, s[16:17]
	s_cbranch_vccz .LBB0_841
	s_barrier

.LBB0_930:
	s_ashr_i32 s37, s36, 31
	s_lshl_b64 s[38:39], s[36:37], 19
	s_add_u32 s38, s19, s38
	s_addc_u32 s39, s21, s39
	s_and_b64 s[40:41], s[4:5], exec
	s_cselect_b32 s9, s39, s45
	s_cselect_b32 s76, s38, s44
	s_ashr_i32 s35, s34, 31
	s_lshl_b64 s[40:41], s[34:35], 19
	s_add_u32 s40, s23, s40
	s_addc_u32 s41, s25, s41
	s_and_b64 s[46:47], s[4:5], exec
	ds_read_b128 v[0:3], v226 offset:3072
	ds_read_b128 v[4:7], v226 offset:2048
	ds_read_b128 v[8:11], v226 offset:1024
	ds_read_b128 v[12:15], v226
	ds_read_b128 v[16:19], v227 offset:3072
	ds_read_b128 v[20:23], v227 offset:2048
	ds_read_b128 v[24:27], v227 offset:1024
	ds_read_b128 v[28:31], v227
	ds_read_b128 v[32:35], v228
	ds_read_b128 v[36:39], v228 offset:1024
	ds_read_b128 v[40:43], v228 offset:2048
	ds_read_b128 v[44:47], v228 offset:3072
	ds_read_b128 v[48:51], v228 offset:4096
	ds_read_b128 v[52:55], v228 offset:5120
	ds_read_b128 v[56:59], v228 offset:6144
	ds_read_b128 v[60:63], v228 offset:7168
	s_cselect_b32 s35, s41, s43
	s_cselect_b32 s77, s40, s42
	s_lshl_b32 s46, s78, 11
	s_and_b32 s46, s46, 0x800
	s_or_b32 s54, s46, s56
	s_lshl_b64 s[48:49], s[36:37], 11
	s_add_u32 s46, s44, 0x100
	s_addc_u32 s47, s45, 0
	s_add_u32 s80, s42, 0x100
	s_addc_u32 s81, s43, 0
	s_add_u32 s50, s44, 0x180
	s_addc_u32 s51, s45, 0
	s_add_u32 s52, s42, 0x180
	s_addc_u32 s53, s43, 0
	s_add_u32 s82, s44, 0x40080
	s_addc_u32 s83, s45, 0
	s_add_i32 m0, s31, 0xc000
	s_nop 0
	global_load_lds_dwordx4 v219, s[82:83]
	s_nop 0
	s_add_i32 m0, s31, 0xe000
	s_nop 0
	global_load_lds_dwordx4 v221, s[82:83]
	s_waitcnt vmcnt(8)
	s_waitcnt lgkmcnt(0)
	s_barrier
	s_waitcnt lgkmcnt(7)
	v_mfma_i32_16x16x64_i8 v[64:67], v[28:31], v[32:35], 0
	s_mov_b32 s37, 0
	v_mfma_i32_16x16x64_i8 v[68:71], v[20:23], v[32:35], 0
	s_waitcnt lgkmcnt(5)
	v_mfma_i32_16x16x64_i8 v[72:75], v[28:31], v[40:43], 0
	v_mfma_i32_16x16x64_i8 v[76:79], v[20:23], v[40:43], 0
	s_waitcnt lgkmcnt(3)
	v_mfma_i32_16x16x64_i8 v[80:83], v[28:31], v[48:51], 0
	v_mfma_i32_16x16x64_i8 v[84:87], v[20:23], v[48:51], 0
	s_waitcnt lgkmcnt(1)
	v_mfma_i32_16x16x64_i8 v[92:95], v[20:23], v[56:59], 0
	v_mfma_i32_16x16x64_i8 v[136:139], v[24:27], v[36:39], v[64:67]
	v_mfma_i32_16x16x64_i8 v[148:151], v[24:27], v[44:47], v[72:75]
	v_mfma_i32_16x16x64_i8 v[144:147], v[16:19], v[36:39], v[68:71]
	v_mfma_i32_16x16x64_i8 v[76:79], v[16:19], v[44:47], v[76:79]
	v_mfma_i32_16x16x64_i8 v[80:83], v[24:27], v[52:55], v[80:83]
	v_mfma_i32_16x16x64_i8 v[88:91], v[28:31], v[56:59], 0
	v_mfma_i32_16x16x64_i8 v[84:87], v[16:19], v[52:55], v[84:87]
	s_waitcnt lgkmcnt(0)
	v_mfma_i32_16x16x64_i8 v[92:95], v[16:19], v[60:63], v[92:95]
	v_mfma_i32_16x16x64_i8 v[88:91], v[24:27], v[60:63], v[88:91]
	v_mfma_i32_16x16x64_i8 v[96:99], v[12:15], v[32:35], 0
	v_mfma_i32_16x16x64_i8 v[32:35], v[4:7], v[32:35], 0
	v_mfma_i32_16x16x64_i8 v[96:99], v[8:11], v[36:39], v[96:99]
	v_mfma_i32_16x16x64_i8 v[32:35], v[0:3], v[36:39], v[32:35]
	v_mfma_i32_16x16x64_i8 v[36:39], v[12:15], v[40:43], 0
	v_mfma_i32_16x16x64_i8 v[40:43], v[4:7], v[40:43], 0
	v_mfma_i32_16x16x64_i8 v[36:39], v[8:11], v[44:47], v[36:39]
	v_mfma_i32_16x16x64_i8 v[40:43], v[0:3], v[44:47], v[40:43]
	v_mfma_i32_16x16x64_i8 v[44:47], v[12:15], v[48:51], 0
	v_mfma_i32_16x16x64_i8 v[48:51], v[4:7], v[48:51], 0
	v_mfma_i32_16x16x64_i8 v[44:47], v[8:11], v[52:55], v[44:47]
	v_mfma_i32_16x16x64_i8 v[48:51], v[0:3], v[52:55], v[48:51]
	v_mfma_i32_16x16x64_i8 v[52:55], v[12:15], v[56:59], 0
	v_mfma_i32_16x16x64_i8 v[56:59], v[4:7], v[56:59], 0
	v_mfma_i32_16x16x64_i8 v[52:55], v[8:11], v[60:63], v[52:55]
	v_mfma_i32_16x16x64_i8 v[56:59], v[0:3], v[60:63], v[56:59]
	s_barrier
	ds_read_b128 v[60:63], v228 offset:16384
	ds_read_b128 v[100:103], v228 offset:17408
	ds_read_b128 v[104:107], v228 offset:18432
	ds_read_b128 v[108:111], v228 offset:19456
	ds_read_b128 v[112:115], v228 offset:20480
	ds_read_b128 v[116:119], v228 offset:21504
	ds_read_b128 v[120:123], v228 offset:22528
	ds_read_b128 v[124:127], v228 offset:23552
	s_add_i32 m0, s31, 0x10000
	s_nop 0
	global_load_lds_dwordx4 v220, s[80:81]
	s_nop 0
	s_add_i32 m0, s31, 0x12000
	s_nop 0
	global_load_lds_dwordx4 v222, s[80:81]
	s_add_u32 s80, s42, 0x40100
	s_addc_u32 s81, s43, 0
	s_add_i32 m0, s31, 0x14000
	s_nop 0
	global_load_lds_dwordx4 v220, s[80:81]
	s_nop 0
	s_add_i32 m0, s31, 0x16000
	s_nop 0
	global_load_lds_dwordx4 v222, s[80:81]
	s_nop 0
	s_add_i32 m0, s31, 0
	s_nop 0
	global_load_lds_dwordx4 v219, s[46:47]
	s_nop 0
	s_add_i32 m0, s31, 0x2000
	s_nop 0
	global_load_lds_dwordx4 v221, s[46:47]
	s_waitcnt vmcnt(8)
	s_waitcnt lgkmcnt(0)
	s_barrier
	v_mfma_i32_16x16x64_i8 v[132:135], v[20:23], v[60:63], 0
	v_mfma_i32_16x16x64_i8 v[168:171], v[16:19], v[100:103], v[132:135]
	v_mfma_i32_16x16x64_i8 v[132:135], v[28:31], v[104:107], 0
	v_mfma_i32_16x16x64_i8 v[204:207], v[24:27], v[108:111], v[132:135]
	v_mfma_i32_16x16x64_i8 v[132:135], v[20:23], v[104:107], 0
	v_mfma_i32_16x16x64_i8 v[128:131], v[28:31], v[60:63], 0
	v_mfma_i32_16x16x64_i8 v[214:217], v[16:19], v[108:111], v[132:135]
	v_mfma_i32_16x16x64_i8 v[132:135], v[28:31], v[112:115], 0
	v_mfma_i32_16x16x64_i8 v[128:131], v[24:27], v[100:103], v[128:131]
	v_mfma_i32_16x16x64_i8 v[232:235], v[24:27], v[116:119], v[132:135]
	v_mfma_i32_16x16x64_i8 v[132:135], v[20:23], v[112:115], 0
	v_mfma_i32_16x16x64_i8 v[28:31], v[28:31], v[120:123], 0
	v_mfma_i32_16x16x64_i8 v[20:23], v[20:23], v[120:123], 0
	v_mfma_i32_16x16x64_i8 v[236:239], v[16:19], v[116:119], v[132:135]
	v_mfma_i32_16x16x64_i8 v[24:27], v[24:27], v[124:127], v[28:31]
	v_mfma_i32_16x16x64_i8 v[16:19], v[16:19], v[124:127], v[20:23]
	v_mfma_i32_16x16x64_i8 v[20:23], v[12:15], v[60:63], 0
	v_mfma_i32_16x16x64_i8 v[28:31], v[4:7], v[60:63], 0
	v_mfma_i32_16x16x64_i8 v[20:23], v[8:11], v[100:103], v[20:23]
	v_mfma_i32_16x16x64_i8 v[28:31], v[0:3], v[100:103], v[28:31]
	v_mfma_i32_16x16x64_i8 v[60:63], v[12:15], v[104:107], 0
	v_mfma_i32_16x16x64_i8 v[100:103], v[4:7], v[104:107], 0
	v_mfma_i32_16x16x64_i8 v[104:107], v[12:15], v[112:115], 0
	v_mfma_i32_16x16x64_i8 v[100:103], v[0:3], v[108:111], v[100:103]
	v_mfma_i32_16x16x64_i8 v[240:243], v[8:11], v[116:119], v[104:107]
	v_mfma_i32_16x16x64_i8 v[104:107], v[4:7], v[112:115], 0
	v_mfma_i32_16x16x64_i8 v[12:15], v[12:15], v[120:123], 0
	v_mfma_i32_16x16x64_i8 v[4:7], v[4:7], v[120:123], 0
	v_mfma_i32_16x16x64_i8 v[60:63], v[8:11], v[108:111], v[60:63]
	v_mfma_i32_16x16x64_i8 v[244:247], v[0:3], v[116:119], v[104:107]
	v_mfma_i32_16x16x64_i8 v[8:11], v[8:11], v[124:127], v[12:15]
	v_mfma_i32_16x16x64_i8 v[0:3], v[0:3], v[124:127], v[4:7]
	s_barrier
	s_nop 1
	ds_read_b128 v[4:7], v229
	ds_read_b128 v[12:15], v229 offset:1024
	ds_read_b128 v[104:107], v229 offset:2048
	ds_read_b128 v[116:119], v229 offset:3072
	ds_read_b128 v[124:127], v230
	ds_read_b128 v[248:251], v230 offset:1024
	ds_read_b128 v[208:211], v230 offset:2048
	ds_read_b128 v[64:67], v230 offset:3072
	ds_read_b128 v[108:111], v228 offset:32768
	ds_read_b128 v[112:115], v228 offset:33792
	ds_read_b128 v[120:123], v228 offset:34816
	ds_read_b128 v[132:135], v228 offset:35840
	ds_read_b128 v[140:143], v228 offset:36864
	ds_read_b128 v[152:155], v228 offset:37888
	ds_read_b128 v[68:71], v228 offset:38912
	ds_read_b128 v[72:75], v228 offset:39936
	s_add_u32 s44, s44, 0x40100
	s_addc_u32 s45, s45, 0
	s_add_i32 m0, s31, 0x4000
	s_nop 0
	global_load_lds_dwordx4 v219, s[44:45]
	s_nop 0
	s_add_i32 m0, s31, 0x6000
	s_nop 0
	global_load_lds_dwordx4 v221, s[44:45]
	s_waitcnt vmcnt(8)
	s_waitcnt lgkmcnt(0)
	s_barrier
	v_mfma_i32_16x16x64_i8 v[76:79], v[104:107], v[120:123], v[76:79]
	v_mfma_i32_16x16x64_i8 v[180:183], v[116:119], v[132:135], v[76:79]
	v_mfma_i32_16x16x64_i8 v[76:79], v[4:7], v[140:143], v[80:83]
	v_mfma_i32_16x16x64_i8 v[136:139], v[4:7], v[108:111], v[136:139]
	v_mfma_i32_16x16x64_i8 v[164:167], v[12:15], v[152:155], v[76:79]
	v_mfma_i32_16x16x64_i8 v[76:79], v[104:107], v[140:143], v[84:87]
	v_mfma_i32_16x16x64_i8 v[200:203], v[12:15], v[112:115], v[136:139]
	v_mfma_i32_16x16x64_i8 v[136:139], v[104:107], v[108:111], v[144:147]
	v_mfma_i32_16x16x64_i8 v[160:163], v[116:119], v[152:155], v[76:79]
	v_mfma_i32_16x16x64_i8 v[76:79], v[4:7], v[68:71], v[88:91]
	v_mfma_i32_16x16x64_i8 v[196:199], v[116:119], v[112:115], v[136:139]
	v_mfma_i32_16x16x64_i8 v[136:139], v[4:7], v[120:123], v[148:151]
	v_mfma_i32_16x16x64_i8 v[148:151], v[12:15], v[72:75], v[76:79]
	v_mfma_i32_16x16x64_i8 v[76:79], v[104:107], v[68:71], v[92:95]
	v_mfma_i32_16x16x64_i8 v[184:187], v[12:15], v[132:135], v[136:139]
	v_mfma_i32_16x16x64_i8 v[144:147], v[116:119], v[72:75], v[76:79]
	v_mfma_i32_16x16x64_i8 v[32:35], v[208:211], v[108:111], v[32:35]
	v_mfma_i32_16x16x64_i8 v[188:191], v[64:67], v[112:115], v[32:35]
	v_mfma_i32_16x16x64_i8 v[32:35], v[124:127], v[120:123], v[36:39]
	v_mfma_i32_16x16x64_i8 v[176:179], v[248:251], v[132:135], v[32:35]
	v_mfma_i32_16x16x64_i8 v[32:35], v[208:211], v[120:123], v[40:43]
	v_mfma_i32_16x16x64_i8 v[172:175], v[64:67], v[132:135], v[32:35]
	v_mfma_i32_16x16x64_i8 v[32:35], v[124:127], v[140:143], v[44:47]
	v_mfma_i32_16x16x64_i8 v[156:159], v[248:251], v[152:155], v[32:35]
	v_mfma_i32_16x16x64_i8 v[32:35], v[208:211], v[140:143], v[48:51]
	v_mfma_i32_16x16x64_i8 v[152:155], v[64:67], v[152:155], v[32:35]
	v_mfma_i32_16x16x64_i8 v[32:35], v[124:127], v[68:71], v[52:55]
	v_mfma_i32_16x16x64_i8 v[76:79], v[124:127], v[108:111], v[96:99]
	v_mfma_i32_16x16x64_i8 v[140:143], v[248:251], v[72:75], v[32:35]
	v_mfma_i32_16x16x64_i8 v[32:35], v[208:211], v[68:71], v[56:59]
	v_mfma_i32_16x16x64_i8 v[192:195], v[248:251], v[112:115], v[76:79]
	v_mfma_i32_16x16x64_i8 v[136:139], v[64:67], v[72:75], v[32:35]
	s_barrier
	s_nop 3
	ds_read_b128 v[32:35], v228 offset:49152
	ds_read_b128 v[36:39], v228 offset:50176
	ds_read_b128 v[40:43], v228 offset:51200
	ds_read_b128 v[44:47], v228 offset:52224
	ds_read_b128 v[48:51], v228 offset:53248
	ds_read_b128 v[52:55], v228 offset:54272
	ds_read_b128 v[56:59], v228 offset:55296
	ds_read_b128 v[88:91], v228 offset:56320
	s_add_i32 m0, s31, 0x18000
	s_nop 0
	global_load_lds_dwordx4 v220, s[52:53]
	s_nop 0
	s_add_i32 m0, s31, 0x1a000
	s_nop 0
	global_load_lds_dwordx4 v222, s[52:53]
	s_add_u32 s44, s42, 0x40180
	s_addc_u32 s45, s43, 0
	s_add_i32 m0, s31, 0x1c000
	s_nop 0
	global_load_lds_dwordx4 v220, s[44:45]
	s_nop 0
	s_add_i32 m0, s31, 0x1e000
	s_nop 0
	global_load_lds_dwordx4 v222, s[44:45]
	s_nop 0
	s_add_i32 m0, s31, 0x8000
	s_nop 0
	global_load_lds_dwordx4 v219, s[50:51]
	s_nop 0
	s_add_i32 m0, s31, 0xa000
	s_nop 0
	global_load_lds_dwordx4 v221, s[50:51]
	s_waitcnt vmcnt(8)
	s_waitcnt lgkmcnt(0)
	s_barrier
	v_mfma_i32_16x16x64_i8 v[68:71], v[4:7], v[32:35], v[128:131]
	v_mfma_i32_16x16x64_i8 v[132:135], v[12:15], v[36:39], v[68:71]
	v_mfma_i32_16x16x64_i8 v[68:71], v[104:107], v[32:35], v[168:171]
	v_mfma_i32_16x16x64_i8 v[128:131], v[116:119], v[36:39], v[68:71]
	v_mfma_i32_16x16x64_i8 v[68:71], v[4:7], v[40:43], v[204:207]
	v_mfma_i32_16x16x64_i8 v[112:115], v[12:15], v[44:47], v[68:71]
	v_mfma_i32_16x16x64_i8 v[68:71], v[104:107], v[40:43], v[214:217]
	v_mfma_i32_16x16x64_i8 v[108:111], v[116:119], v[44:47], v[68:71]
	v_mfma_i32_16x16x64_i8 v[68:71], v[4:7], v[48:51], v[232:235]
	v_mfma_i32_16x16x64_i8 v[4:7], v[4:7], v[56:59], v[24:27]
	v_mfma_i32_16x16x64_i8 v[96:99], v[12:15], v[52:55], v[68:71]
	v_mfma_i32_16x16x64_i8 v[68:71], v[104:107], v[48:51], v[236:239]
	v_mfma_i32_16x16x64_i8 v[76:79], v[12:15], v[88:91], v[4:7]
	v_mfma_i32_16x16x64_i8 v[4:7], v[104:107], v[56:59], v[16:19]
	v_mfma_i32_16x16x64_i8 v[92:95], v[116:119], v[52:55], v[68:71]
	v_mfma_i32_16x16x64_i8 v[72:75], v[116:119], v[88:91], v[4:7]
	v_mfma_i32_16x16x64_i8 v[4:7], v[124:127], v[32:35], v[20:23]
	v_mfma_i32_16x16x64_i8 v[120:123], v[248:251], v[36:39], v[4:7]
	v_mfma_i32_16x16x64_i8 v[4:7], v[208:211], v[32:35], v[28:31]
	v_mfma_i32_16x16x64_i8 v[116:119], v[64:67], v[36:39], v[4:7]
	v_mfma_i32_16x16x64_i8 v[4:7], v[124:127], v[40:43], v[60:63]
	v_mfma_i32_16x16x64_i8 v[104:107], v[248:251], v[44:47], v[4:7]
	v_mfma_i32_16x16x64_i8 v[4:7], v[208:211], v[40:43], v[100:103]
	v_mfma_i32_16x16x64_i8 v[100:103], v[64:67], v[44:47], v[4:7]
	v_mfma_i32_16x16x64_i8 v[4:7], v[124:127], v[48:51], v[240:243]
	v_mfma_i32_16x16x64_i8 v[84:87], v[248:251], v[52:55], v[4:7]
	v_mfma_i32_16x16x64_i8 v[4:7], v[208:211], v[48:51], v[244:247]
	v_mfma_i32_16x16x64_i8 v[80:83], v[64:67], v[52:55], v[4:7]
	v_mfma_i32_16x16x64_i8 v[4:7], v[124:127], v[56:59], v[8:11]
	v_mfma_i32_16x16x64_i8 v[0:3], v[208:211], v[56:59], v[0:3]
	v_mfma_i32_16x16x64_i8 v[68:71], v[248:251], v[88:91], v[4:7]
	v_mfma_i32_16x16x64_i8 v[64:67], v[64:67], v[88:91], v[0:3]
	s_barrier
	s_add_u32 s44, s27, s48
	s_addc_u32 s45, s29, s49
	s_add_u32 s79, s42, 0x200
	s_addc_u32 s80, s43, 0
	s_add_i32 s81, s54, 0
	s_add_i32 s81, s81, 0x20000

.LBB0_933:
	ds_read_b128 v[0:3], v227
	ds_read_b128 v[4:7], v227 offset:1024
	ds_read_b128 v[8:11], v227 offset:2048
	ds_read_b128 v[12:15], v227 offset:3072
	ds_read_b128 v[16:19], v226
	ds_read_b128 v[20:23], v226 offset:1024
	ds_read_b128 v[24:27], v226 offset:2048
	ds_read_b128 v[28:31], v226 offset:3072
	ds_read_b128 v[32:35], v228
	ds_read_b128 v[36:39], v228 offset:1024
	ds_read_b128 v[40:43], v228 offset:2048
	ds_read_b128 v[44:47], v228 offset:3072
	ds_read_b128 v[48:51], v228 offset:4096
	ds_read_b128 v[52:55], v228 offset:5120
	ds_read_b128 v[56:59], v228 offset:6144
	ds_read_b128 v[60:63], v228 offset:7168
	s_add_u32 s42, s46, 0x100
	s_addc_u32 s43, s47, 0
	s_and_b64 s[48:49], s[48:49], exec
	s_cselect_b32 s54, s76, s42
	s_cselect_b32 s55, s9, s43
	s_cselect_b32 s51, s35, s80
	s_cselect_b32 s50, s77, s79
	s_add_u32 s48, s54, 0x80
	s_addc_u32 s49, s55, 0
	s_add_u32 s52, s50, 0x80
	s_addc_u32 s53, s51, 0
	s_add_u32 s46, s46, 0x40080
	s_addc_u32 s47, s47, 0
	s_add_i32 m0, s31, 0xc000
	s_nop 0
	global_load_lds_dwordx4 v219, s[46:47]
	s_nop 0
	s_add_i32 m0, s31, 0xe000
	s_nop 0
	global_load_lds_dwordx4 v221, s[46:47]
	s_waitcnt vmcnt(8)
	s_waitcnt lgkmcnt(0)
	s_barrier
	v_mfma_i32_16x16x64_i8 v[180:183], v[8:11], v[40:43], v[180:183]
	v_mfma_i32_16x16x64_i8 v[164:167], v[0:3], v[48:51], v[164:167]
	v_mfma_i32_16x16x64_i8 v[148:151], v[0:3], v[56:59], v[148:151]
	v_mfma_i32_16x16x64_i8 v[160:163], v[8:11], v[48:51], v[160:163]
	v_mfma_i32_16x16x64_i8 v[144:147], v[8:11], v[56:59], v[144:147]
	v_mfma_i32_16x16x64_i8 v[88:91], v[0:3], v[32:35], v[200:203]
	v_mfma_i32_16x16x64_i8 v[168:171], v[0:3], v[40:43], v[184:187]
	v_mfma_i32_16x16x64_i8 v[124:127], v[8:11], v[32:35], v[196:199]
	v_mfma_i32_16x16x64_i8 v[180:183], v[12:15], v[44:47], v[180:183]
	v_mfma_i32_16x16x64_i8 v[164:167], v[4:7], v[52:55], v[164:167]
	v_mfma_i32_16x16x64_i8 v[148:151], v[4:7], v[60:63], v[148:151]
	v_mfma_i32_16x16x64_i8 v[160:163], v[12:15], v[52:55], v[160:163]
	v_mfma_i32_16x16x64_i8 v[144:147], v[12:15], v[60:63], v[144:147]
	v_mfma_i32_16x16x64_i8 v[88:91], v[4:7], v[36:39], v[88:91]
	v_mfma_i32_16x16x64_i8 v[168:171], v[4:7], v[44:47], v[168:171]
	v_mfma_i32_16x16x64_i8 v[124:127], v[12:15], v[36:39], v[124:127]
	v_mfma_i32_16x16x64_i8 v[184:187], v[16:19], v[32:35], v[192:195]
	v_mfma_i32_16x16x64_i8 v[32:35], v[24:27], v[32:35], v[188:191]
	v_mfma_i32_16x16x64_i8 v[192:195], v[20:23], v[36:39], v[184:187]
	v_mfma_i32_16x16x64_i8 v[32:35], v[28:31], v[36:39], v[32:35]
	v_mfma_i32_16x16x64_i8 v[36:39], v[16:19], v[40:43], v[176:179]
	v_mfma_i32_16x16x64_i8 v[40:43], v[24:27], v[40:43], v[172:175]
	v_mfma_i32_16x16x64_i8 v[36:39], v[20:23], v[44:47], v[36:39]
	v_mfma_i32_16x16x64_i8 v[40:43], v[28:31], v[44:47], v[40:43]
	v_mfma_i32_16x16x64_i8 v[44:47], v[16:19], v[48:51], v[156:159]
	v_mfma_i32_16x16x64_i8 v[48:51], v[24:27], v[48:51], v[152:155]
	v_mfma_i32_16x16x64_i8 v[44:47], v[20:23], v[52:55], v[44:47]
	v_mfma_i32_16x16x64_i8 v[48:51], v[28:31], v[52:55], v[48:51]
	v_mfma_i32_16x16x64_i8 v[52:55], v[16:19], v[56:59], v[140:143]
	v_mfma_i32_16x16x64_i8 v[56:59], v[24:27], v[56:59], v[136:139]
	v_mfma_i32_16x16x64_i8 v[52:55], v[20:23], v[60:63], v[52:55]
	v_mfma_i32_16x16x64_i8 v[56:59], v[28:31], v[60:63], v[56:59]
	s_barrier
	ds_read_b128 v[60:63], v228 offset:16384
	ds_read_b128 v[136:139], v228 offset:17408
	ds_read_b128 v[140:143], v228 offset:18432
	ds_read_b128 v[152:155], v228 offset:19456
	ds_read_b128 v[156:159], v228 offset:20480
	ds_read_b128 v[172:175], v228 offset:21504
	ds_read_b128 v[176:179], v228 offset:22528
	ds_read_b128 v[184:187], v228 offset:23552
	s_add_i32 m0, s31, 0x10000
	s_nop 0
	global_load_lds_dwordx4 v220, s[50:51]
	s_nop 0
	s_add_i32 m0, s31, 0x12000
	s_nop 0
	global_load_lds_dwordx4 v222, s[50:51]
	s_add_u32 s46, s50, 0x40000
	s_addc_u32 s47, s51, 0
	s_add_i32 m0, s31, 0x14000
	s_nop 0
	global_load_lds_dwordx4 v220, s[46:47]
	s_nop 0
	s_add_i32 m0, s31, 0x16000
	s_nop 0
	global_load_lds_dwordx4 v222, s[46:47]
	s_nop 0
	s_add_i32 m0, s31, 0
	s_nop 0
	global_load_lds_dwordx4 v219, s[54:55]
	s_nop 0
	s_add_i32 m0, s31, 0x2000
	s_nop 0
	global_load_lds_dwordx4 v221, s[54:55]
	s_waitcnt vmcnt(8)
	s_waitcnt lgkmcnt(0)
	s_barrier
	v_mfma_i32_16x16x64_i8 v[132:135], v[0:3], v[60:63], v[132:135]
	v_mfma_i32_16x16x64_i8 v[112:115], v[0:3], v[140:143], v[112:115]
	v_mfma_i32_16x16x64_i8 v[96:99], v[0:3], v[156:159], v[96:99]
	v_mfma_i32_16x16x64_i8 v[0:3], v[0:3], v[176:179], v[76:79]
	v_mfma_i32_16x16x64_i8 v[128:131], v[8:11], v[60:63], v[128:131]
	v_mfma_i32_16x16x64_i8 v[108:111], v[8:11], v[140:143], v[108:111]
	v_mfma_i32_16x16x64_i8 v[92:95], v[8:11], v[156:159], v[92:95]
	v_mfma_i32_16x16x64_i8 v[76:79], v[4:7], v[184:187], v[0:3]
	v_mfma_i32_16x16x64_i8 v[0:3], v[8:11], v[176:179], v[72:75]
	v_mfma_i32_16x16x64_i8 v[132:135], v[4:7], v[136:139], v[132:135]
	v_mfma_i32_16x16x64_i8 v[128:131], v[12:15], v[136:139], v[128:131]
	v_mfma_i32_16x16x64_i8 v[112:115], v[4:7], v[152:155], v[112:115]
	v_mfma_i32_16x16x64_i8 v[108:111], v[12:15], v[152:155], v[108:111]
	v_mfma_i32_16x16x64_i8 v[96:99], v[4:7], v[172:175], v[96:99]
	v_mfma_i32_16x16x64_i8 v[92:95], v[12:15], v[172:175], v[92:95]
	v_mfma_i32_16x16x64_i8 v[72:75], v[12:15], v[184:187], v[0:3]
	v_mfma_i32_16x16x64_i8 v[0:3], v[16:19], v[60:63], v[120:123]
	v_mfma_i32_16x16x64_i8 v[120:123], v[20:23], v[136:139], v[0:3]
	v_mfma_i32_16x16x64_i8 v[0:3], v[24:27], v[60:63], v[116:119]
	v_mfma_i32_16x16x64_i8 v[116:119], v[28:31], v[136:139], v[0:3]
	v_mfma_i32_16x16x64_i8 v[0:3], v[16:19], v[140:143], v[104:107]
	v_mfma_i32_16x16x64_i8 v[104:107], v[20:23], v[152:155], v[0:3]
	v_mfma_i32_16x16x64_i8 v[0:3], v[24:27], v[140:143], v[100:103]
	v_mfma_i32_16x16x64_i8 v[100:103], v[28:31], v[152:155], v[0:3]
	v_mfma_i32_16x16x64_i8 v[0:3], v[16:19], v[156:159], v[84:87]
	v_mfma_i32_16x16x64_i8 v[84:87], v[20:23], v[172:175], v[0:3]
	v_mfma_i32_16x16x64_i8 v[0:3], v[24:27], v[156:159], v[80:83]
	v_mfma_i32_16x16x64_i8 v[80:83], v[28:31], v[172:175], v[0:3]
	v_mfma_i32_16x16x64_i8 v[0:3], v[16:19], v[176:179], v[68:71]
	v_mfma_i32_16x16x64_i8 v[68:71], v[20:23], v[184:187], v[0:3]
	v_mfma_i32_16x16x64_i8 v[0:3], v[24:27], v[176:179], v[64:67]
	v_mfma_i32_16x16x64_i8 v[64:67], v[28:31], v[184:187], v[0:3]
	s_barrier
	ds_read_b128 v[16:19], v229
	ds_read_b128 v[8:11], v229 offset:1024
	ds_read_b128 v[4:7], v229 offset:2048
	s_nop 1
	ds_read_b128 v[0:3], v229 offset:3072
	ds_read_b128 v[28:31], v230
	ds_read_b128 v[24:27], v230 offset:1024
	ds_read_b128 v[20:23], v230 offset:2048
	ds_read_b128 v[12:15], v230 offset:3072
	ds_read_b128 v[60:63], v228 offset:32768
	ds_read_b128 v[136:139], v228 offset:33792
	ds_read_b128 v[140:143], v228 offset:34816
	ds_read_b128 v[152:155], v228 offset:35840
	ds_read_b128 v[204:207], v228 offset:36864
	ds_read_b128 v[208:211], v228 offset:37888
	ds_read_b128 v[214:217], v228 offset:38912
	ds_read_b128 v[232:235], v228 offset:39936
	s_add_u32 s46, s54, 0x40000
	s_addc_u32 s47, s55, 0
	s_add_i32 m0, s31, 0x4000
	s_nop 0
	global_load_lds_dwordx4 v219, s[46:47]
	s_nop 0
	s_add_i32 m0, s31, 0x6000
	s_nop 0
	global_load_lds_dwordx4 v221, s[46:47]
	s_waitcnt vmcnt(8)
	s_waitcnt lgkmcnt(0)
	s_barrier
	v_mfma_i32_16x16x64_i8 v[88:91], v[16:19], v[60:63], v[88:91]
	v_mfma_i32_16x16x64_i8 v[200:203], v[8:11], v[136:139], v[88:91]
	v_mfma_i32_16x16x64_i8 v[88:91], v[4:7], v[60:63], v[124:127]
	v_mfma_i32_16x16x64_i8 v[196:199], v[0:3], v[136:139], v[88:91]
	v_mfma_i32_16x16x64_i8 v[88:91], v[16:19], v[140:143], v[168:171]
	v_mfma_i32_16x16x64_i8 v[184:187], v[8:11], v[152:155], v[88:91]
	v_mfma_i32_16x16x64_i8 v[88:91], v[4:7], v[140:143], v[180:183]
	v_mfma_i32_16x16x64_i8 v[180:183], v[0:3], v[152:155], v[88:91]
	v_mfma_i32_16x16x64_i8 v[88:91], v[16:19], v[204:207], v[164:167]
	v_mfma_i32_16x16x64_i8 v[164:167], v[8:11], v[208:211], v[88:91]
	v_mfma_i32_16x16x64_i8 v[88:91], v[4:7], v[204:207], v[160:163]
	v_mfma_i32_16x16x64_i8 v[160:163], v[0:3], v[208:211], v[88:91]
	v_mfma_i32_16x16x64_i8 v[88:91], v[16:19], v[214:217], v[148:151]
	v_mfma_i32_16x16x64_i8 v[148:151], v[8:11], v[232:235], v[88:91]
	v_mfma_i32_16x16x64_i8 v[88:91], v[4:7], v[214:217], v[144:147]
	v_mfma_i32_16x16x64_i8 v[144:147], v[0:3], v[232:235], v[88:91]
	v_mfma_i32_16x16x64_i8 v[32:35], v[20:23], v[60:63], v[32:35]
	v_mfma_i32_16x16x64_i8 v[188:191], v[12:15], v[136:139], v[32:35]
	v_mfma_i32_16x16x64_i8 v[32:35], v[28:31], v[140:143], v[36:39]
	v_mfma_i32_16x16x64_i8 v[176:179], v[24:27], v[152:155], v[32:35]
	v_mfma_i32_16x16x64_i8 v[32:35], v[20:23], v[140:143], v[40:43]
	v_mfma_i32_16x16x64_i8 v[172:175], v[12:15], v[152:155], v[32:35]
	v_mfma_i32_16x16x64_i8 v[32:35], v[28:31], v[204:207], v[44:47]
	v_mfma_i32_16x16x64_i8 v[156:159], v[24:27], v[208:211], v[32:35]
	v_mfma_i32_16x16x64_i8 v[32:35], v[20:23], v[204:207], v[48:51]
	v_mfma_i32_16x16x64_i8 v[152:155], v[12:15], v[208:211], v[32:35]
	v_mfma_i32_16x16x64_i8 v[32:35], v[28:31], v[214:217], v[52:55]
	v_mfma_i32_16x16x64_i8 v[88:91], v[28:31], v[60:63], v[192:195]
	v_mfma_i32_16x16x64_i8 v[140:143], v[24:27], v[232:235], v[32:35]
	v_mfma_i32_16x16x64_i8 v[32:35], v[20:23], v[214:217], v[56:59]
	v_mfma_i32_16x16x64_i8 v[192:195], v[24:27], v[136:139], v[88:91]
	v_mfma_i32_16x16x64_i8 v[136:139], v[12:15], v[232:235], v[32:35]
	s_barrier
	ds_read_b128 v[60:63], v228 offset:49152
	ds_read_b128 v[56:59], v228 offset:50176
	ds_read_b128 v[52:55], v228 offset:51200
	ds_read_b128 v[48:51], v228 offset:52224
	ds_read_b128 v[44:47], v228 offset:53248
	ds_read_b128 v[40:43], v228 offset:54272
	ds_read_b128 v[36:39], v228 offset:55296
	ds_read_b128 v[32:35], v228 offset:56320
	s_add_i32 m0, s31, 0x18000
	s_nop 0
	global_load_lds_dwordx4 v220, s[52:53]
	s_nop 0
	s_add_i32 m0, s31, 0x1a000
	s_nop 0
	global_load_lds_dwordx4 v222, s[52:53]
	s_add_u32 s46, s50, 0x40080
	s_addc_u32 s47, s51, 0
	s_add_i32 m0, s31, 0x1c000
	s_nop 0
	global_load_lds_dwordx4 v220, s[46:47]
	s_nop 0
	s_add_i32 m0, s31, 0x1e000
	s_nop 0
	global_load_lds_dwordx4 v222, s[46:47]
	s_nop 0
	s_add_i32 m0, s31, 0x8000
	s_nop 0
	global_load_lds_dwordx4 v219, s[48:49]
	s_nop 0
	s_add_i32 m0, s31, 0xa000
	s_nop 0
	global_load_lds_dwordx4 v221, s[48:49]
	s_waitcnt vmcnt(8)
	s_waitcnt lgkmcnt(0)
	s_barrier
	v_mfma_i32_16x16x64_i8 v[88:91], v[16:19], v[60:63], v[132:135]
	v_mfma_i32_16x16x64_i8 v[132:135], v[8:11], v[56:59], v[88:91]
	v_mfma_i32_16x16x64_i8 v[88:91], v[4:7], v[60:63], v[128:131]
	v_mfma_i32_16x16x64_i8 v[128:131], v[0:3], v[56:59], v[88:91]
	v_mfma_i32_16x16x64_i8 v[88:91], v[16:19], v[52:55], v[112:115]
	v_mfma_i32_16x16x64_i8 v[112:115], v[8:11], v[48:51], v[88:91]
	v_mfma_i32_16x16x64_i8 v[88:91], v[4:7], v[52:55], v[108:111]
	v_mfma_i32_16x16x64_i8 v[108:111], v[0:3], v[48:51], v[88:91]
	v_mfma_i32_16x16x64_i8 v[88:91], v[16:19], v[44:47], v[96:99]
	v_mfma_i32_16x16x64_i8 v[96:99], v[8:11], v[40:43], v[88:91]
	v_mfma_i32_16x16x64_i8 v[88:91], v[4:7], v[44:47], v[92:95]
	v_mfma_i32_16x16x64_i8 v[76:79], v[16:19], v[36:39], v[76:79]
	v_mfma_i32_16x16x64_i8 v[72:75], v[4:7], v[36:39], v[72:75]
	v_mfma_i32_16x16x64_i8 v[92:95], v[0:3], v[40:43], v[88:91]
	v_mfma_i32_16x16x64_i8 v[76:79], v[8:11], v[32:35], v[76:79]
	v_mfma_i32_16x16x64_i8 v[72:75], v[0:3], v[32:35], v[72:75]
	v_mfma_i32_16x16x64_i8 v[88:91], v[28:31], v[60:63], v[120:123]
	v_mfma_i32_16x16x64_i8 v[120:123], v[24:27], v[56:59], v[88:91]
	v_mfma_i32_16x16x64_i8 v[88:91], v[20:23], v[60:63], v[116:119]
	v_mfma_i32_16x16x64_i8 v[116:119], v[12:15], v[56:59], v[88:91]
	v_mfma_i32_16x16x64_i8 v[88:91], v[28:31], v[52:55], v[104:107]
	v_mfma_i32_16x16x64_i8 v[104:107], v[24:27], v[48:51], v[88:91]
	v_mfma_i32_16x16x64_i8 v[88:91], v[20:23], v[52:55], v[100:103]
	v_mfma_i32_16x16x64_i8 v[84:87], v[28:31], v[44:47], v[84:87]
	v_mfma_i32_16x16x64_i8 v[80:83], v[20:23], v[44:47], v[80:83]
	v_mfma_i32_16x16x64_i8 v[68:71], v[28:31], v[36:39], v[68:71]
	v_mfma_i32_16x16x64_i8 v[64:67], v[20:23], v[36:39], v[64:67]
	v_mfma_i32_16x16x64_i8 v[100:103], v[12:15], v[48:51], v[88:91]
	v_mfma_i32_16x16x64_i8 v[84:87], v[24:27], v[40:43], v[84:87]
	v_mfma_i32_16x16x64_i8 v[80:83], v[12:15], v[40:43], v[80:83]
	v_mfma_i32_16x16x64_i8 v[68:71], v[24:27], v[32:35], v[68:71]
	v_mfma_i32_16x16x64_i8 v[64:67], v[12:15], v[32:35], v[64:67]
	s_barrier
	s_add_i32 s37, s37, 2
	s_add_u32 s79, s79, 0x100
	s_addc_u32 s80, s80, 0
	s_cmp_gt_u32 s37, 13
	s_cbranch_scc1 .LBB0_935
	s_mov_b64 s[46:47], s[42:43]
	s_branch .LBB0_931

.LBB0_1109:
	ds_read_b128 v[132:135], v143
	ds_read_b128 v[148:151], v143 offset:1024
	ds_read_b128 v[152:155], v143 offset:2048
	ds_read_b128 v[156:159], v143 offset:3072
	ds_read_b128 v[160:163], v144
	ds_read_b128 v[164:167], v144 offset:1024
	ds_read_b128 v[168:171], v144 offset:2048
	ds_read_b128 v[172:175], v144 offset:3072
	ds_read_b128 v[176:179], v145
	ds_read_b128 v[180:183], v145 offset:1024
	ds_read_b128 v[184:187], v145 offset:2048
	ds_read_b128 v[188:191], v145 offset:3072
	ds_read_b128 v[192:195], v145 offset:4096
	ds_read_b128 v[196:199], v145 offset:5120
	ds_read_b128 v[200:203], v145 offset:6144
	ds_read_b128 v[204:207], v145 offset:7168
	s_cmp_eq_u32 s57, 28
	s_cselect_b32 s40, s51, s53
	s_cselect_b32 s41, s23, s54
	s_cselect_b32 s36, s52, s55
	s_cselect_b32 s37, s21, s56
	s_add_u32 s34, s40, 0x80
	s_addc_u32 s35, s41, 0
	s_add_u32 s38, s36, 0x80
	s_addc_u32 s39, s37, 0
	s_add_i32 m0, s2, 0xc000
	s_nop 0
	global_load_lds_dwordx4 v139, s[30:31]
	s_nop 0
	s_add_i32 m0, s2, 0xe000
	s_nop 0
	global_load_lds_dwordx4 v141, s[30:31]
	s_waitcnt vmcnt(8)
	s_waitcnt lgkmcnt(0)
	s_barrier
	v_mfma_f32_16x16x32_bf16 v[116:119], v[132:135], v[176:179], v[116:119]
	v_mfma_f32_16x16x32_bf16 v[112:115], v[152:155], v[176:179], v[112:115]
	v_mfma_f32_16x16x32_bf16 v[100:103], v[152:155], v[184:187], v[100:103]
	v_mfma_f32_16x16x32_bf16 v[108:111], v[132:135], v[184:187], v[108:111]
	v_mfma_f32_16x16x32_bf16 v[92:95], v[132:135], v[192:195], v[92:95]
	v_mfma_f32_16x16x32_bf16 v[84:87], v[152:155], v[192:195], v[84:87]
	v_mfma_f32_16x16x32_bf16 v[56:59], v[152:155], v[200:203], v[56:59]
	v_mfma_f32_16x16x32_bf16 v[72:75], v[132:135], v[200:203], v[72:75]
	v_mfma_f32_16x16x32_bf16 v[116:119], v[148:151], v[180:183], v[116:119]
	v_mfma_f32_16x16x32_bf16 v[112:115], v[156:159], v[180:183], v[112:115]
	v_mfma_f32_16x16x32_bf16 v[100:103], v[156:159], v[188:191], v[100:103]
	v_mfma_f32_16x16x32_bf16 v[108:111], v[148:151], v[188:191], v[108:111]
	v_mfma_f32_16x16x32_bf16 v[92:95], v[148:151], v[196:199], v[92:95]
	v_mfma_f32_16x16x32_bf16 v[84:87], v[156:159], v[196:199], v[84:87]
	v_mfma_f32_16x16x32_bf16 v[56:59], v[156:159], v[204:207], v[56:59]
	v_mfma_f32_16x16x32_bf16 v[72:75], v[148:151], v[204:207], v[72:75]
	v_mfma_f32_16x16x32_bf16 v[124:127], v[160:163], v[176:179], v[124:127]
	v_mfma_f32_16x16x32_bf16 v[120:123], v[168:171], v[176:179], v[120:123]
	v_mfma_f32_16x16x32_bf16 v[96:99], v[168:171], v[184:187], v[96:99]
	v_mfma_f32_16x16x32_bf16 v[104:107], v[160:163], v[184:187], v[104:107]
	v_mfma_f32_16x16x32_bf16 v[88:91], v[160:163], v[192:195], v[88:91]
	v_mfma_f32_16x16x32_bf16 v[80:83], v[168:171], v[192:195], v[80:83]
	v_mfma_f32_16x16x32_bf16 v[48:51], v[168:171], v[200:203], v[48:51]
	v_mfma_f32_16x16x32_bf16 v[64:67], v[160:163], v[200:203], v[64:67]
	v_mfma_f32_16x16x32_bf16 v[124:127], v[164:167], v[180:183], v[124:127]
	v_mfma_f32_16x16x32_bf16 v[120:123], v[172:175], v[180:183], v[120:123]
	v_mfma_f32_16x16x32_bf16 v[96:99], v[172:175], v[188:191], v[96:99]
	v_mfma_f32_16x16x32_bf16 v[104:107], v[164:167], v[188:191], v[104:107]
	v_mfma_f32_16x16x32_bf16 v[88:91], v[164:167], v[196:199], v[88:91]
	v_mfma_f32_16x16x32_bf16 v[80:83], v[172:175], v[196:199], v[80:83]
	v_mfma_f32_16x16x32_bf16 v[48:51], v[172:175], v[204:207], v[48:51]
	v_mfma_f32_16x16x32_bf16 v[64:67], v[164:167], v[204:207], v[64:67]
	s_barrier
	ds_read_b128 v[176:179], v145 offset:16384
	ds_read_b128 v[180:183], v145 offset:17408
	ds_read_b128 v[184:187], v145 offset:18432
	ds_read_b128 v[188:191], v145 offset:19456
	ds_read_b128 v[192:195], v145 offset:20480
	ds_read_b128 v[196:199], v145 offset:21504
	ds_read_b128 v[200:203], v145 offset:22528
	ds_read_b128 v[204:207], v145 offset:23552
	s_add_i32 m0, s2, 0x10000
	s_nop 0
	global_load_lds_dwordx4 v140, s[36:37]
	s_nop 0
	s_add_i32 m0, s2, 0x12000
	s_nop 0
	global_load_lds_dwordx4 v142, s[36:37]
	s_add_u32 s58, s36, 0x80000
	s_addc_u32 s59, s37, 0
	s_add_i32 m0, s2, 0x14000
	s_nop 0
	global_load_lds_dwordx4 v140, s[58:59]
	s_nop 0
	s_add_i32 m0, s2, 0x16000
	s_nop 0
	global_load_lds_dwordx4 v142, s[58:59]
	s_nop 0
	s_add_i32 m0, s2, 0
	s_nop 0
	global_load_lds_dwordx4 v139, s[40:41]
	s_nop 0
	s_add_i32 m0, s2, 0x2000
	s_nop 0
	global_load_lds_dwordx4 v141, s[40:41]
	s_waitcnt vmcnt(8)
	s_waitcnt lgkmcnt(0)
	s_barrier
	v_mfma_f32_16x16x32_bf16 v[76:79], v[132:135], v[176:179], v[76:79]
	v_mfma_f32_16x16x32_bf16 v[60:63], v[152:155], v[176:179], v[60:63]
	v_mfma_f32_16x16x32_bf16 v[36:39], v[152:155], v[184:187], v[36:39]
	v_mfma_f32_16x16x32_bf16 v[44:47], v[132:135], v[184:187], v[44:47]
	v_mfma_f32_16x16x32_bf16 v[28:31], v[132:135], v[192:195], v[28:31]
	v_mfma_f32_16x16x32_bf16 v[20:23], v[152:155], v[192:195], v[20:23]
	v_mfma_f32_16x16x32_bf16 v[4:7], v[152:155], v[200:203], v[4:7]
	v_mfma_f32_16x16x32_bf16 v[12:15], v[132:135], v[200:203], v[12:15]
	v_mfma_f32_16x16x32_bf16 v[76:79], v[148:151], v[180:183], v[76:79]
	v_mfma_f32_16x16x32_bf16 v[60:63], v[156:159], v[180:183], v[60:63]
	v_mfma_f32_16x16x32_bf16 v[36:39], v[156:159], v[188:191], v[36:39]
	v_mfma_f32_16x16x32_bf16 v[44:47], v[148:151], v[188:191], v[44:47]
	v_mfma_f32_16x16x32_bf16 v[28:31], v[148:151], v[196:199], v[28:31]
	v_mfma_f32_16x16x32_bf16 v[20:23], v[156:159], v[196:199], v[20:23]
	v_mfma_f32_16x16x32_bf16 v[4:7], v[156:159], v[204:207], v[4:7]
	v_mfma_f32_16x16x32_bf16 v[12:15], v[148:151], v[204:207], v[12:15]
	v_mfma_f32_16x16x32_bf16 v[68:71], v[160:163], v[176:179], v[68:71]
	v_mfma_f32_16x16x32_bf16 v[52:55], v[168:171], v[176:179], v[52:55]
	v_mfma_f32_16x16x32_bf16 v[32:35], v[168:171], v[184:187], v[32:35]
	v_mfma_f32_16x16x32_bf16 v[40:43], v[160:163], v[184:187], v[40:43]
	v_mfma_f32_16x16x32_bf16 v[24:27], v[160:163], v[192:195], v[24:27]
	v_mfma_f32_16x16x32_bf16 v[16:19], v[168:171], v[192:195], v[16:19]
	v_mfma_f32_16x16x32_bf16 v[0:3], v[168:171], v[200:203], v[0:3]
	v_mfma_f32_16x16x32_bf16 v[8:11], v[160:163], v[200:203], v[8:11]
	v_mfma_f32_16x16x32_bf16 v[68:71], v[164:167], v[180:183], v[68:71]
	v_mfma_f32_16x16x32_bf16 v[52:55], v[172:175], v[180:183], v[52:55]
	v_mfma_f32_16x16x32_bf16 v[32:35], v[172:175], v[188:191], v[32:35]
	v_mfma_f32_16x16x32_bf16 v[40:43], v[164:167], v[188:191], v[40:43]
	v_mfma_f32_16x16x32_bf16 v[24:27], v[164:167], v[196:199], v[24:27]
	v_mfma_f32_16x16x32_bf16 v[16:19], v[172:175], v[196:199], v[16:19]
	v_mfma_f32_16x16x32_bf16 v[0:3], v[172:175], v[204:207], v[0:3]
	v_mfma_f32_16x16x32_bf16 v[8:11], v[164:167], v[204:207], v[8:11]
	s_barrier
	ds_read_b128 v[132:135], v146
	ds_read_b128 v[148:151], v146 offset:1024
	ds_read_b128 v[152:155], v146 offset:2048
	ds_read_b128 v[156:159], v146 offset:3072
	ds_read_b128 v[160:163], v147
	ds_read_b128 v[164:167], v147 offset:1024
	ds_read_b128 v[168:171], v147 offset:2048
	ds_read_b128 v[172:175], v147 offset:3072
	ds_read_b128 v[176:179], v145 offset:32768
	ds_read_b128 v[180:183], v145 offset:33792
	ds_read_b128 v[184:187], v145 offset:34816
	ds_read_b128 v[188:191], v145 offset:35840
	ds_read_b128 v[192:195], v145 offset:36864
	ds_read_b128 v[196:199], v145 offset:37888
	ds_read_b128 v[200:203], v145 offset:38912
	ds_read_b128 v[204:207], v145 offset:39936
	s_add_u32 s40, s40, 0x80000
	s_addc_u32 s41, s41, 0
	s_add_i32 m0, s2, 0x4000
	s_nop 0
	global_load_lds_dwordx4 v139, s[40:41]
	s_nop 0
	s_add_i32 m0, s2, 0x6000
	s_nop 0
	global_load_lds_dwordx4 v141, s[40:41]
	s_waitcnt vmcnt(8)
	s_waitcnt lgkmcnt(0)
	s_barrier
	v_mfma_f32_16x16x32_bf16 v[116:119], v[132:135], v[176:179], v[116:119]
	v_mfma_f32_16x16x32_bf16 v[112:115], v[152:155], v[176:179], v[112:115]
	v_mfma_f32_16x16x32_bf16 v[100:103], v[152:155], v[184:187], v[100:103]
	v_mfma_f32_16x16x32_bf16 v[108:111], v[132:135], v[184:187], v[108:111]
	v_mfma_f32_16x16x32_bf16 v[92:95], v[132:135], v[192:195], v[92:95]
	v_mfma_f32_16x16x32_bf16 v[84:87], v[152:155], v[192:195], v[84:87]
	v_mfma_f32_16x16x32_bf16 v[56:59], v[152:155], v[200:203], v[56:59]
	v_mfma_f32_16x16x32_bf16 v[72:75], v[132:135], v[200:203], v[72:75]
	v_mfma_f32_16x16x32_bf16 v[116:119], v[148:151], v[180:183], v[116:119]
	v_mfma_f32_16x16x32_bf16 v[112:115], v[156:159], v[180:183], v[112:115]
	v_mfma_f32_16x16x32_bf16 v[100:103], v[156:159], v[188:191], v[100:103]
	v_mfma_f32_16x16x32_bf16 v[108:111], v[148:151], v[188:191], v[108:111]
	v_mfma_f32_16x16x32_bf16 v[92:95], v[148:151], v[196:199], v[92:95]
	v_mfma_f32_16x16x32_bf16 v[84:87], v[156:159], v[196:199], v[84:87]
	v_mfma_f32_16x16x32_bf16 v[56:59], v[156:159], v[204:207], v[56:59]
	v_mfma_f32_16x16x32_bf16 v[72:75], v[148:151], v[204:207], v[72:75]
	v_mfma_f32_16x16x32_bf16 v[124:127], v[160:163], v[176:179], v[124:127]
	v_mfma_f32_16x16x32_bf16 v[120:123], v[168:171], v[176:179], v[120:123]
	v_mfma_f32_16x16x32_bf16 v[96:99], v[168:171], v[184:187], v[96:99]
	v_mfma_f32_16x16x32_bf16 v[104:107], v[160:163], v[184:187], v[104:107]
	v_mfma_f32_16x16x32_bf16 v[88:91], v[160:163], v[192:195], v[88:91]
	v_mfma_f32_16x16x32_bf16 v[80:83], v[168:171], v[192:195], v[80:83]
	v_mfma_f32_16x16x32_bf16 v[48:51], v[168:171], v[200:203], v[48:51]
	v_mfma_f32_16x16x32_bf16 v[64:67], v[160:163], v[200:203], v[64:67]
	v_mfma_f32_16x16x32_bf16 v[124:127], v[164:167], v[180:183], v[124:127]
	v_mfma_f32_16x16x32_bf16 v[120:123], v[172:175], v[180:183], v[120:123]
	v_mfma_f32_16x16x32_bf16 v[96:99], v[172:175], v[188:191], v[96:99]
	v_mfma_f32_16x16x32_bf16 v[104:107], v[164:167], v[188:191], v[104:107]
	v_mfma_f32_16x16x32_bf16 v[88:91], v[164:167], v[196:199], v[88:91]
	v_mfma_f32_16x16x32_bf16 v[80:83], v[172:175], v[196:199], v[80:83]
	v_mfma_f32_16x16x32_bf16 v[48:51], v[172:175], v[204:207], v[48:51]
	v_mfma_f32_16x16x32_bf16 v[64:67], v[164:167], v[204:207], v[64:67]
	s_barrier
	ds_read_b128 v[176:179], v145 offset:49152
	ds_read_b128 v[180:183], v145 offset:50176
	ds_read_b128 v[184:187], v145 offset:51200
	ds_read_b128 v[188:191], v145 offset:52224
	ds_read_b128 v[192:195], v145 offset:53248
	ds_read_b128 v[196:199], v145 offset:54272
	ds_read_b128 v[200:203], v145 offset:55296
	ds_read_b128 v[204:207], v145 offset:56320
	s_add_i32 m0, s2, 0x18000
	s_nop 0
	global_load_lds_dwordx4 v140, s[38:39]
	s_nop 0
	s_add_i32 m0, s2, 0x1a000
	s_nop 0
	global_load_lds_dwordx4 v142, s[38:39]
	s_add_u32 s36, s36, 0x80080
	s_addc_u32 s37, s37, 0
	s_add_i32 m0, s2, 0x1c000
	s_nop 0
	global_load_lds_dwordx4 v140, s[36:37]
	s_nop 0
	s_add_i32 m0, s2, 0x1e000
	s_nop 0
	global_load_lds_dwordx4 v142, s[36:37]
	s_nop 0
	s_add_i32 m0, s2, 0x8000
	s_nop 0
	global_load_lds_dwordx4 v139, s[34:35]
	s_nop 0
	s_add_i32 m0, s2, 0xa000
	s_nop 0
	global_load_lds_dwordx4 v141, s[34:35]
	s_waitcnt vmcnt(8)
	s_waitcnt lgkmcnt(0)
	s_barrier
	v_mfma_f32_16x16x32_bf16 v[76:79], v[132:135], v[176:179], v[76:79]
	v_mfma_f32_16x16x32_bf16 v[60:63], v[152:155], v[176:179], v[60:63]
	v_mfma_f32_16x16x32_bf16 v[36:39], v[152:155], v[184:187], v[36:39]
	v_mfma_f32_16x16x32_bf16 v[44:47], v[132:135], v[184:187], v[44:47]
	v_mfma_f32_16x16x32_bf16 v[28:31], v[132:135], v[192:195], v[28:31]
	v_mfma_f32_16x16x32_bf16 v[20:23], v[152:155], v[192:195], v[20:23]
	v_mfma_f32_16x16x32_bf16 v[4:7], v[152:155], v[200:203], v[4:7]
	v_mfma_f32_16x16x32_bf16 v[12:15], v[132:135], v[200:203], v[12:15]
	v_mfma_f32_16x16x32_bf16 v[76:79], v[148:151], v[180:183], v[76:79]
	v_mfma_f32_16x16x32_bf16 v[60:63], v[156:159], v[180:183], v[60:63]
	v_mfma_f32_16x16x32_bf16 v[36:39], v[156:159], v[188:191], v[36:39]
	v_mfma_f32_16x16x32_bf16 v[44:47], v[148:151], v[188:191], v[44:47]
	v_mfma_f32_16x16x32_bf16 v[28:31], v[148:151], v[196:199], v[28:31]
	v_mfma_f32_16x16x32_bf16 v[20:23], v[156:159], v[196:199], v[20:23]
	v_mfma_f32_16x16x32_bf16 v[4:7], v[156:159], v[204:207], v[4:7]
	v_mfma_f32_16x16x32_bf16 v[12:15], v[148:151], v[204:207], v[12:15]
	v_mfma_f32_16x16x32_bf16 v[68:71], v[160:163], v[176:179], v[68:71]
	v_mfma_f32_16x16x32_bf16 v[52:55], v[168:171], v[176:179], v[52:55]
	v_mfma_f32_16x16x32_bf16 v[32:35], v[168:171], v[184:187], v[32:35]
	v_mfma_f32_16x16x32_bf16 v[40:43], v[160:163], v[184:187], v[40:43]
	v_mfma_f32_16x16x32_bf16 v[24:27], v[160:163], v[192:195], v[24:27]
	v_mfma_f32_16x16x32_bf16 v[16:19], v[168:171], v[192:195], v[16:19]
	v_mfma_f32_16x16x32_bf16 v[0:3], v[168:171], v[200:203], v[0:3]
	v_mfma_f32_16x16x32_bf16 v[8:11], v[160:163], v[200:203], v[8:11]
	v_mfma_f32_16x16x32_bf16 v[68:71], v[164:167], v[180:183], v[68:71]
	v_mfma_f32_16x16x32_bf16 v[52:55], v[172:175], v[180:183], v[52:55]
	v_mfma_f32_16x16x32_bf16 v[32:35], v[172:175], v[188:191], v[32:35]
	v_mfma_f32_16x16x32_bf16 v[40:43], v[164:167], v[188:191], v[40:43]
	v_mfma_f32_16x16x32_bf16 v[24:27], v[164:167], v[196:199], v[24:27]
	v_mfma_f32_16x16x32_bf16 v[16:19], v[172:175], v[196:199], v[16:19]
	v_mfma_f32_16x16x32_bf16 v[0:3], v[172:175], v[204:207], v[0:3]
	v_mfma_f32_16x16x32_bf16 v[8:11], v[164:167], v[204:207], v[8:11]
	s_barrier
	s_add_i32 s57, s57, 2
	s_add_u32 s53, s53, 0x100
	s_addc_u32 s54, s54, 0
	s_add_u32 s55, s55, 0x100
	s_addc_u32 s56, s56, 0
	s_add_u32 s30, s30, 0x100
	s_addc_u32 s31, s31, 0
	s_cmp_gt_u32 s57, 29
	s_cbranch_scc0 .LBB0_1109
	s_and_b64 vcc, exec, s[10:11]
	s_cbranch_vccz .LBB0_1112
	s_barrier

.LBB0_1410:
	ds_read_b128 v[0:3], v138
	ds_read_b128 v[4:7], v138 offset:1024
	ds_read_b128 v[8:11], v138 offset:2048
	ds_read_b128 v[12:15], v138 offset:3072
	ds_read_b128 v[16:19], v139
	ds_read_b128 v[20:23], v139 offset:1024
	ds_read_b128 v[24:27], v139 offset:2048
	ds_read_b128 v[28:31], v139 offset:3072
	ds_read_b128 v[32:35], v140
	ds_read_b128 v[36:39], v140 offset:1024
	ds_read_b128 v[40:43], v140 offset:2048
	ds_read_b128 v[44:47], v140 offset:3072
	ds_read_b128 v[48:51], v140 offset:4096
	ds_read_b128 v[52:55], v140 offset:5120
	ds_read_b128 v[56:59], v140 offset:6144
	ds_read_b128 v[60:63], v140 offset:7168
	s_lshl_b64 s[20:21], s[16:17], 19
	s_add_u32 s20, s39, s20
	s_addc_u32 s21, s40, s21
	s_and_b64 s[6:7], exec, s[6:7]
	s_cselect_b32 s2, s21, s29
	s_cselect_b32 s15, s20, s28
	s_add_u32 s6, s28, 0x100
	s_addc_u32 s7, s29, 0
	s_add_u32 s36, s26, 0x100
	s_addc_u32 s37, s27, 0
	s_add_u32 s30, s28, 0x180
	s_addc_u32 s31, s29, 0
	s_add_u32 s34, s26, 0x180
	s_addc_u32 s35, s27, 0
	s_add_u32 s54, s28, 0x40080
	s_addc_u32 s55, s29, 0
	s_add_i32 m0, s47, 0xc000
	s_nop 0
	global_load_lds_dwordx4 v134, s[54:55]
	s_nop 0
	s_add_i32 m0, s47, 0xe000
	s_nop 0
	global_load_lds_dwordx4 v136, s[54:55]
	s_waitcnt vmcnt(8)
	s_waitcnt lgkmcnt(0)
	s_barrier
	v_mfma_f32_16x16x128_f8f6f4 v[64:67], v[0:7], v[32:39], 0
	v_mfma_f32_16x16x128_f8f6f4 v[68:71], v[8:15], v[32:39], 0
	v_mfma_f32_16x16x128_f8f6f4 v[76:79], v[8:15], v[40:47], 0
	v_mfma_f32_16x16x128_f8f6f4 v[72:75], v[0:7], v[40:47], 0
	v_mfma_f32_16x16x128_f8f6f4 v[80:83], v[0:7], v[48:55], 0
	v_mfma_f32_16x16x128_f8f6f4 v[88:91], v[8:15], v[48:55], 0
	v_mfma_f32_16x16x128_f8f6f4 v[104:107], v[8:15], v[56:63], 0
	v_mfma_f32_16x16x128_f8f6f4 v[92:95], v[0:7], v[56:63], 0
	v_mfma_f32_16x16x128_f8f6f4 v[108:111], v[16:23], v[32:39], 0
	v_mfma_f32_16x16x128_f8f6f4 v[124:127], v[24:31], v[32:39], 0
	v_mfma_f32_16x16x128_f8f6f4 v[166:169], v[24:31], v[40:47], 0
	v_mfma_f32_16x16x128_f8f6f4 v[162:165], v[16:23], v[40:47], 0
	v_mfma_f32_16x16x128_f8f6f4 v[170:173], v[16:23], v[48:55], 0
	v_mfma_f32_16x16x128_f8f6f4 v[174:177], v[24:31], v[48:55], 0
	v_mfma_f32_16x16x128_f8f6f4 v[182:185], v[24:31], v[56:63], 0
	v_mfma_f32_16x16x128_f8f6f4 v[178:181], v[16:23], v[56:63], 0
	s_barrier
	ds_read_b128 v[32:35], v140 offset:16384
	ds_read_b128 v[36:39], v140 offset:17408
	ds_read_b128 v[40:43], v140 offset:18432
	ds_read_b128 v[44:47], v140 offset:19456
	ds_read_b128 v[48:51], v140 offset:20480
	ds_read_b128 v[52:55], v140 offset:21504
	ds_read_b128 v[56:59], v140 offset:22528
	ds_read_b128 v[60:63], v140 offset:23552
	s_add_i32 m0, s47, 0x10000
	s_nop 0
	global_load_lds_dwordx4 v135, s[36:37]
	s_nop 0
	s_add_i32 m0, s47, 0x12000
	s_nop 0
	global_load_lds_dwordx4 v137, s[36:37]
	s_add_u32 s36, s26, 0x40100
	s_addc_u32 s37, s27, 0
	s_add_i32 m0, s47, 0x14000
	s_nop 0
	global_load_lds_dwordx4 v135, s[36:37]
	s_nop 0
	s_add_i32 m0, s47, 0x16000
	s_nop 0
	global_load_lds_dwordx4 v137, s[36:37]
	s_nop 0
	s_add_i32 m0, s47, 0
	s_nop 0
	global_load_lds_dwordx4 v134, s[6:7]
	s_nop 0
	s_add_i32 m0, s47, 0x2000
	s_nop 0
	global_load_lds_dwordx4 v136, s[6:7]
	s_waitcnt vmcnt(8)
	s_waitcnt lgkmcnt(0)
	s_barrier
	v_mfma_f32_16x16x128_f8f6f4 v[186:189], v[0:7], v[32:39], 0
	v_mfma_f32_16x16x128_f8f6f4 v[190:193], v[8:15], v[32:39], 0
	v_mfma_f32_16x16x128_f8f6f4 v[198:201], v[8:15], v[40:47], 0
	v_mfma_f32_16x16x128_f8f6f4 v[194:197], v[0:7], v[40:47], 0
	v_mfma_f32_16x16x128_f8f6f4 v[202:205], v[0:7], v[48:55], 0
	v_mfma_f32_16x16x128_f8f6f4 v[206:209], v[8:15], v[48:55], 0
	v_mfma_f32_16x16x128_f8f6f4 v[214:217], v[8:15], v[56:63], 0
	v_mfma_f32_16x16x128_f8f6f4 v[210:213], v[0:7], v[56:63], 0
	v_mfma_f32_16x16x128_f8f6f4 v[218:221], v[16:23], v[32:39], 0
	v_mfma_f32_16x16x128_f8f6f4 v[222:225], v[24:31], v[32:39], 0
	v_mfma_f32_16x16x128_f8f6f4 v[230:233], v[24:31], v[40:47], 0
	v_mfma_f32_16x16x128_f8f6f4 v[226:229], v[16:23], v[40:47], 0
	v_mfma_f32_16x16x128_f8f6f4 v[234:237], v[16:23], v[48:55], 0
	v_mfma_f32_16x16x128_f8f6f4 v[238:241], v[24:31], v[48:55], 0
	v_mfma_f32_16x16x128_f8f6f4 v[246:249], v[24:31], v[56:63], 0
	v_mfma_f32_16x16x128_f8f6f4 v[242:245], v[16:23], v[56:63], 0
	s_barrier
	ds_read_b128 v[0:3], v141
	ds_read_b128 v[4:7], v141 offset:1024
	ds_read_b128 v[8:11], v141 offset:2048
	ds_read_b128 v[12:15], v141 offset:3072
	ds_read_b128 v[146:149], v142
	ds_read_b128 v[150:153], v142 offset:1024
	ds_read_b128 v[154:157], v142 offset:2048
	ds_read_b128 v[158:161], v142 offset:3072
	ds_read_b128 v[16:19], v140 offset:32768
	ds_read_b128 v[20:23], v140 offset:33792
	ds_read_b128 v[24:27], v140 offset:34816
	ds_read_b128 v[28:31], v140 offset:35840
	ds_read_b128 v[32:35], v140 offset:36864
	ds_read_b128 v[36:39], v140 offset:37888
	ds_read_b128 v[40:43], v140 offset:38912
	ds_read_b128 v[44:47], v140 offset:39936
	s_add_u32 s28, s28, 0x40100
	s_addc_u32 s29, s29, 0
	s_add_i32 m0, s47, 0x4000
	s_nop 0
	global_load_lds_dwordx4 v134, s[28:29]
	s_nop 0
	s_add_i32 m0, s47, 0x6000
	s_nop 0
	global_load_lds_dwordx4 v136, s[28:29]
	s_waitcnt vmcnt(8)
	s_waitcnt lgkmcnt(0)
	s_barrier
	v_mfma_f32_16x16x128_f8f6f4 v[112:115], v[0:7], v[16:23], v[64:67]
	v_mfma_f32_16x16x128_f8f6f4 v[116:119], v[8:15], v[16:23], v[68:71]
	v_mfma_f32_16x16x128_f8f6f4 v[100:103], v[0:7], v[24:31], v[72:75]
	v_mfma_f32_16x16x128_f8f6f4 v[96:99], v[8:15], v[24:31], v[76:79]
	v_mfma_f32_16x16x128_f8f6f4 v[84:87], v[0:7], v[32:39], v[80:83]
	v_mfma_f32_16x16x128_f8f6f4 v[80:83], v[8:15], v[32:39], v[88:91]
	v_mfma_f32_16x16x128_f8f6f4 v[60:63], v[0:7], v[40:47], v[92:95]
	v_mfma_f32_16x16x128_f8f6f4 v[56:59], v[8:15], v[40:47], v[104:107]
	v_mfma_f32_16x16x128_f8f6f4 v[120:123], v[146:153], v[16:23], v[108:111]
	v_mfma_f32_16x16x128_f8f6f4 v[124:127], v[154:161], v[16:23], v[124:127]
	v_mfma_f32_16x16x128_f8f6f4 v[108:111], v[146:153], v[24:31], v[162:165]
	v_mfma_f32_16x16x128_f8f6f4 v[104:107], v[154:161], v[24:31], v[166:169]
	v_mfma_f32_16x16x128_f8f6f4 v[92:95], v[146:153], v[32:39], v[170:173]
	v_mfma_f32_16x16x128_f8f6f4 v[88:91], v[154:161], v[32:39], v[174:177]
	v_mfma_f32_16x16x128_f8f6f4 v[76:79], v[146:153], v[40:47], v[178:181]
	v_mfma_f32_16x16x128_f8f6f4 v[72:75], v[154:161], v[40:47], v[182:185]
	s_barrier
	ds_read_b128 v[24:27], v140 offset:49152
	ds_read_b128 v[28:31], v140 offset:50176
	ds_read_b128 v[162:165], v140 offset:51200
	ds_read_b128 v[166:169], v140 offset:52224
	ds_read_b128 v[170:173], v140 offset:53248
	ds_read_b128 v[174:177], v140 offset:54272
	ds_read_b128 v[178:181], v140 offset:55296
	ds_read_b128 v[182:185], v140 offset:56320
	s_add_i32 m0, s47, 0x18000
	s_nop 0
	global_load_lds_dwordx4 v135, s[34:35]
	s_nop 0
	s_add_i32 m0, s47, 0x1a000
	s_nop 0
	global_load_lds_dwordx4 v137, s[34:35]
	s_add_u32 s28, s26, 0x40180
	s_addc_u32 s29, s27, 0
	s_add_i32 m0, s47, 0x1c000
	s_nop 0
	global_load_lds_dwordx4 v135, s[28:29]
	s_nop 0
	s_add_i32 m0, s47, 0x1e000
	s_nop 0
	global_load_lds_dwordx4 v137, s[28:29]
	s_nop 0
	s_add_i32 m0, s47, 0x8000
	s_nop 0
	global_load_lds_dwordx4 v134, s[30:31]
	s_nop 0
	s_add_i32 m0, s47, 0xa000
	s_nop 0
	global_load_lds_dwordx4 v136, s[30:31]
	s_waitcnt vmcnt(8)
	s_waitcnt lgkmcnt(0)
	s_barrier
	v_mfma_f32_16x16x128_f8f6f4 v[52:55], v[0:7], v[24:31], v[186:189]
	v_mfma_f32_16x16x128_f8f6f4 v[48:51], v[8:15], v[24:31], v[190:193]
	v_mfma_f32_16x16x128_f8f6f4 v[36:39], v[0:7], v[162:169], v[194:197]
	v_mfma_f32_16x16x128_f8f6f4 v[32:35], v[8:15], v[162:169], v[198:201]
	v_mfma_f32_16x16x128_f8f6f4 v[20:23], v[0:7], v[170:177], v[202:205]
	v_mfma_f32_16x16x128_f8f6f4 v[16:19], v[8:15], v[170:177], v[206:209]
	v_mfma_f32_16x16x128_f8f6f4 v[4:7], v[0:7], v[178:185], v[210:213]
	v_mfma_f32_16x16x128_f8f6f4 v[0:3], v[8:15], v[178:185], v[214:217]
	v_mfma_f32_16x16x128_f8f6f4 v[68:71], v[146:153], v[24:31], v[218:221]
	v_mfma_f32_16x16x128_f8f6f4 v[64:67], v[154:161], v[24:31], v[222:225]
	v_mfma_f32_16x16x128_f8f6f4 v[44:47], v[146:153], v[162:169], v[226:229]
	v_mfma_f32_16x16x128_f8f6f4 v[40:43], v[154:161], v[162:169], v[230:233]
	v_mfma_f32_16x16x128_f8f6f4 v[28:31], v[146:153], v[170:177], v[234:237]
	v_mfma_f32_16x16x128_f8f6f4 v[24:27], v[154:161], v[170:177], v[238:241]
	v_mfma_f32_16x16x128_f8f6f4 v[12:15], v[146:153], v[178:185], v[242:245]
	v_mfma_f32_16x16x128_f8f6f4 v[8:11], v[154:161], v[178:185], v[246:249]
	s_barrier
	s_add_u32 s17, s26, 0x200
	s_addc_u32 s54, s27, 0
	s_mov_b32 s55, 0
.LBB0_1411:
	ds_read_b128 v[146:149], v138
	ds_read_b128 v[150:153], v138 offset:1024
	ds_read_b128 v[154:157], v138 offset:2048
	ds_read_b128 v[158:161], v138 offset:3072
	ds_read_b128 v[162:165], v139
	ds_read_b128 v[166:169], v139 offset:1024
	ds_read_b128 v[170:173], v139 offset:2048
	ds_read_b128 v[174:177], v139 offset:3072
	ds_read_b128 v[178:181], v140
	ds_read_b128 v[182:185], v140 offset:1024
	ds_read_b128 v[186:189], v140 offset:2048
	ds_read_b128 v[190:193], v140 offset:3072
	ds_read_b128 v[194:197], v140 offset:4096
	ds_read_b128 v[198:201], v140 offset:5120
	ds_read_b128 v[202:205], v140 offset:6144
	ds_read_b128 v[206:209], v140 offset:7168
	s_add_u32 s26, s6, 0x100
	s_addc_u32 s27, s7, 0
	s_cmp_eq_u32 s55, 12
	s_cselect_b32 s36, s15, s26
	s_cselect_b32 s37, s2, s27
	s_cselect_b32 s30, s18, s17
	s_cselect_b32 s31, s19, s54
	s_add_u32 s28, s36, 0x80
	s_addc_u32 s29, s37, 0
	s_add_u32 s34, s30, 0x80
	s_addc_u32 s35, s31, 0
	s_add_u32 s6, s6, 0x40080
	s_addc_u32 s7, s7, 0
	s_add_i32 m0, s47, 0xc000
	s_nop 0
	global_load_lds_dwordx4 v134, s[6:7]
	s_nop 0
	s_add_i32 m0, s47, 0xe000
	s_nop 0
	global_load_lds_dwordx4 v136, s[6:7]
	s_waitcnt vmcnt(8)
	s_waitcnt lgkmcnt(0)
	s_barrier
	v_mfma_f32_16x16x128_f8f6f4 v[112:115], v[146:153], v[178:185], v[112:115]
	v_mfma_f32_16x16x128_f8f6f4 v[116:119], v[154:161], v[178:185], v[116:119]
	v_mfma_f32_16x16x128_f8f6f4 v[96:99], v[154:161], v[186:193], v[96:99]
	v_mfma_f32_16x16x128_f8f6f4 v[100:103], v[146:153], v[186:193], v[100:103]
	v_mfma_f32_16x16x128_f8f6f4 v[210:213], v[146:153], v[194:201], v[84:87]
	v_mfma_f32_16x16x128_f8f6f4 v[214:217], v[154:161], v[194:201], v[80:83]
	v_mfma_f32_16x16x128_f8f6f4 v[222:225], v[154:161], v[202:209], v[56:59]
	v_mfma_f32_16x16x128_f8f6f4 v[218:221], v[146:153], v[202:209], v[60:63]
	v_mfma_f32_16x16x128_f8f6f4 v[120:123], v[162:169], v[178:185], v[120:123]
	v_mfma_f32_16x16x128_f8f6f4 v[124:127], v[170:177], v[178:185], v[124:127]
	v_mfma_f32_16x16x128_f8f6f4 v[108:111], v[162:169], v[186:193], v[108:111]
	v_mfma_f32_16x16x128_f8f6f4 v[104:107], v[170:177], v[186:193], v[104:107]
	v_mfma_f32_16x16x128_f8f6f4 v[178:181], v[162:169], v[194:201], v[92:95]
	v_mfma_f32_16x16x128_f8f6f4 v[182:185], v[170:177], v[194:201], v[88:91]
	v_mfma_f32_16x16x128_f8f6f4 v[186:189], v[162:169], v[202:209], v[76:79]
	v_mfma_f32_16x16x128_f8f6f4 v[190:193], v[170:177], v[202:209], v[72:75]
	s_barrier
	ds_read_b128 v[56:59], v140 offset:16384
	ds_read_b128 v[60:63], v140 offset:17408
	s_nop 2
	ds_read_b128 v[72:75], v140 offset:18432
	ds_read_b128 v[76:79], v140 offset:19456
	ds_read_b128 v[80:83], v140 offset:20480
	ds_read_b128 v[84:87], v140 offset:21504
	ds_read_b128 v[88:91], v140 offset:22528
	ds_read_b128 v[92:95], v140 offset:23552
	s_add_i32 m0, s47, 0x10000
	s_nop 0
	global_load_lds_dwordx4 v135, s[30:31]
	s_nop 0
	s_add_i32 m0, s47, 0x12000
	s_nop 0
	global_load_lds_dwordx4 v137, s[30:31]
	s_add_u32 s6, s30, 0x40000
	s_addc_u32 s7, s31, 0
	s_add_i32 m0, s47, 0x14000
	s_nop 0
	global_load_lds_dwordx4 v135, s[6:7]
	s_nop 0
	s_add_i32 m0, s47, 0x16000
	s_nop 0
	global_load_lds_dwordx4 v137, s[6:7]
	s_nop 0
	s_add_i32 m0, s47, 0
	s_nop 0
	global_load_lds_dwordx4 v134, s[36:37]
	s_nop 0
	s_add_i32 m0, s47, 0x2000
	s_nop 0
	global_load_lds_dwordx4 v136, s[36:37]
	s_waitcnt vmcnt(8)
	s_waitcnt lgkmcnt(0)
	s_barrier
	v_mfma_f32_16x16x128_f8f6f4 v[52:55], v[146:153], v[56:63], v[52:55]
	v_mfma_f32_16x16x128_f8f6f4 v[48:51], v[154:161], v[56:63], v[48:51]
	v_mfma_f32_16x16x128_f8f6f4 v[198:201], v[154:161], v[72:79], v[32:35]
	v_mfma_f32_16x16x128_f8f6f4 v[194:197], v[146:153], v[72:79], v[36:39]
	v_mfma_f32_16x16x128_f8f6f4 v[202:205], v[146:153], v[80:87], v[20:23]
	v_mfma_f32_16x16x128_f8f6f4 v[206:209], v[154:161], v[80:87], v[16:19]
	v_mfma_f32_16x16x128_f8f6f4 v[230:233], v[154:161], v[88:95], v[0:3]
	v_mfma_f32_16x16x128_f8f6f4 v[226:229], v[146:153], v[88:95], v[4:7]
	v_mfma_f32_16x16x128_f8f6f4 v[68:71], v[162:169], v[56:63], v[68:71]
	v_mfma_f32_16x16x128_f8f6f4 v[64:67], v[170:177], v[56:63], v[64:67]
	v_mfma_f32_16x16x128_f8f6f4 v[238:241], v[170:177], v[72:79], v[40:43]
	v_mfma_f32_16x16x128_f8f6f4 v[234:237], v[162:169], v[72:79], v[44:47]
	v_mfma_f32_16x16x128_f8f6f4 v[242:245], v[162:169], v[80:87], v[28:31]
	v_mfma_f32_16x16x128_f8f6f4 v[246:249], v[170:177], v[80:87], v[24:27]
	v_mfma_f32_16x16x128_f8f6f4 v[130:133], v[170:177], v[88:95], v[8:11]
	v_mfma_f32_16x16x128_f8f6f4 v[250:253], v[162:169], v[88:95], v[12:15]
	s_barrier
	ds_read_b128 v[0:3], v141
	ds_read_b128 v[4:7], v141 offset:1024
	s_nop 2
	ds_read_b128 v[8:11], v141 offset:2048
	ds_read_b128 v[12:15], v141 offset:3072
	ds_read_b128 v[146:149], v142
	ds_read_b128 v[150:153], v142 offset:1024
	ds_read_b128 v[154:157], v142 offset:2048
	ds_read_b128 v[158:161], v142 offset:3072
	ds_read_b128 v[16:19], v140 offset:32768
	ds_read_b128 v[20:23], v140 offset:33792
	ds_read_b128 v[24:27], v140 offset:34816
	ds_read_b128 v[28:31], v140 offset:35840
	ds_read_b128 v[32:35], v140 offset:36864
	ds_read_b128 v[36:39], v140 offset:37888
	ds_read_b128 v[40:43], v140 offset:38912
	ds_read_b128 v[44:47], v140 offset:39936
	s_add_u32 s6, s36, 0x40000
	s_addc_u32 s7, s37, 0
	s_add_i32 m0, s47, 0x4000
	s_nop 0
	global_load_lds_dwordx4 v134, s[6:7]
	s_nop 0
	s_add_i32 m0, s47, 0x6000
	s_nop 0
	global_load_lds_dwordx4 v136, s[6:7]
	s_waitcnt vmcnt(8)
	s_waitcnt lgkmcnt(0)
	s_barrier
	v_mfma_f32_16x16x128_f8f6f4 v[112:115], v[0:7], v[16:23], v[112:115]
	v_mfma_f32_16x16x128_f8f6f4 v[116:119], v[8:15], v[16:23], v[116:119]
	v_mfma_f32_16x16x128_f8f6f4 v[96:99], v[8:15], v[24:31], v[96:99]
	v_mfma_f32_16x16x128_f8f6f4 v[100:103], v[0:7], v[24:31], v[100:103]
	v_mfma_f32_16x16x128_f8f6f4 v[84:87], v[0:7], v[32:39], v[210:213]
	v_mfma_f32_16x16x128_f8f6f4 v[80:83], v[8:15], v[32:39], v[214:217]
	v_mfma_f32_16x16x128_f8f6f4 v[56:59], v[8:15], v[40:47], v[222:225]
	v_mfma_f32_16x16x128_f8f6f4 v[60:63], v[0:7], v[40:47], v[218:221]
	v_mfma_f32_16x16x128_f8f6f4 v[120:123], v[146:153], v[16:23], v[120:123]
	v_mfma_f32_16x16x128_f8f6f4 v[124:127], v[154:161], v[16:23], v[124:127]
	v_mfma_f32_16x16x128_f8f6f4 v[104:107], v[154:161], v[24:31], v[104:107]
	v_mfma_f32_16x16x128_f8f6f4 v[108:111], v[146:153], v[24:31], v[108:111]
	v_mfma_f32_16x16x128_f8f6f4 v[92:95], v[146:153], v[32:39], v[178:181]
	v_mfma_f32_16x16x128_f8f6f4 v[88:91], v[154:161], v[32:39], v[182:185]
	v_mfma_f32_16x16x128_f8f6f4 v[72:75], v[154:161], v[40:47], v[190:193]
	v_mfma_f32_16x16x128_f8f6f4 v[76:79], v[146:153], v[40:47], v[186:189]
	s_barrier
	ds_read_b128 v[24:27], v140 offset:49152
	ds_read_b128 v[28:31], v140 offset:50176
	ds_read_b128 v[162:165], v140 offset:51200
	ds_read_b128 v[166:169], v140 offset:52224
	ds_read_b128 v[170:173], v140 offset:53248
	ds_read_b128 v[174:177], v140 offset:54272
	ds_read_b128 v[178:181], v140 offset:55296
	ds_read_b128 v[182:185], v140 offset:56320
	s_add_i32 m0, s47, 0x18000
	s_nop 0
	global_load_lds_dwordx4 v135, s[34:35]
	s_nop 0
	s_add_i32 m0, s47, 0x1a000
	s_nop 0
	global_load_lds_dwordx4 v137, s[34:35]
	s_add_u32 s6, s30, 0x40080
	s_addc_u32 s7, s31, 0
	s_add_i32 m0, s47, 0x1c000
	s_nop 0
	global_load_lds_dwordx4 v135, s[6:7]
	s_nop 0
	s_add_i32 m0, s47, 0x1e000
	s_nop 0
	global_load_lds_dwordx4 v137, s[6:7]
	s_nop 0
	s_add_i32 m0, s47, 0x8000
	s_nop 0
	global_load_lds_dwordx4 v134, s[28:29]
	s_nop 0
	s_add_i32 m0, s47, 0xa000
	s_nop 0
	global_load_lds_dwordx4 v136, s[28:29]
	s_waitcnt vmcnt(8)
	s_waitcnt lgkmcnt(0)
	s_barrier
	v_mfma_f32_16x16x128_f8f6f4 v[52:55], v[0:7], v[24:31], v[52:55]
	v_mfma_f32_16x16x128_f8f6f4 v[48:51], v[8:15], v[24:31], v[48:51]
	v_mfma_f32_16x16x128_f8f6f4 v[36:39], v[0:7], v[162:169], v[194:197]
	v_mfma_f32_16x16x128_f8f6f4 v[32:35], v[8:15], v[162:169], v[198:201]
	v_mfma_f32_16x16x128_f8f6f4 v[20:23], v[0:7], v[170:177], v[202:205]
	v_mfma_f32_16x16x128_f8f6f4 v[16:19], v[8:15], v[170:177], v[206:209]
	v_mfma_f32_16x16x128_f8f6f4 v[4:7], v[0:7], v[178:185], v[226:229]
	v_mfma_f32_16x16x128_f8f6f4 v[0:3], v[8:15], v[178:185], v[230:233]
	v_mfma_f32_16x16x128_f8f6f4 v[68:71], v[146:153], v[24:31], v[68:71]
	v_mfma_f32_16x16x128_f8f6f4 v[64:67], v[154:161], v[24:31], v[64:67]
	v_mfma_f32_16x16x128_f8f6f4 v[44:47], v[146:153], v[162:169], v[234:237]
	v_mfma_f32_16x16x128_f8f6f4 v[40:43], v[154:161], v[162:169], v[238:241]
	v_mfma_f32_16x16x128_f8f6f4 v[28:31], v[146:153], v[170:177], v[242:245]
	v_mfma_f32_16x16x128_f8f6f4 v[24:27], v[154:161], v[170:177], v[246:249]
	v_mfma_f32_16x16x128_f8f6f4 v[12:15], v[146:153], v[178:185], v[250:253]
	v_mfma_f32_16x16x128_f8f6f4 v[8:11], v[154:161], v[178:185], v[130:133]
	s_barrier
	s_add_i32 s55, s55, 2
	s_add_u32 s17, s17, 0x100
	s_addc_u32 s54, s54, 0
	s_cmp_gt_u32 s55, 13
	s_mov_b64 s[6:7], s[26:27]
	s_cbranch_scc0 .LBB0_1411
	s_and_b64 vcc, exec, s[12:13]
	s_cbranch_vccz .LBB0_1414
	s_barrier

.LBB0_1487:
	ds_read_b128 v[0:3], v153
	ds_read_b128 v[4:7], v153 offset:1024
	ds_read_b128 v[8:11], v153 offset:2048
	ds_read_b128 v[12:15], v153 offset:3072
	ds_read_b128 v[16:19], v154
	ds_read_b128 v[20:23], v154 offset:1024
	ds_read_b128 v[24:27], v154 offset:2048
	ds_read_b128 v[28:31], v154 offset:3072
	ds_read_b128 v[32:35], v155
	ds_read_b128 v[36:39], v155 offset:1024
	ds_read_b128 v[40:43], v155 offset:2048
	ds_read_b128 v[44:47], v155 offset:3072
	ds_read_b128 v[48:51], v155 offset:4096
	ds_read_b128 v[52:55], v155 offset:5120
	ds_read_b128 v[56:59], v155 offset:6144
	ds_read_b128 v[60:63], v155 offset:7168
	s_add_u32 s26, s28, 0x100
	s_addc_u32 s27, s29, 0
	s_add_u32 s36, s24, 0x100
	s_addc_u32 s37, s25, 0
	s_add_u32 s30, s28, 0x180
	s_addc_u32 s31, s29, 0
	s_add_u32 s34, s24, 0x180
	s_addc_u32 s35, s25, 0
	s_add_u32 s52, s28, 0xe0080
	s_addc_u32 s53, s29, 0
	s_add_i32 m0, s44, 0xc000
	s_nop 0
	global_load_lds_dwordx4 v149, s[52:53]
	s_nop 0
	s_add_i32 m0, s44, 0xe000
	s_nop 0
	global_load_lds_dwordx4 v151, s[52:53]
	s_waitcnt vmcnt(8)
	s_waitcnt lgkmcnt(0)
	s_barrier
	v_mfma_f32_16x16x128_f8f6f4 v[64:67], v[0:7], v[32:39], 0
	v_mfma_f32_16x16x128_f8f6f4 v[68:71], v[8:15], v[32:39], 0
	v_mfma_f32_16x16x128_f8f6f4 v[76:79], v[8:15], v[40:47], 0
	v_mfma_f32_16x16x128_f8f6f4 v[72:75], v[0:7], v[40:47], 0
	v_mfma_f32_16x16x128_f8f6f4 v[80:83], v[0:7], v[48:55], 0
	v_mfma_f32_16x16x128_f8f6f4 v[88:91], v[8:15], v[48:55], 0
	v_mfma_f32_16x16x128_f8f6f4 v[104:107], v[8:15], v[56:63], 0
	v_mfma_f32_16x16x128_f8f6f4 v[92:95], v[0:7], v[56:63], 0
	v_mfma_f32_16x16x128_f8f6f4 v[108:111], v[16:23], v[32:39], 0
	v_mfma_f32_16x16x128_f8f6f4 v[124:127], v[24:31], v[32:39], 0
	v_mfma_f32_16x16x128_f8f6f4 v[162:165], v[24:31], v[40:47], 0
	v_mfma_f32_16x16x128_f8f6f4 v[158:161], v[16:23], v[40:47], 0
	v_mfma_f32_16x16x128_f8f6f4 v[166:169], v[16:23], v[48:55], 0
	v_mfma_f32_16x16x128_f8f6f4 v[170:173], v[24:31], v[48:55], 0
	v_mfma_f32_16x16x128_f8f6f4 v[178:181], v[24:31], v[56:63], 0
	v_mfma_f32_16x16x128_f8f6f4 v[174:177], v[16:23], v[56:63], 0
	s_barrier
	ds_read_b128 v[32:35], v155 offset:16384
	ds_read_b128 v[36:39], v155 offset:17408
	ds_read_b128 v[40:43], v155 offset:18432
	ds_read_b128 v[44:47], v155 offset:19456
	ds_read_b128 v[48:51], v155 offset:20480
	ds_read_b128 v[52:55], v155 offset:21504
	ds_read_b128 v[56:59], v155 offset:22528
	ds_read_b128 v[60:63], v155 offset:23552
	s_add_i32 m0, s44, 0x10000
	s_nop 0
	global_load_lds_dwordx4 v150, s[36:37]
	s_nop 0
	s_add_i32 m0, s44, 0x12000
	s_nop 0
	global_load_lds_dwordx4 v152, s[36:37]
	s_add_u32 s36, s24, 0xe0100
	s_addc_u32 s37, s25, 0
	s_add_i32 m0, s44, 0x14000
	s_nop 0
	global_load_lds_dwordx4 v150, s[36:37]
	s_nop 0
	s_add_i32 m0, s44, 0x16000
	s_nop 0
	global_load_lds_dwordx4 v152, s[36:37]
	s_nop 0
	s_add_i32 m0, s44, 0
	s_nop 0
	global_load_lds_dwordx4 v149, s[26:27]
	s_nop 0
	s_add_i32 m0, s44, 0x2000
	s_nop 0
	global_load_lds_dwordx4 v151, s[26:27]
	s_waitcnt vmcnt(8)
	s_waitcnt lgkmcnt(0)
	s_barrier
	v_mfma_f32_16x16x128_f8f6f4 v[190:193], v[0:7], v[32:39], 0
	v_mfma_f32_16x16x128_f8f6f4 v[194:197], v[8:15], v[32:39], 0
	v_mfma_f32_16x16x128_f8f6f4 v[202:205], v[8:15], v[40:47], 0
	v_mfma_f32_16x16x128_f8f6f4 v[198:201], v[0:7], v[40:47], 0
	v_mfma_f32_16x16x128_f8f6f4 v[206:209], v[0:7], v[48:55], 0
	v_mfma_f32_16x16x128_f8f6f4 v[210:213], v[8:15], v[48:55], 0
	v_mfma_f32_16x16x128_f8f6f4 v[218:221], v[8:15], v[56:63], 0
	v_mfma_f32_16x16x128_f8f6f4 v[214:217], v[0:7], v[56:63], 0
	v_mfma_f32_16x16x128_f8f6f4 v[222:225], v[16:23], v[32:39], 0
	v_mfma_f32_16x16x128_f8f6f4 v[226:229], v[24:31], v[32:39], 0
	v_mfma_f32_16x16x128_f8f6f4 v[234:237], v[24:31], v[40:47], 0
	v_mfma_f32_16x16x128_f8f6f4 v[230:233], v[16:23], v[40:47], 0
	v_mfma_f32_16x16x128_f8f6f4 v[238:241], v[16:23], v[48:55], 0
	v_mfma_f32_16x16x128_f8f6f4 v[242:245], v[24:31], v[48:55], 0
	v_mfma_f32_16x16x128_f8f6f4 v[250:253], v[24:31], v[56:63], 0
	v_mfma_f32_16x16x128_f8f6f4 v[246:249], v[16:23], v[56:63], 0
	s_barrier
	ds_read_b128 v[0:3], v156
	ds_read_b128 v[4:7], v156 offset:1024
	ds_read_b128 v[16:19], v156 offset:2048
	ds_read_b128 v[20:23], v156 offset:3072
	ds_read_b128 v[132:135], v157
	ds_read_b128 v[136:139], v157 offset:1024
	ds_read_b128 v[140:143], v157 offset:2048
	ds_read_b128 v[144:147], v157 offset:3072
	ds_read_b128 v[8:11], v155 offset:32768
	ds_read_b128 v[12:15], v155 offset:33792
	ds_read_b128 v[24:27], v155 offset:34816
	ds_read_b128 v[28:31], v155 offset:35840
	ds_read_b128 v[32:35], v155 offset:36864
	ds_read_b128 v[36:39], v155 offset:37888
	ds_read_b128 v[40:43], v155 offset:38912
	ds_read_b128 v[44:47], v155 offset:39936
	s_add_u32 s28, s28, 0xe0100
	s_addc_u32 s29, s29, 0
	s_add_i32 m0, s44, 0x4000
	s_nop 0
	global_load_lds_dwordx4 v149, s[28:29]
	s_nop 0
	s_add_i32 m0, s44, 0x6000
	s_nop 0
	global_load_lds_dwordx4 v151, s[28:29]
	s_waitcnt vmcnt(8)
	s_waitcnt lgkmcnt(0)
	s_barrier
	v_mfma_f32_16x16x128_f8f6f4 v[112:115], v[0:7], v[8:15], v[64:67]
	v_mfma_f32_16x16x128_f8f6f4 v[116:119], v[16:23], v[8:15], v[68:71]
	v_mfma_f32_16x16x128_f8f6f4 v[100:103], v[0:7], v[24:31], v[72:75]
	v_mfma_f32_16x16x128_f8f6f4 v[96:99], v[16:23], v[24:31], v[76:79]
	v_mfma_f32_16x16x128_f8f6f4 v[84:87], v[0:7], v[32:39], v[80:83]
	v_mfma_f32_16x16x128_f8f6f4 v[80:83], v[16:23], v[32:39], v[88:91]
	v_mfma_f32_16x16x128_f8f6f4 v[60:63], v[0:7], v[40:47], v[92:95]
	v_mfma_f32_16x16x128_f8f6f4 v[52:55], v[16:23], v[40:47], v[104:107]
	v_mfma_f32_16x16x128_f8f6f4 v[120:123], v[132:139], v[8:15], v[108:111]
	v_mfma_f32_16x16x128_f8f6f4 v[124:127], v[140:147], v[8:15], v[124:127]
	v_mfma_f32_16x16x128_f8f6f4 v[108:111], v[132:139], v[24:31], v[158:161]
	v_mfma_f32_16x16x128_f8f6f4 v[104:107], v[140:147], v[24:31], v[162:165]
	v_mfma_f32_16x16x128_f8f6f4 v[92:95], v[132:139], v[32:39], v[166:169]
	v_mfma_f32_16x16x128_f8f6f4 v[88:91], v[140:147], v[32:39], v[170:173]
	v_mfma_f32_16x16x128_f8f6f4 v[56:59], v[132:139], v[40:47], v[174:177]
	v_mfma_f32_16x16x128_f8f6f4 v[48:51], v[140:147], v[40:47], v[178:181]
	s_barrier
	ds_read_b128 v[158:161], v155 offset:49152
	ds_read_b128 v[162:165], v155 offset:50176
	ds_read_b128 v[166:169], v155 offset:51200
	ds_read_b128 v[170:173], v155 offset:52224
	ds_read_b128 v[174:177], v155 offset:53248
	ds_read_b128 v[178:181], v155 offset:54272
	ds_read_b128 v[182:185], v155 offset:55296
	ds_read_b128 v[186:189], v155 offset:56320
	s_add_i32 m0, s44, 0x18000
	s_nop 0
	global_load_lds_dwordx4 v150, s[34:35]
	s_nop 0
	s_add_i32 m0, s44, 0x1a000
	s_nop 0
	global_load_lds_dwordx4 v152, s[34:35]
	s_add_u32 s28, s24, 0xe0180
	s_addc_u32 s29, s25, 0
	s_add_i32 m0, s44, 0x1c000
	s_nop 0
	global_load_lds_dwordx4 v150, s[28:29]
	s_nop 0
	s_add_i32 m0, s44, 0x1e000
	s_nop 0
	global_load_lds_dwordx4 v152, s[28:29]
	s_nop 0
	s_add_i32 m0, s44, 0x8000
	s_nop 0
	global_load_lds_dwordx4 v149, s[30:31]
	s_nop 0
	s_add_i32 m0, s44, 0xa000
	s_nop 0
	global_load_lds_dwordx4 v151, s[30:31]
	s_waitcnt vmcnt(8)
	s_waitcnt lgkmcnt(0)
	s_barrier
	v_mfma_f32_16x16x128_f8f6f4 v[68:71], v[0:7], v[158:165], v[190:193]
	v_mfma_f32_16x16x128_f8f6f4 v[64:67], v[16:23], v[158:165], v[194:197]
	v_mfma_f32_16x16x128_f8f6f4 v[36:39], v[16:23], v[166:173], v[202:205]
	v_mfma_f32_16x16x128_f8f6f4 v[44:47], v[0:7], v[166:173], v[198:201]
	v_mfma_f32_16x16x128_f8f6f4 v[28:31], v[0:7], v[174:181], v[206:209]
	v_mfma_f32_16x16x128_f8f6f4 v[24:27], v[16:23], v[174:181], v[210:213]
	v_mfma_f32_16x16x128_f8f6f4 v[8:11], v[16:23], v[182:189], v[218:221]
	v_mfma_f32_16x16x128_f8f6f4 v[12:15], v[0:7], v[182:189], v[214:217]
	v_mfma_f32_16x16x128_f8f6f4 v[76:79], v[132:139], v[158:165], v[222:225]
	v_mfma_f32_16x16x128_f8f6f4 v[72:75], v[140:147], v[158:165], v[226:229]
	v_mfma_f32_16x16x128_f8f6f4 v[32:35], v[140:147], v[166:173], v[234:237]
	v_mfma_f32_16x16x128_f8f6f4 v[40:43], v[132:139], v[166:173], v[230:233]
	v_mfma_f32_16x16x128_f8f6f4 v[20:23], v[132:139], v[174:181], v[238:241]
	v_mfma_f32_16x16x128_f8f6f4 v[16:19], v[140:147], v[174:181], v[242:245]
	v_mfma_f32_16x16x128_f8f6f4 v[0:3], v[140:147], v[182:189], v[250:253]
	v_mfma_f32_16x16x128_f8f6f4 v[4:7], v[132:139], v[182:189], v[246:249]
	s_barrier
	s_add_u32 s23, s24, 0x200
	s_addc_u32 s51, s25, 0
	s_mov_b32 s52, 0
.LBB0_1488:
	ds_read_b128 v[132:135], v153
	ds_read_b128 v[136:139], v153 offset:1024
	ds_read_b128 v[140:143], v153 offset:2048
	ds_read_b128 v[144:147], v153 offset:3072
	ds_read_b128 v[158:161], v154
	ds_read_b128 v[162:165], v154 offset:1024
	ds_read_b128 v[166:169], v154 offset:2048
	ds_read_b128 v[170:173], v154 offset:3072
	ds_read_b128 v[174:177], v155
	ds_read_b128 v[178:181], v155 offset:1024
	ds_read_b128 v[182:185], v155 offset:2048
	ds_read_b128 v[186:189], v155 offset:3072
	ds_read_b128 v[190:193], v155 offset:4096
	ds_read_b128 v[194:197], v155 offset:5120
	ds_read_b128 v[198:201], v155 offset:6144
	ds_read_b128 v[202:205], v155 offset:7168
	s_add_u32 s24, s26, 0x100
	s_addc_u32 s25, s27, 0
	s_cmp_eq_u32 s52, 52
	s_cselect_b32 s36, s6, s24
	s_cselect_b32 s37, s7, s25
	s_cselect_b32 s30, s20, s23
	s_cselect_b32 s31, s21, s51
	s_add_u32 s28, s36, 0x80
	s_addc_u32 s29, s37, 0
	s_add_u32 s34, s30, 0x80
	s_addc_u32 s35, s31, 0
	s_add_u32 s26, s26, 0xe0080
	s_addc_u32 s27, s27, 0
	s_add_i32 m0, s44, 0xc000
	s_nop 0
	global_load_lds_dwordx4 v149, s[26:27]
	s_nop 0
	s_add_i32 m0, s44, 0xe000
	s_nop 0
	global_load_lds_dwordx4 v151, s[26:27]
	s_waitcnt vmcnt(8)
	s_waitcnt lgkmcnt(0)
	s_barrier
	v_mfma_f32_16x16x128_f8f6f4 v[112:115], v[132:139], v[174:181], v[112:115]
	v_mfma_f32_16x16x128_f8f6f4 v[116:119], v[140:147], v[174:181], v[116:119]
	v_mfma_f32_16x16x128_f8f6f4 v[96:99], v[140:147], v[182:189], v[96:99]
	v_mfma_f32_16x16x128_f8f6f4 v[100:103], v[132:139], v[182:189], v[100:103]
	v_mfma_f32_16x16x128_f8f6f4 v[206:209], v[132:139], v[190:197], v[84:87]
	v_mfma_f32_16x16x128_f8f6f4 v[210:213], v[140:147], v[190:197], v[80:83]
	v_mfma_f32_16x16x128_f8f6f4 v[218:221], v[140:147], v[198:205], v[52:55]
	v_mfma_f32_16x16x128_f8f6f4 v[214:217], v[132:139], v[198:205], v[60:63]
	v_mfma_f32_16x16x128_f8f6f4 v[120:123], v[158:165], v[174:181], v[120:123]
	v_mfma_f32_16x16x128_f8f6f4 v[124:127], v[166:173], v[174:181], v[124:127]
	v_mfma_f32_16x16x128_f8f6f4 v[108:111], v[158:165], v[182:189], v[108:111]
	v_mfma_f32_16x16x128_f8f6f4 v[104:107], v[166:173], v[182:189], v[104:107]
	v_mfma_f32_16x16x128_f8f6f4 v[174:177], v[158:165], v[190:197], v[92:95]
	v_mfma_f32_16x16x128_f8f6f4 v[178:181], v[166:173], v[190:197], v[88:91]
	v_mfma_f32_16x16x128_f8f6f4 v[182:185], v[158:165], v[198:205], v[56:59]
	v_mfma_f32_16x16x128_f8f6f4 v[186:189], v[166:173], v[198:205], v[48:51]
	s_barrier
	s_nop 4
	ds_read_b128 v[48:51], v155 offset:16384
	ds_read_b128 v[52:55], v155 offset:17408
	ds_read_b128 v[56:59], v155 offset:18432
	ds_read_b128 v[60:63], v155 offset:19456
	ds_read_b128 v[80:83], v155 offset:20480
	ds_read_b128 v[84:87], v155 offset:21504
	ds_read_b128 v[88:91], v155 offset:22528
	ds_read_b128 v[92:95], v155 offset:23552
	s_add_i32 m0, s44, 0x10000
	s_nop 0
	global_load_lds_dwordx4 v150, s[30:31]
	s_nop 0
	s_add_i32 m0, s44, 0x12000
	s_nop 0
	global_load_lds_dwordx4 v152, s[30:31]
	s_add_u32 s26, s30, 0xe0000
	s_addc_u32 s27, s31, 0
	s_add_i32 m0, s44, 0x14000
	s_nop 0
	global_load_lds_dwordx4 v150, s[26:27]
	s_nop 0
	s_add_i32 m0, s44, 0x16000
	s_nop 0
	global_load_lds_dwordx4 v152, s[26:27]
	s_nop 0
	s_add_i32 m0, s44, 0
	s_nop 0
	global_load_lds_dwordx4 v149, s[36:37]
	s_nop 0
	s_add_i32 m0, s44, 0x2000
	s_nop 0
	global_load_lds_dwordx4 v151, s[36:37]
	s_waitcnt vmcnt(8)
	s_waitcnt lgkmcnt(0)
	s_barrier
	v_mfma_f32_16x16x128_f8f6f4 v[68:71], v[132:139], v[48:55], v[68:71]
	v_mfma_f32_16x16x128_f8f6f4 v[64:67], v[140:147], v[48:55], v[64:67]
	v_mfma_f32_16x16x128_f8f6f4 v[194:197], v[140:147], v[56:63], v[36:39]
	v_mfma_f32_16x16x128_f8f6f4 v[190:193], v[132:139], v[56:63], v[44:47]
	v_mfma_f32_16x16x128_f8f6f4 v[198:201], v[132:139], v[80:87], v[28:31]
	v_mfma_f32_16x16x128_f8f6f4 v[202:205], v[140:147], v[80:87], v[24:27]
	v_mfma_f32_16x16x128_f8f6f4 v[226:229], v[140:147], v[88:95], v[8:11]
	v_mfma_f32_16x16x128_f8f6f4 v[222:225], v[132:139], v[88:95], v[12:15]
	v_mfma_f32_16x16x128_f8f6f4 v[76:79], v[158:165], v[48:55], v[76:79]
	v_mfma_f32_16x16x128_f8f6f4 v[72:75], v[166:173], v[48:55], v[72:75]
	v_mfma_f32_16x16x128_f8f6f4 v[234:237], v[166:173], v[56:63], v[32:35]
	v_mfma_f32_16x16x128_f8f6f4 v[230:233], v[158:165], v[56:63], v[40:43]
	v_mfma_f32_16x16x128_f8f6f4 v[238:241], v[158:165], v[80:87], v[20:23]
	v_mfma_f32_16x16x128_f8f6f4 v[242:245], v[166:173], v[80:87], v[16:19]
	v_mfma_f32_16x16x128_f8f6f4 v[250:253], v[166:173], v[88:95], v[0:3]
	v_mfma_f32_16x16x128_f8f6f4 v[246:249], v[158:165], v[88:95], v[4:7]
	s_barrier
	s_nop 4
	ds_read_b128 v[0:3], v156
	ds_read_b128 v[4:7], v156 offset:1024
	ds_read_b128 v[16:19], v156 offset:2048
	ds_read_b128 v[20:23], v156 offset:3072
	ds_read_b128 v[132:135], v157
	ds_read_b128 v[136:139], v157 offset:1024
	ds_read_b128 v[140:143], v157 offset:2048
	ds_read_b128 v[144:147], v157 offset:3072
	ds_read_b128 v[8:11], v155 offset:32768
	ds_read_b128 v[12:15], v155 offset:33792
	ds_read_b128 v[24:27], v155 offset:34816
	ds_read_b128 v[28:31], v155 offset:35840
	ds_read_b128 v[32:35], v155 offset:36864
	ds_read_b128 v[36:39], v155 offset:37888
	ds_read_b128 v[40:43], v155 offset:38912
	ds_read_b128 v[44:47], v155 offset:39936
	s_add_u32 s26, s36, 0xe0000
	s_addc_u32 s27, s37, 0
	s_add_i32 m0, s44, 0x4000
	s_nop 0
	global_load_lds_dwordx4 v149, s[26:27]
	s_nop 0
	s_add_i32 m0, s44, 0x6000
	s_nop 0
	global_load_lds_dwordx4 v151, s[26:27]
	s_waitcnt vmcnt(8)
	s_waitcnt lgkmcnt(0)
	s_barrier
	v_mfma_f32_16x16x128_f8f6f4 v[112:115], v[0:7], v[8:15], v[112:115]
	v_mfma_f32_16x16x128_f8f6f4 v[116:119], v[16:23], v[8:15], v[116:119]
	v_mfma_f32_16x16x128_f8f6f4 v[96:99], v[16:23], v[24:31], v[96:99]
	v_mfma_f32_16x16x128_f8f6f4 v[100:103], v[0:7], v[24:31], v[100:103]
	v_mfma_f32_16x16x128_f8f6f4 v[84:87], v[0:7], v[32:39], v[206:209]
	v_mfma_f32_16x16x128_f8f6f4 v[80:83], v[16:23], v[32:39], v[210:213]
	v_mfma_f32_16x16x128_f8f6f4 v[52:55], v[16:23], v[40:47], v[218:221]
	v_mfma_f32_16x16x128_f8f6f4 v[60:63], v[0:7], v[40:47], v[214:217]
	v_mfma_f32_16x16x128_f8f6f4 v[120:123], v[132:139], v[8:15], v[120:123]
	v_mfma_f32_16x16x128_f8f6f4 v[124:127], v[140:147], v[8:15], v[124:127]
	v_mfma_f32_16x16x128_f8f6f4 v[104:107], v[140:147], v[24:31], v[104:107]
	v_mfma_f32_16x16x128_f8f6f4 v[108:111], v[132:139], v[24:31], v[108:111]
	v_mfma_f32_16x16x128_f8f6f4 v[92:95], v[132:139], v[32:39], v[174:177]
	v_mfma_f32_16x16x128_f8f6f4 v[88:91], v[140:147], v[32:39], v[178:181]
	v_mfma_f32_16x16x128_f8f6f4 v[48:51], v[140:147], v[40:47], v[186:189]
	v_mfma_f32_16x16x128_f8f6f4 v[56:59], v[132:139], v[40:47], v[182:185]
	s_barrier
	ds_read_b128 v[158:161], v155 offset:49152
	ds_read_b128 v[162:165], v155 offset:50176
	ds_read_b128 v[166:169], v155 offset:51200
	ds_read_b128 v[170:173], v155 offset:52224
	ds_read_b128 v[174:177], v155 offset:53248
	ds_read_b128 v[178:181], v155 offset:54272
	ds_read_b128 v[182:185], v155 offset:55296
	ds_read_b128 v[186:189], v155 offset:56320
	s_add_i32 m0, s44, 0x18000
	s_nop 0
	global_load_lds_dwordx4 v150, s[34:35]
	s_nop 0
	s_add_i32 m0, s44, 0x1a000
	s_nop 0
	global_load_lds_dwordx4 v152, s[34:35]
	s_add_u32 s26, s30, 0xe0080
	s_addc_u32 s27, s31, 0
	s_add_i32 m0, s44, 0x1c000
	s_nop 0
	global_load_lds_dwordx4 v150, s[26:27]
	s_nop 0
	s_add_i32 m0, s44, 0x1e000
	s_nop 0
	global_load_lds_dwordx4 v152, s[26:27]
	s_nop 0
	s_add_i32 m0, s44, 0x8000
	s_nop 0
	global_load_lds_dwordx4 v149, s[28:29]
	s_nop 0
	s_add_i32 m0, s44, 0xa000
	s_nop 0
	global_load_lds_dwordx4 v151, s[28:29]
	s_waitcnt vmcnt(8)
	s_waitcnt lgkmcnt(0)
	s_barrier
	v_mfma_f32_16x16x128_f8f6f4 v[68:71], v[0:7], v[158:165], v[68:71]
	v_mfma_f32_16x16x128_f8f6f4 v[64:67], v[16:23], v[158:165], v[64:67]
	v_mfma_f32_16x16x128_f8f6f4 v[36:39], v[16:23], v[166:173], v[194:197]
	v_mfma_f32_16x16x128_f8f6f4 v[44:47], v[0:7], v[166:173], v[190:193]
	v_mfma_f32_16x16x128_f8f6f4 v[28:31], v[0:7], v[174:181], v[198:201]
	v_mfma_f32_16x16x128_f8f6f4 v[24:27], v[16:23], v[174:181], v[202:205]
	v_mfma_f32_16x16x128_f8f6f4 v[8:11], v[16:23], v[182:189], v[226:229]
	v_mfma_f32_16x16x128_f8f6f4 v[12:15], v[0:7], v[182:189], v[222:225]
	v_mfma_f32_16x16x128_f8f6f4 v[76:79], v[132:139], v[158:165], v[76:79]
	v_mfma_f32_16x16x128_f8f6f4 v[72:75], v[140:147], v[158:165], v[72:75]
	v_mfma_f32_16x16x128_f8f6f4 v[32:35], v[140:147], v[166:173], v[234:237]
	v_mfma_f32_16x16x128_f8f6f4 v[40:43], v[132:139], v[166:173], v[230:233]
	v_mfma_f32_16x16x128_f8f6f4 v[20:23], v[132:139], v[174:181], v[238:241]
	v_mfma_f32_16x16x128_f8f6f4 v[16:19], v[140:147], v[174:181], v[242:245]
	v_mfma_f32_16x16x128_f8f6f4 v[0:3], v[140:147], v[182:189], v[250:253]
	v_mfma_f32_16x16x128_f8f6f4 v[4:7], v[132:139], v[182:189], v[246:249]
	s_barrier
	s_add_i32 s52, s52, 2
	s_add_u32 s23, s23, 0x100
	s_addc_u32 s51, s51, 0
	s_cmp_gt_u32 s52, 53
	s_mov_b64 s[26:27], s[24:25]
	s_cbranch_scc0 .LBB0_1488
	s_and_b64 vcc, exec, s[16:17]
	s_cbranch_vccz .LBB0_1491
	s_barrier
